# GEMM K-loops: redundant back-to-back s_setprio 0/1 pairs between the two MMA groups removed (48 pairs)
# baseline (speedup 1.0000x reference)
.LBB0_1025:
	ds_read_b128 v[140:143], v134
	ds_read_b128 v[144:147], v134 offset:1024
	ds_read_b128 v[148:151], v134 offset:2048
	ds_read_b128 v[152:155], v134 offset:3072
	ds_read_b128 v[156:159], v135
	ds_read_b128 v[160:163], v135 offset:1024
	ds_read_b128 v[164:167], v135 offset:2048
	ds_read_b128 v[168:171], v135 offset:3072
	s_add_i32 s13, s12, 0xfffc0080
	s_cmp_eq_u32 s1, 12
	s_cselect_b32 s45, s29, s41
	s_cselect_b32 s44, s28, s40
	s_cselect_b32 s47, s31, s43
	s_cselect_b32 s46, s30, s42
	s_cselect_b32 s13, 0, s13
	s_cselect_b32 s49, s35, s53
	s_cselect_b32 s48, s34, s52
	s_cselect_b32 s51, s63, s5
	s_cselect_b32 s50, s62, s4
	s_mov_b32 m0, s91
	ds_read_b128 v[198:201], v136
	ds_read_b128 v[202:205], v136 offset:1024
	ds_read_b128 v[206:209], v136 offset:2048
	ds_read_b128 v[210:213], v136 offset:3072
	ds_read_b128 v[214:217], v136 offset:4096
	ds_read_b128 v[218:221], v136 offset:5120
	ds_read_b128 v[222:225], v136 offset:6144
	ds_read_b128 v[226:229], v136 offset:7168
	buffer_load_dwordx4 v132, s[40:43], s12 offen lds
	s_mov_b32 m0, s92
	s_nop 0
	buffer_load_dwordx4 v133, s[40:43], s12 offen lds
	s_waitcnt vmcnt(8)
	s_waitcnt lgkmcnt(0)
	s_barrier
	s_setprio 1
	s_waitcnt lgkmcnt(6)
	v_mfma_f32_16x16x128_f8f6f4 v[124:127], v[140:147], v[198:205], v[124:127]
	v_mfma_f32_16x16x128_f8f6f4 v[120:123], v[148:155], v[198:205], v[120:123]
	s_waitcnt lgkmcnt(4)
	v_mfma_f32_16x16x128_f8f6f4 v[108:111], v[140:147], v[206:213], v[108:111]
	v_mfma_f32_16x16x128_f8f6f4 v[104:107], v[148:155], v[206:213], v[104:107]
	s_waitcnt lgkmcnt(2)
	v_mfma_f32_16x16x128_f8f6f4 v[172:175], v[140:147], v[214:221], v[92:95]
	v_mfma_f32_16x16x128_f8f6f4 v[246:249], v[148:155], v[214:221], v[88:91]
	s_waitcnt lgkmcnt(0)
	v_mfma_f32_16x16x128_f8f6f4 v[250:253], v[140:147], v[222:229], v[76:79]
	v_mfma_f32_16x16x128_f8f6f4 v[194:197], v[148:155], v[222:229], v[72:75]
	v_mfma_f32_16x16x128_f8f6f4 v[116:119], v[156:163], v[198:205], v[116:119]
	v_mfma_f32_16x16x128_f8f6f4 v[112:115], v[164:171], v[198:205], v[112:115]
	v_mfma_f32_16x16x128_f8f6f4 v[100:103], v[156:163], v[206:213], v[100:103]
	v_mfma_f32_16x16x128_f8f6f4 v[96:99], v[164:171], v[206:213], v[96:99]
	v_mfma_f32_16x16x128_f8f6f4 v[198:201], v[156:163], v[214:221], v[84:87]
	v_mfma_f32_16x16x128_f8f6f4 v[202:205], v[164:171], v[214:221], v[80:83]
	v_mfma_f32_16x16x128_f8f6f4 v[206:209], v[156:163], v[222:229], v[68:71]
	v_mfma_f32_16x16x128_f8f6f4 v[210:213], v[164:171], v[222:229], v[64:67]
	s_setprio 0
	s_barrier
	s_mov_b32 m0, s69
	s_nop 3
	ds_read_b128 v[64:67], v136 offset:16384
	ds_read_b128 v[68:71], v136 offset:17408
	ds_read_b128 v[72:75], v136 offset:18432
	ds_read_b128 v[76:79], v136 offset:19456
	ds_read_b128 v[80:83], v136 offset:20480
	ds_read_b128 v[84:87], v136 offset:21504
	ds_read_b128 v[88:91], v136 offset:22528
	ds_read_b128 v[92:95], v136 offset:23552
	buffer_load_dwordx4 v245, s[48:51], s13 offen lds
	s_mov_b32 m0, s70
	s_add_i32 s21, s13, 0x40000
	buffer_load_dwordx4 v244, s[48:51], s13 offen lds
	s_mov_b32 m0, s71
	s_nop 0
	buffer_load_dwordx4 v245, s[48:51], s21 offen lds
	s_mov_b32 m0, s72
	s_nop 0
	buffer_load_dwordx4 v244, s[48:51], s21 offen lds
	s_mov_b32 m0, s68
	s_nop 0
	buffer_load_dwordx4 v132, s[44:47], s13 offen lds
	s_mov_b32 m0, s73
	s_nop 0
	buffer_load_dwordx4 v133, s[44:47], s13 offen lds
	s_waitcnt vmcnt(8)
	s_waitcnt lgkmcnt(0)
	s_barrier
	s_setprio 1
	s_waitcnt lgkmcnt(6)
	v_mfma_f32_16x16x128_f8f6f4 v[60:63], v[140:147], v[64:71], v[60:63]
	s_waitcnt lgkmcnt(0)
	v_mfma_f32_16x16x128_f8f6f4 v[16:19], v[140:147], v[88:95], v[16:19]
	v_mfma_f32_16x16x128_f8f6f4 v[214:217], v[148:155], v[64:71], v[12:15]
	v_mfma_f32_16x16x128_f8f6f4 v[218:221], v[140:147], v[72:79], v[48:51]
	v_mfma_f32_16x16x128_f8f6f4 v[222:225], v[148:155], v[72:79], v[44:47]
	v_mfma_f32_16x16x128_f8f6f4 v[226:229], v[140:147], v[80:87], v[32:35]
	v_mfma_f32_16x16x128_f8f6f4 v[178:181], v[148:155], v[80:87], v[28:31]
	v_mfma_f32_16x16x128_f8f6f4 v[182:185], v[148:155], v[88:95], v[8:11]
	v_mfma_f32_16x16x128_f8f6f4 v[56:59], v[156:163], v[64:71], v[56:59]
	v_mfma_f32_16x16x128_f8f6f4 v[52:55], v[164:171], v[64:71], v[52:55]
	v_mfma_f32_16x16x128_f8f6f4 v[186:189], v[156:163], v[72:79], v[40:43]
	v_mfma_f32_16x16x128_f8f6f4 v[190:193], v[164:171], v[72:79], v[36:39]
	v_mfma_f32_16x16x128_f8f6f4 v[236:239], v[156:163], v[80:87], v[24:27]
	v_mfma_f32_16x16x128_f8f6f4 v[240:243], v[164:171], v[80:87], v[20:23]
	v_mfma_f32_16x16x128_f8f6f4 v[232:235], v[156:163], v[88:95], v[4:7]
	v_mfma_f32_16x16x128_f8f6f4 v[128:131], v[164:171], v[88:95], v[0:3]
	s_setprio 0
	s_barrier
	s_nop 4
	ds_read_b128 v[0:3], v137
	ds_read_b128 v[4:7], v137 offset:1024
	ds_read_b128 v[20:23], v137 offset:2048
	ds_read_b128 v[24:27], v137 offset:3072
	ds_read_b128 v[140:143], v138
	ds_read_b128 v[144:147], v138 offset:1024
	ds_read_b128 v[148:151], v138 offset:2048
	ds_read_b128 v[152:155], v138 offset:3072
	s_mov_b32 m0, s76
	ds_read_b128 v[8:11], v136 offset:32768
	ds_read_b128 v[12:15], v136 offset:33792
	ds_read_b128 v[28:31], v136 offset:34816
	ds_read_b128 v[32:35], v136 offset:35840
	ds_read_b128 v[36:39], v136 offset:36864
	ds_read_b128 v[40:43], v136 offset:37888
	ds_read_b128 v[44:47], v136 offset:38912
	ds_read_b128 v[48:51], v136 offset:39936
	buffer_load_dwordx4 v132, s[44:47], s21 offen lds
	s_mov_b32 m0, s77
	s_nop 0
	buffer_load_dwordx4 v133, s[44:47], s21 offen lds
	s_waitcnt vmcnt(8)
	s_waitcnt lgkmcnt(0)
	s_barrier
	s_setprio 1
	s_waitcnt lgkmcnt(6)
	v_mfma_f32_16x16x128_f8f6f4 v[124:127], v[0:7], v[8:15], v[124:127]
	v_mfma_f32_16x16x128_f8f6f4 v[120:123], v[20:27], v[8:15], v[120:123]
	s_waitcnt lgkmcnt(4)
	v_mfma_f32_16x16x128_f8f6f4 v[108:111], v[0:7], v[28:35], v[108:111]
	v_mfma_f32_16x16x128_f8f6f4 v[104:107], v[20:27], v[28:35], v[104:107]
	s_waitcnt lgkmcnt(2)
	v_mfma_f32_16x16x128_f8f6f4 v[92:95], v[0:7], v[36:43], v[172:175]
	v_mfma_f32_16x16x128_f8f6f4 v[88:91], v[20:27], v[36:43], v[246:249]
	s_waitcnt lgkmcnt(0)
	v_mfma_f32_16x16x128_f8f6f4 v[76:79], v[0:7], v[44:51], v[250:253]
	v_mfma_f32_16x16x128_f8f6f4 v[72:75], v[20:27], v[44:51], v[194:197]
	v_mfma_f32_16x16x128_f8f6f4 v[116:119], v[140:147], v[8:15], v[116:119]
	v_mfma_f32_16x16x128_f8f6f4 v[112:115], v[148:155], v[8:15], v[112:115]
	v_mfma_f32_16x16x128_f8f6f4 v[100:103], v[140:147], v[28:35], v[100:103]
	v_mfma_f32_16x16x128_f8f6f4 v[96:99], v[148:155], v[28:35], v[96:99]
	v_mfma_f32_16x16x128_f8f6f4 v[84:87], v[140:147], v[36:43], v[198:201]
	v_mfma_f32_16x16x128_f8f6f4 v[80:83], v[148:155], v[36:43], v[202:205]
	v_mfma_f32_16x16x128_f8f6f4 v[68:71], v[140:147], v[44:51], v[206:209]
	v_mfma_f32_16x16x128_f8f6f4 v[64:67], v[148:155], v[44:51], v[210:213]
	s_setprio 0
	s_barrier
	s_mov_b32 m0, s78
	s_or_b32 s21, s13, 0x80
	ds_read_b128 v[36:39], v136 offset:49152
	ds_read_b128 v[40:43], v136 offset:50176
	ds_read_b128 v[156:159], v136 offset:51200
	ds_read_b128 v[160:163], v136 offset:52224
	ds_read_b128 v[164:167], v136 offset:53248
	ds_read_b128 v[168:171], v136 offset:54272
	ds_read_b128 v[198:201], v136 offset:55296
	ds_read_b128 v[202:205], v136 offset:56320
	buffer_load_dwordx4 v245, s[48:51], s21 offen lds
	s_mov_b32 m0, s79
	s_add_i32 s13, s13, 0x40080
	buffer_load_dwordx4 v244, s[48:51], s21 offen lds
	s_mov_b32 m0, s83
	s_nop 0
	buffer_load_dwordx4 v245, s[48:51], s13 offen lds
	s_mov_b32 m0, s88
	s_nop 0
	buffer_load_dwordx4 v244, s[48:51], s13 offen lds
	s_mov_b32 m0, s80
	s_nop 0
	buffer_load_dwordx4 v132, s[44:47], s21 offen lds
	s_mov_b32 m0, s82
	s_nop 0
	buffer_load_dwordx4 v133, s[44:47], s21 offen lds
	s_waitcnt vmcnt(8)
	s_waitcnt lgkmcnt(0)
	s_barrier
	s_setprio 1
	s_waitcnt lgkmcnt(6)
	v_mfma_f32_16x16x128_f8f6f4 v[60:63], v[0:7], v[36:43], v[60:63]
	v_mfma_f32_16x16x128_f8f6f4 v[12:15], v[20:27], v[36:43], v[214:217]
	s_waitcnt lgkmcnt(4)
	v_mfma_f32_16x16x128_f8f6f4 v[48:51], v[0:7], v[156:163], v[218:221]
	v_mfma_f32_16x16x128_f8f6f4 v[44:47], v[20:27], v[156:163], v[222:225]
	s_waitcnt lgkmcnt(2)
	v_mfma_f32_16x16x128_f8f6f4 v[32:35], v[0:7], v[164:171], v[226:229]
	v_mfma_f32_16x16x128_f8f6f4 v[28:31], v[20:27], v[164:171], v[178:181]
	s_waitcnt lgkmcnt(0)
	v_mfma_f32_16x16x128_f8f6f4 v[16:19], v[0:7], v[198:205], v[16:19]
	v_mfma_f32_16x16x128_f8f6f4 v[8:11], v[20:27], v[198:205], v[182:185]
	v_mfma_f32_16x16x128_f8f6f4 v[56:59], v[140:147], v[36:43], v[56:59]
	v_mfma_f32_16x16x128_f8f6f4 v[52:55], v[148:155], v[36:43], v[52:55]
	v_mfma_f32_16x16x128_f8f6f4 v[40:43], v[140:147], v[156:163], v[186:189]
	v_mfma_f32_16x16x128_f8f6f4 v[36:39], v[148:155], v[156:163], v[190:193]
	v_mfma_f32_16x16x128_f8f6f4 v[24:27], v[140:147], v[164:171], v[236:239]
	v_mfma_f32_16x16x128_f8f6f4 v[20:23], v[148:155], v[164:171], v[240:243]
	v_mfma_f32_16x16x128_f8f6f4 v[4:7], v[140:147], v[198:205], v[232:235]
	v_mfma_f32_16x16x128_f8f6f4 v[0:3], v[148:155], v[198:205], v[128:131]
	s_setprio 0
	s_barrier
	s_add_i32 s1, s1, 2
	s_addk_i32 s12, 0x100
	s_cmp_gt_u32 s1, 13
	s_cbranch_scc0 .LBB0_1025
	s_and_b64 vcc, exec, s[18:19]
	s_cbranch_vccz .LBB0_1028
	s_barrier

.LBB0_1051:
	v_add_u32_e32 v140, 0x10000, v150
	v_add_u32_e32 v144, 0x14000, v150
	ds_read_b128 v[120:123], v140
	ds_read_b128 v[124:127], v140 offset:1024
	ds_read_b128 v[136:139], v140 offset:2048
	ds_read_b128 v[140:143], v140 offset:3072
	ds_read_b128 v[152:155], v144
	ds_read_b128 v[156:159], v144 offset:1024
	ds_read_b128 v[160:163], v144 offset:2048
	ds_read_b128 v[164:167], v144 offset:3072
	s_add_i32 s38, s31, 0xfffc0080
	s_cmp_eq_u32 s29, 12
	s_cselect_b32 s45, s35, s41
	s_cselect_b32 s44, s34, s40
	s_cselect_b32 s47, s9, s43
	s_cselect_b32 s46, s8, s42
	s_cselect_b32 s38, 0, s38
	s_cselect_b32 s49, s3, s53
	s_cselect_b32 s48, s2, s52
	s_cselect_b32 s51, s13, s1
	s_cselect_b32 s50, s12, s0
	s_mov_b32 m0, s89
	ds_read_b128 v[168:171], v151
	ds_read_b128 v[172:175], v151 offset:1024
	ds_read_b128 v[198:201], v151 offset:2048
	ds_read_b128 v[202:205], v151 offset:3072
	ds_read_b128 v[206:209], v151 offset:4096
	ds_read_b128 v[210:213], v151 offset:5120
	ds_read_b128 v[214:217], v151 offset:6144
	ds_read_b128 v[218:221], v151 offset:7168
	buffer_load_dwordx4 v148, s[40:43], s31 offen lds
	s_mov_b32 m0, s88
	s_nop 0
	buffer_load_dwordx4 v149, s[40:43], s31 offen lds
	s_waitcnt vmcnt(8)
	s_waitcnt lgkmcnt(0)
	s_barrier
	s_setprio 1
	s_waitcnt lgkmcnt(6)
	v_mfma_f32_16x16x128_f8f6f4 v[132:135], v[120:127], v[168:175], v[132:135]
	v_mfma_f32_16x16x128_f8f6f4 v[128:131], v[136:143], v[168:175], v[128:131]
	s_waitcnt lgkmcnt(4)
	v_mfma_f32_16x16x128_f8f6f4 v[108:111], v[120:127], v[198:205], v[108:111]
	v_mfma_f32_16x16x128_f8f6f4 v[104:107], v[136:143], v[198:205], v[104:107]
	s_waitcnt lgkmcnt(2)
	v_mfma_f32_16x16x128_f8f6f4 v[178:181], v[120:127], v[206:213], v[92:95]
	v_mfma_f32_16x16x128_f8f6f4 v[182:185], v[136:143], v[206:213], v[88:91]
	s_waitcnt lgkmcnt(0)
	v_mfma_f32_16x16x128_f8f6f4 v[186:189], v[120:127], v[214:221], v[76:79]
	v_mfma_f32_16x16x128_f8f6f4 v[190:193], v[136:143], v[214:221], v[72:75]
	v_mfma_f32_16x16x128_f8f6f4 v[116:119], v[152:159], v[168:175], v[116:119]
	v_mfma_f32_16x16x128_f8f6f4 v[112:115], v[160:167], v[168:175], v[112:115]
	v_mfma_f32_16x16x128_f8f6f4 v[100:103], v[152:159], v[198:205], v[100:103]
	v_mfma_f32_16x16x128_f8f6f4 v[96:99], v[160:167], v[198:205], v[96:99]
	v_mfma_f32_16x16x128_f8f6f4 v[168:171], v[152:159], v[206:213], v[84:87]
	v_mfma_f32_16x16x128_f8f6f4 v[172:175], v[160:167], v[206:213], v[80:83]
	v_mfma_f32_16x16x128_f8f6f4 v[194:197], v[152:159], v[214:221], v[68:71]
	v_mfma_f32_16x16x128_f8f6f4 v[198:201], v[160:167], v[214:221], v[64:67]
	s_setprio 0
	s_barrier
	s_mov_b32 m0, s77
	s_nop 3
	ds_read_b128 v[64:67], v151 offset:16384
	ds_read_b128 v[68:71], v151 offset:17408
	ds_read_b128 v[72:75], v151 offset:18432
	ds_read_b128 v[76:79], v151 offset:19456
	ds_read_b128 v[80:83], v151 offset:20480
	ds_read_b128 v[84:87], v151 offset:21504
	ds_read_b128 v[88:91], v151 offset:22528
	ds_read_b128 v[92:95], v151 offset:23552
	buffer_load_dwordx4 v146, s[48:51], s38 offen lds
	s_mov_b32 m0, s64
	s_add_i32 s39, s38, 0x40000
	buffer_load_dwordx4 v147, s[48:51], s38 offen lds
	s_mov_b32 m0, s65
	s_nop 0
	buffer_load_dwordx4 v146, s[48:51], s39 offen lds
	s_mov_b32 m0, s22
	s_nop 0
	buffer_load_dwordx4 v147, s[48:51], s39 offen lds
	s_mov_b32 m0, s92
	s_nop 0
	buffer_load_dwordx4 v148, s[44:47], s38 offen lds
	s_mov_b32 m0, s23
	s_nop 0
	buffer_load_dwordx4 v149, s[44:47], s38 offen lds
	s_waitcnt vmcnt(8)
	s_waitcnt lgkmcnt(0)
	s_barrier
	s_setprio 1
	s_waitcnt lgkmcnt(6)
	v_mfma_f32_16x16x128_f8f6f4 v[60:63], v[120:127], v[64:71], v[60:63]
	v_mfma_f32_16x16x128_f8f6f4 v[16:19], v[136:143], v[64:71], v[16:19]
	s_waitcnt lgkmcnt(4)
	v_mfma_f32_16x16x128_f8f6f4 v[202:205], v[120:127], v[72:79], v[48:51]
	v_mfma_f32_16x16x128_f8f6f4 v[206:209], v[136:143], v[72:79], v[44:47]
	s_waitcnt lgkmcnt(2)
	v_mfma_f32_16x16x128_f8f6f4 v[210:213], v[120:127], v[80:87], v[32:35]
	v_mfma_f32_16x16x128_f8f6f4 v[214:217], v[136:143], v[80:87], v[28:31]
	s_waitcnt lgkmcnt(0)
	v_mfma_f32_16x16x128_f8f6f4 v[218:221], v[120:127], v[88:95], v[12:15]
	v_mfma_f32_16x16x128_f8f6f4 v[222:225], v[136:143], v[88:95], v[8:11]
	v_mfma_f32_16x16x128_f8f6f4 v[56:59], v[152:159], v[64:71], v[56:59]
	v_mfma_f32_16x16x128_f8f6f4 v[52:55], v[160:167], v[64:71], v[52:55]
	v_mfma_f32_16x16x128_f8f6f4 v[226:229], v[152:159], v[72:79], v[40:43]
	v_mfma_f32_16x16x128_f8f6f4 v[232:235], v[160:167], v[72:79], v[36:39]
	v_mfma_f32_16x16x128_f8f6f4 v[236:239], v[152:159], v[80:87], v[24:27]
	v_mfma_f32_16x16x128_f8f6f4 v[240:243], v[160:167], v[80:87], v[20:23]
	v_mfma_f32_16x16x128_f8f6f4 v[244:247], v[152:159], v[88:95], v[4:7]
	v_mfma_f32_16x16x128_f8f6f4 v[248:251], v[160:167], v[88:95], v[0:3]
	s_setprio 0
	s_barrier
	v_add_u32_e32 v8, 0x18000, v150
	s_nop 3
	ds_read_b128 v[0:3], v8
	ds_read_b128 v[4:7], v8 offset:1024
	ds_read_b128 v[20:23], v8 offset:2048
	ds_read_b128 v[24:27], v8 offset:3072
	v_add_u32_e32 v8, 0x1c000, v150
	ds_read_b128 v[120:123], v8
	ds_read_b128 v[124:127], v8 offset:1024
	ds_read_b128 v[136:139], v8 offset:2048
	ds_read_b128 v[140:143], v8 offset:3072
	s_mov_b32 m0, s33
	ds_read_b128 v[8:11], v151 offset:32768
	ds_read_b128 v[12:15], v151 offset:33792
	ds_read_b128 v[28:31], v151 offset:34816
	ds_read_b128 v[32:35], v151 offset:35840
	ds_read_b128 v[36:39], v151 offset:36864
	ds_read_b128 v[40:43], v151 offset:37888
	ds_read_b128 v[44:47], v151 offset:38912
	ds_read_b128 v[48:51], v151 offset:39936
	buffer_load_dwordx4 v148, s[44:47], s39 offen lds
	s_mov_b32 m0, s96
	s_nop 0
	buffer_load_dwordx4 v149, s[44:47], s39 offen lds
	s_waitcnt vmcnt(8)
	s_waitcnt lgkmcnt(0)
	s_barrier
	s_setprio 1
	s_waitcnt lgkmcnt(6)
	v_mfma_f32_16x16x128_f8f6f4 v[132:135], v[0:7], v[8:15], v[132:135]
	v_mfma_f32_16x16x128_f8f6f4 v[128:131], v[20:27], v[8:15], v[128:131]
	s_waitcnt lgkmcnt(4)
	v_mfma_f32_16x16x128_f8f6f4 v[108:111], v[0:7], v[28:35], v[108:111]
	v_mfma_f32_16x16x128_f8f6f4 v[104:107], v[20:27], v[28:35], v[104:107]
	s_waitcnt lgkmcnt(2)
	v_mfma_f32_16x16x128_f8f6f4 v[92:95], v[0:7], v[36:43], v[178:181]
	v_mfma_f32_16x16x128_f8f6f4 v[88:91], v[20:27], v[36:43], v[182:185]
	s_waitcnt lgkmcnt(0)
	v_mfma_f32_16x16x128_f8f6f4 v[76:79], v[0:7], v[44:51], v[186:189]
	v_mfma_f32_16x16x128_f8f6f4 v[72:75], v[20:27], v[44:51], v[190:193]
	v_mfma_f32_16x16x128_f8f6f4 v[116:119], v[120:127], v[8:15], v[116:119]
	v_mfma_f32_16x16x128_f8f6f4 v[112:115], v[136:143], v[8:15], v[112:115]
	v_mfma_f32_16x16x128_f8f6f4 v[100:103], v[120:127], v[28:35], v[100:103]
	v_mfma_f32_16x16x128_f8f6f4 v[96:99], v[136:143], v[28:35], v[96:99]
	v_mfma_f32_16x16x128_f8f6f4 v[84:87], v[120:127], v[36:43], v[168:171]
	v_mfma_f32_16x16x128_f8f6f4 v[80:83], v[136:143], v[36:43], v[172:175]
	v_mfma_f32_16x16x128_f8f6f4 v[68:71], v[120:127], v[44:51], v[194:197]
	v_mfma_f32_16x16x128_f8f6f4 v[64:67], v[136:143], v[44:51], v[198:201]
	s_setprio 0
	s_barrier
	s_mov_b32 m0, s69
	s_or_b32 s39, s38, 0x80
	ds_read_b128 v[36:39], v151 offset:49152
	ds_read_b128 v[40:43], v151 offset:50176
	ds_read_b128 v[152:155], v151 offset:51200
	ds_read_b128 v[156:159], v151 offset:52224
	ds_read_b128 v[160:163], v151 offset:53248
	ds_read_b128 v[164:167], v151 offset:54272
	ds_read_b128 v[168:171], v151 offset:55296
	ds_read_b128 v[172:175], v151 offset:56320
	buffer_load_dwordx4 v146, s[48:51], s39 offen lds
	s_mov_b32 m0, s61
	s_add_i32 s38, s38, 0x40080
	buffer_load_dwordx4 v147, s[48:51], s39 offen lds
	s_mov_b32 m0, s83
	s_nop 0
	buffer_load_dwordx4 v146, s[48:51], s38 offen lds
	s_mov_b32 m0, s82
	s_nop 0
	buffer_load_dwordx4 v147, s[48:51], s38 offen lds
	s_mov_b32 m0, s71
	s_nop 0
	buffer_load_dwordx4 v148, s[44:47], s39 offen lds
	s_mov_b32 m0, s70
	s_nop 0
	buffer_load_dwordx4 v149, s[44:47], s39 offen lds
	s_waitcnt vmcnt(8)
	s_waitcnt lgkmcnt(0)
	s_barrier
	s_setprio 1
	s_waitcnt lgkmcnt(6)
	v_mfma_f32_16x16x128_f8f6f4 v[60:63], v[0:7], v[36:43], v[60:63]
	v_mfma_f32_16x16x128_f8f6f4 v[16:19], v[20:27], v[36:43], v[16:19]
	s_waitcnt lgkmcnt(4)
	v_mfma_f32_16x16x128_f8f6f4 v[48:51], v[0:7], v[152:159], v[202:205]
	v_mfma_f32_16x16x128_f8f6f4 v[44:47], v[20:27], v[152:159], v[206:209]
	s_waitcnt lgkmcnt(2)
	v_mfma_f32_16x16x128_f8f6f4 v[32:35], v[0:7], v[160:167], v[210:213]
	v_mfma_f32_16x16x128_f8f6f4 v[28:31], v[20:27], v[160:167], v[214:217]
	s_waitcnt lgkmcnt(0)
	v_mfma_f32_16x16x128_f8f6f4 v[12:15], v[0:7], v[168:175], v[218:221]
	v_mfma_f32_16x16x128_f8f6f4 v[8:11], v[20:27], v[168:175], v[222:225]
	v_mfma_f32_16x16x128_f8f6f4 v[56:59], v[120:127], v[36:43], v[56:59]
	v_mfma_f32_16x16x128_f8f6f4 v[52:55], v[136:143], v[36:43], v[52:55]
	v_mfma_f32_16x16x128_f8f6f4 v[40:43], v[120:127], v[152:159], v[226:229]
	v_mfma_f32_16x16x128_f8f6f4 v[36:39], v[136:143], v[152:159], v[232:235]
	v_mfma_f32_16x16x128_f8f6f4 v[24:27], v[120:127], v[160:167], v[236:239]
	v_mfma_f32_16x16x128_f8f6f4 v[20:23], v[136:143], v[160:167], v[240:243]
	v_mfma_f32_16x16x128_f8f6f4 v[4:7], v[120:127], v[168:175], v[244:247]
	v_mfma_f32_16x16x128_f8f6f4 v[0:3], v[136:143], v[168:175], v[248:251]
	s_setprio 0
	s_barrier
	s_add_i32 s29, s29, 2
	s_addk_i32 s31, 0x100
	s_cmp_gt_u32 s29, 13
	s_cbranch_scc0 .LBB0_1051
	s_and_b64 vcc, exec, s[62:63]
	s_cbranch_vccz .LBB0_1054
	s_barrier

.LBB0_1187:
	v_add_u32_e32 v140, 0x10000, v148
	v_add_u32_e32 v162, 0x14000, v148
	ds_read_b128 v[128:131], v140
	ds_read_b128 v[132:135], v140 offset:1024
	ds_read_b128 v[136:139], v140 offset:2048
	ds_read_b128 v[140:143], v140 offset:3072
	ds_read_b128 v[150:153], v162
	ds_read_b128 v[154:157], v162 offset:1024
	ds_read_b128 v[158:161], v162 offset:2048
	ds_read_b128 v[162:165], v162 offset:3072
	s_add_i32 s19, s13, 0xfffc0080
	s_cmp_eq_u32 s12, 12
	s_cselect_b32 s45, s23, s41
	s_cselect_b32 s44, s22, s40
	s_cselect_b32 s47, s29, s43
	s_cselect_b32 s46, s28, s42
	s_cselect_b32 s19, 0, s19
	s_cselect_b32 s49, s31, s53
	s_cselect_b32 s48, s30, s52
	s_cselect_b32 s51, s35, s5
	s_cselect_b32 s50, s34, s4
	s_mov_b32 m0, s83
	ds_read_b128 v[166:169], v149
	ds_read_b128 v[170:173], v149 offset:1024
	ds_read_b128 v[198:201], v149 offset:2048
	ds_read_b128 v[202:205], v149 offset:3072
	ds_read_b128 v[206:209], v149 offset:4096
	ds_read_b128 v[210:213], v149 offset:5120
	ds_read_b128 v[214:217], v149 offset:6144
	ds_read_b128 v[218:221], v149 offset:7168
	buffer_load_dwordx4 v146, s[40:43], s13 offen lds
	s_mov_b32 m0, s91
	s_nop 0
	buffer_load_dwordx4 v147, s[40:43], s13 offen lds
	s_waitcnt vmcnt(8)
	s_waitcnt lgkmcnt(0)
	s_barrier
	s_setprio 1
	s_waitcnt lgkmcnt(6)
	v_mfma_f32_16x16x128_f8f6f4 v[124:127], v[128:135], v[166:173], v[124:127]
	v_mfma_f32_16x16x128_f8f6f4 v[120:123], v[136:143], v[166:173], v[120:123]
	s_waitcnt lgkmcnt(4)
	v_mfma_f32_16x16x128_f8f6f4 v[108:111], v[128:135], v[198:205], v[108:111]
	v_mfma_f32_16x16x128_f8f6f4 v[104:107], v[136:143], v[198:205], v[104:107]
	s_waitcnt lgkmcnt(2)
	v_mfma_f32_16x16x128_f8f6f4 v[178:181], v[128:135], v[206:213], v[92:95]
	v_mfma_f32_16x16x128_f8f6f4 v[182:185], v[136:143], v[206:213], v[88:91]
	s_waitcnt lgkmcnt(0)
	v_mfma_f32_16x16x128_f8f6f4 v[186:189], v[128:135], v[214:221], v[76:79]
	v_mfma_f32_16x16x128_f8f6f4 v[190:193], v[136:143], v[214:221], v[72:75]
	v_mfma_f32_16x16x128_f8f6f4 v[116:119], v[150:157], v[166:173], v[116:119]
	v_mfma_f32_16x16x128_f8f6f4 v[112:115], v[158:165], v[166:173], v[112:115]
	v_mfma_f32_16x16x128_f8f6f4 v[100:103], v[150:157], v[198:205], v[100:103]
	v_mfma_f32_16x16x128_f8f6f4 v[96:99], v[158:165], v[198:205], v[96:99]
	v_mfma_f32_16x16x128_f8f6f4 v[166:169], v[150:157], v[206:213], v[84:87]
	v_mfma_f32_16x16x128_f8f6f4 v[170:173], v[158:165], v[206:213], v[80:83]
	v_mfma_f32_16x16x128_f8f6f4 v[194:197], v[150:157], v[214:221], v[68:71]
	v_mfma_f32_16x16x128_f8f6f4 v[198:201], v[158:165], v[214:221], v[64:67]
	s_setprio 0
	s_barrier
	s_mov_b32 m0, s66
	s_nop 3
	ds_read_b128 v[64:67], v149 offset:16384
	ds_read_b128 v[68:71], v149 offset:17408
	ds_read_b128 v[72:75], v149 offset:18432
	ds_read_b128 v[76:79], v149 offset:19456
	ds_read_b128 v[80:83], v149 offset:20480
	ds_read_b128 v[84:87], v149 offset:21504
	ds_read_b128 v[88:91], v149 offset:22528
	ds_read_b128 v[92:95], v149 offset:23552
	buffer_load_dwordx4 v144, s[48:51], s19 offen lds
	s_mov_b32 m0, s67
	s_add_i32 s21, s19, 0x40000
	buffer_load_dwordx4 v145, s[48:51], s19 offen lds
	s_mov_b32 m0, s68
	s_nop 0
	buffer_load_dwordx4 v144, s[48:51], s21 offen lds
	s_mov_b32 m0, s69
	s_nop 0
	buffer_load_dwordx4 v145, s[48:51], s21 offen lds
	s_mov_b32 m0, s63
	s_nop 0
	buffer_load_dwordx4 v146, s[44:47], s19 offen lds
	s_mov_b32 m0, s70
	s_nop 0
	buffer_load_dwordx4 v147, s[44:47], s19 offen lds
	s_waitcnt vmcnt(8)
	s_waitcnt lgkmcnt(0)
	s_barrier
	s_setprio 1
	s_waitcnt lgkmcnt(6)
	v_mfma_f32_16x16x128_f8f6f4 v[60:63], v[128:135], v[64:71], v[60:63]
	v_mfma_f32_16x16x128_f8f6f4 v[0:3], v[136:143], v[64:71], v[0:3]
	s_waitcnt lgkmcnt(4)
	v_mfma_f32_16x16x128_f8f6f4 v[202:205], v[128:135], v[72:79], v[48:51]
	v_mfma_f32_16x16x128_f8f6f4 v[206:209], v[136:143], v[72:79], v[44:47]
	s_waitcnt lgkmcnt(2)
	v_mfma_f32_16x16x128_f8f6f4 v[210:213], v[128:135], v[80:87], v[32:35]
	v_mfma_f32_16x16x128_f8f6f4 v[214:217], v[136:143], v[80:87], v[28:31]
	s_waitcnt lgkmcnt(0)
	v_mfma_f32_16x16x128_f8f6f4 v[218:221], v[128:135], v[88:95], v[16:19]
	v_mfma_f32_16x16x128_f8f6f4 v[222:225], v[136:143], v[88:95], v[12:15]
	v_mfma_f32_16x16x128_f8f6f4 v[56:59], v[150:157], v[64:71], v[56:59]
	v_mfma_f32_16x16x128_f8f6f4 v[52:55], v[158:165], v[64:71], v[52:55]
	v_mfma_f32_16x16x128_f8f6f4 v[226:229], v[150:157], v[72:79], v[40:43]
	v_mfma_f32_16x16x128_f8f6f4 v[232:235], v[158:165], v[72:79], v[36:39]
	v_mfma_f32_16x16x128_f8f6f4 v[236:239], v[150:157], v[80:87], v[24:27]
	v_mfma_f32_16x16x128_f8f6f4 v[240:243], v[158:165], v[80:87], v[20:23]
	v_mfma_f32_16x16x128_f8f6f4 v[244:247], v[150:157], v[88:95], v[8:11]
	v_mfma_f32_16x16x128_f8f6f4 v[248:251], v[158:165], v[88:95], v[4:7]
	s_setprio 0
	s_barrier
	v_add_u32_e32 v12, 0x18000, v148
	s_nop 3
	ds_read_b128 v[4:7], v12
	ds_read_b128 v[8:11], v12 offset:1024
	ds_read_b128 v[20:23], v12 offset:2048
	ds_read_b128 v[24:27], v12 offset:3072
	v_add_u32_e32 v12, 0x1c000, v148
	ds_read_b128 v[128:131], v12
	ds_read_b128 v[132:135], v12 offset:1024
	ds_read_b128 v[136:139], v12 offset:2048
	ds_read_b128 v[140:143], v12 offset:3072
	s_mov_b32 m0, s71
	ds_read_b128 v[12:15], v149 offset:32768
	ds_read_b128 v[16:19], v149 offset:33792
	ds_read_b128 v[28:31], v149 offset:34816
	ds_read_b128 v[32:35], v149 offset:35840
	ds_read_b128 v[36:39], v149 offset:36864
	ds_read_b128 v[40:43], v149 offset:37888
	ds_read_b128 v[44:47], v149 offset:38912
	ds_read_b128 v[48:51], v149 offset:39936
	buffer_load_dwordx4 v146, s[44:47], s21 offen lds
	s_mov_b32 m0, s72
	s_nop 0
	buffer_load_dwordx4 v147, s[44:47], s21 offen lds
	s_waitcnt vmcnt(8)
	s_waitcnt lgkmcnt(0)
	s_barrier
	s_setprio 1
	s_waitcnt lgkmcnt(6)
	v_mfma_f32_16x16x128_f8f6f4 v[124:127], v[4:11], v[12:19], v[124:127]
	v_mfma_f32_16x16x128_f8f6f4 v[120:123], v[20:27], v[12:19], v[120:123]
	s_waitcnt lgkmcnt(4)
	v_mfma_f32_16x16x128_f8f6f4 v[108:111], v[4:11], v[28:35], v[108:111]
	v_mfma_f32_16x16x128_f8f6f4 v[104:107], v[20:27], v[28:35], v[104:107]
	s_waitcnt lgkmcnt(2)
	v_mfma_f32_16x16x128_f8f6f4 v[92:95], v[4:11], v[36:43], v[178:181]
	v_mfma_f32_16x16x128_f8f6f4 v[88:91], v[20:27], v[36:43], v[182:185]
	s_waitcnt lgkmcnt(0)
	v_mfma_f32_16x16x128_f8f6f4 v[76:79], v[4:11], v[44:51], v[186:189]
	v_mfma_f32_16x16x128_f8f6f4 v[72:75], v[20:27], v[44:51], v[190:193]
	v_mfma_f32_16x16x128_f8f6f4 v[116:119], v[128:135], v[12:19], v[116:119]
	v_mfma_f32_16x16x128_f8f6f4 v[112:115], v[136:143], v[12:19], v[112:115]
	v_mfma_f32_16x16x128_f8f6f4 v[100:103], v[128:135], v[28:35], v[100:103]
	v_mfma_f32_16x16x128_f8f6f4 v[96:99], v[136:143], v[28:35], v[96:99]
	v_mfma_f32_16x16x128_f8f6f4 v[84:87], v[128:135], v[36:43], v[166:169]
	v_mfma_f32_16x16x128_f8f6f4 v[80:83], v[136:143], v[36:43], v[170:173]
	v_mfma_f32_16x16x128_f8f6f4 v[68:71], v[128:135], v[44:51], v[194:197]
	v_mfma_f32_16x16x128_f8f6f4 v[64:67], v[136:143], v[44:51], v[198:201]
	s_setprio 0
	s_barrier
	s_mov_b32 m0, s76
	s_or_b32 s21, s19, 0x80
	ds_read_b128 v[36:39], v149 offset:49152
	ds_read_b128 v[40:43], v149 offset:50176
	ds_read_b128 v[150:153], v149 offset:51200
	ds_read_b128 v[154:157], v149 offset:52224
	ds_read_b128 v[158:161], v149 offset:53248
	ds_read_b128 v[162:165], v149 offset:54272
	ds_read_b128 v[166:169], v149 offset:55296
	ds_read_b128 v[170:173], v149 offset:56320
	buffer_load_dwordx4 v144, s[48:51], s21 offen lds
	s_mov_b32 m0, s77
	s_add_i32 s19, s19, 0x40080
	buffer_load_dwordx4 v145, s[48:51], s21 offen lds
	s_mov_b32 m0, s80
	s_nop 0
	buffer_load_dwordx4 v144, s[48:51], s19 offen lds
	s_mov_b32 m0, s82
	s_nop 0
	buffer_load_dwordx4 v145, s[48:51], s19 offen lds
	s_mov_b32 m0, s78
	s_nop 0
	buffer_load_dwordx4 v146, s[44:47], s21 offen lds
	s_mov_b32 m0, s79
	s_nop 0
	buffer_load_dwordx4 v147, s[44:47], s21 offen lds
	s_waitcnt vmcnt(8)
	s_waitcnt lgkmcnt(0)
	s_barrier
	s_setprio 1
	s_waitcnt lgkmcnt(6)
	v_mfma_f32_16x16x128_f8f6f4 v[60:63], v[4:11], v[36:43], v[60:63]
	v_mfma_f32_16x16x128_f8f6f4 v[0:3], v[20:27], v[36:43], v[0:3]
	s_waitcnt lgkmcnt(4)
	v_mfma_f32_16x16x128_f8f6f4 v[48:51], v[4:11], v[150:157], v[202:205]
	v_mfma_f32_16x16x128_f8f6f4 v[44:47], v[20:27], v[150:157], v[206:209]
	s_waitcnt lgkmcnt(2)
	v_mfma_f32_16x16x128_f8f6f4 v[32:35], v[4:11], v[158:165], v[210:213]
	v_mfma_f32_16x16x128_f8f6f4 v[28:31], v[20:27], v[158:165], v[214:217]
	s_waitcnt lgkmcnt(0)
	v_mfma_f32_16x16x128_f8f6f4 v[16:19], v[4:11], v[166:173], v[218:221]
	v_mfma_f32_16x16x128_f8f6f4 v[12:15], v[20:27], v[166:173], v[222:225]
	v_mfma_f32_16x16x128_f8f6f4 v[56:59], v[128:135], v[36:43], v[56:59]
	v_mfma_f32_16x16x128_f8f6f4 v[52:55], v[136:143], v[36:43], v[52:55]
	v_mfma_f32_16x16x128_f8f6f4 v[40:43], v[128:135], v[150:157], v[226:229]
	v_mfma_f32_16x16x128_f8f6f4 v[36:39], v[136:143], v[150:157], v[232:235]
	v_mfma_f32_16x16x128_f8f6f4 v[24:27], v[128:135], v[158:165], v[236:239]
	v_mfma_f32_16x16x128_f8f6f4 v[20:23], v[136:143], v[158:165], v[240:243]
	v_mfma_f32_16x16x128_f8f6f4 v[8:11], v[128:135], v[166:173], v[244:247]
	v_mfma_f32_16x16x128_f8f6f4 v[4:7], v[136:143], v[166:173], v[248:251]
	s_setprio 0
	s_barrier
	s_add_i32 s12, s12, 2
	s_addk_i32 s13, 0x100
	s_cmp_gt_u32 s12, 13
	s_cbranch_scc0 .LBB0_1187
	s_and_b64 vcc, exec, s[8:9]
	s_cbranch_vccz .LBB0_1190
	s_barrier

.LBB0_1217:
	v_add_u32_e32 v132, 0x10000, v150
	v_add_u32_e32 v144, 0x14000, v150
	ds_read_b128 v[112:115], v132
	ds_read_b128 v[116:119], v132 offset:1024
	ds_read_b128 v[128:131], v132 offset:2048
	ds_read_b128 v[132:135], v132 offset:3072
	ds_read_b128 v[152:155], v144
	ds_read_b128 v[156:159], v144 offset:1024
	ds_read_b128 v[160:163], v144 offset:2048
	ds_read_b128 v[164:167], v144 offset:3072
	s_add_i32 s19, s13, 0xfff80080
	s_cmp_eq_u32 s12, 28
	s_cselect_b32 s45, s21, s41
	s_cselect_b32 s44, s20, s40
	s_cselect_b32 s47, s23, s43
	s_cselect_b32 s46, s22, s42
	s_cselect_b32 s19, 0, s19
	s_cselect_b32 s49, s29, s53
	s_cselect_b32 s48, s28, s52
	s_cselect_b32 s51, s31, s5
	s_cselect_b32 s50, s30, s4
	s_mov_b32 m0, s83
	ds_read_b128 v[168:171], v151
	ds_read_b128 v[172:175], v151 offset:1024
	ds_read_b128 v[178:181], v151 offset:2048
	ds_read_b128 v[182:185], v151 offset:3072
	ds_read_b128 v[186:189], v151 offset:4096
	ds_read_b128 v[190:193], v151 offset:5120
	ds_read_b128 v[194:197], v151 offset:6144
	ds_read_b128 v[198:201], v151 offset:7168
	buffer_load_dwordx4 v148, s[40:43], s13 offen lds
	s_mov_b32 m0, s90
	s_nop 0
	buffer_load_dwordx4 v149, s[40:43], s13 offen lds
	s_waitcnt vmcnt(8)
	s_waitcnt lgkmcnt(0)
	s_barrier
	s_setprio 1
	s_waitcnt lgkmcnt(7)
	v_mfma_f32_16x16x32_bf16 v[140:143], v[112:115], v[168:171], v[140:143]
	v_mfma_f32_16x16x32_bf16 v[136:139], v[128:131], v[168:171], v[136:139]
	s_waitcnt lgkmcnt(5)
	v_mfma_f32_16x16x32_bf16 v[108:111], v[112:115], v[178:181], v[108:111]
	v_mfma_f32_16x16x32_bf16 v[104:107], v[128:131], v[178:181], v[104:107]
	s_waitcnt lgkmcnt(3)
	v_mfma_f32_16x16x32_bf16 v[92:95], v[112:115], v[186:189], v[92:95]
	v_mfma_f32_16x16x32_bf16 v[88:91], v[128:131], v[186:189], v[88:91]
	s_waitcnt lgkmcnt(1)
	v_mfma_f32_16x16x32_bf16 v[76:79], v[112:115], v[194:197], v[76:79]
	v_mfma_f32_16x16x32_bf16 v[72:75], v[128:131], v[194:197], v[72:75]
	v_mfma_f32_16x16x32_bf16 v[140:143], v[116:119], v[172:175], v[140:143]
	v_mfma_f32_16x16x32_bf16 v[136:139], v[132:135], v[172:175], v[136:139]
	v_mfma_f32_16x16x32_bf16 v[108:111], v[116:119], v[182:185], v[108:111]
	v_mfma_f32_16x16x32_bf16 v[104:107], v[132:135], v[182:185], v[104:107]
	v_mfma_f32_16x16x32_bf16 v[92:95], v[116:119], v[190:193], v[92:95]
	v_mfma_f32_16x16x32_bf16 v[88:91], v[132:135], v[190:193], v[88:91]
	s_waitcnt lgkmcnt(0)
	v_mfma_f32_16x16x32_bf16 v[76:79], v[116:119], v[198:201], v[76:79]
	v_mfma_f32_16x16x32_bf16 v[72:75], v[132:135], v[198:201], v[72:75]
	v_mfma_f32_16x16x32_bf16 v[124:127], v[152:155], v[168:171], v[124:127]
	v_mfma_f32_16x16x32_bf16 v[120:123], v[160:163], v[168:171], v[120:123]
	v_mfma_f32_16x16x32_bf16 v[100:103], v[152:155], v[178:181], v[100:103]
	v_mfma_f32_16x16x32_bf16 v[96:99], v[160:163], v[178:181], v[96:99]
	v_mfma_f32_16x16x32_bf16 v[84:87], v[152:155], v[186:189], v[84:87]
	v_mfma_f32_16x16x32_bf16 v[80:83], v[160:163], v[186:189], v[80:83]
	v_mfma_f32_16x16x32_bf16 v[68:71], v[152:155], v[194:197], v[68:71]
	v_mfma_f32_16x16x32_bf16 v[64:67], v[160:163], v[194:197], v[64:67]
	v_mfma_f32_16x16x32_bf16 v[124:127], v[156:159], v[172:175], v[124:127]
	v_mfma_f32_16x16x32_bf16 v[120:123], v[164:167], v[172:175], v[120:123]
	v_mfma_f32_16x16x32_bf16 v[100:103], v[156:159], v[182:185], v[100:103]
	v_mfma_f32_16x16x32_bf16 v[96:99], v[164:167], v[182:185], v[96:99]
	v_mfma_f32_16x16x32_bf16 v[84:87], v[156:159], v[190:193], v[84:87]
	v_mfma_f32_16x16x32_bf16 v[80:83], v[164:167], v[190:193], v[80:83]
	v_mfma_f32_16x16x32_bf16 v[68:71], v[156:159], v[198:201], v[68:71]
	v_mfma_f32_16x16x32_bf16 v[64:67], v[164:167], v[198:201], v[64:67]
	s_setprio 0
	s_barrier
	s_mov_b32 m0, s65
	ds_read_b128 v[168:171], v151 offset:16384
	ds_read_b128 v[172:175], v151 offset:17408
	ds_read_b128 v[178:181], v151 offset:18432
	ds_read_b128 v[182:185], v151 offset:19456
	ds_read_b128 v[186:189], v151 offset:20480
	ds_read_b128 v[190:193], v151 offset:21504
	ds_read_b128 v[194:197], v151 offset:22528
	ds_read_b128 v[198:201], v151 offset:23552
	buffer_load_dwordx4 v146, s[48:51], s19 offen lds
	s_mov_b32 m0, s66
	s_add_i32 s35, s19, 0x1000
	buffer_load_dwordx4 v147, s[48:51], s19 offen lds
	s_mov_b32 m0, s67
	s_nop 0
	buffer_load_dwordx4 v146, s[48:51], s35 offen lds
	s_mov_b32 m0, s68
	s_nop 0
	buffer_load_dwordx4 v147, s[48:51], s35 offen lds
	s_mov_b32 m0, s64
	s_nop 0
	buffer_load_dwordx4 v148, s[44:47], s19 offen lds
	s_mov_b32 m0, s69
	s_nop 0
	buffer_load_dwordx4 v149, s[44:47], s19 offen lds
	s_waitcnt vmcnt(8)
	s_waitcnt lgkmcnt(0)
	s_barrier
	s_setprio 1
	s_waitcnt lgkmcnt(7)
	v_mfma_f32_16x16x32_bf16 v[60:63], v[112:115], v[168:171], v[60:63]
	v_mfma_f32_16x16x32_bf16 v[0:3], v[128:131], v[168:171], v[0:3]
	s_waitcnt lgkmcnt(5)
	v_mfma_f32_16x16x32_bf16 v[48:51], v[112:115], v[178:181], v[48:51]
	v_mfma_f32_16x16x32_bf16 v[44:47], v[128:131], v[178:181], v[44:47]
	s_waitcnt lgkmcnt(3)
	v_mfma_f32_16x16x32_bf16 v[32:35], v[112:115], v[186:189], v[32:35]
	v_mfma_f32_16x16x32_bf16 v[28:31], v[128:131], v[186:189], v[28:31]
	s_waitcnt lgkmcnt(1)
	v_mfma_f32_16x16x32_bf16 v[16:19], v[112:115], v[194:197], v[16:19]
	v_mfma_f32_16x16x32_bf16 v[12:15], v[128:131], v[194:197], v[12:15]
	v_mfma_f32_16x16x32_bf16 v[60:63], v[116:119], v[172:175], v[60:63]
	v_mfma_f32_16x16x32_bf16 v[0:3], v[132:135], v[172:175], v[0:3]
	v_mfma_f32_16x16x32_bf16 v[48:51], v[116:119], v[182:185], v[48:51]
	v_mfma_f32_16x16x32_bf16 v[44:47], v[132:135], v[182:185], v[44:47]
	v_mfma_f32_16x16x32_bf16 v[32:35], v[116:119], v[190:193], v[32:35]
	v_mfma_f32_16x16x32_bf16 v[28:31], v[132:135], v[190:193], v[28:31]
	s_waitcnt lgkmcnt(0)
	v_mfma_f32_16x16x32_bf16 v[16:19], v[116:119], v[198:201], v[16:19]
	v_mfma_f32_16x16x32_bf16 v[12:15], v[132:135], v[198:201], v[12:15]
	v_mfma_f32_16x16x32_bf16 v[56:59], v[152:155], v[168:171], v[56:59]
	v_mfma_f32_16x16x32_bf16 v[52:55], v[160:163], v[168:171], v[52:55]
	v_mfma_f32_16x16x32_bf16 v[40:43], v[152:155], v[178:181], v[40:43]
	v_mfma_f32_16x16x32_bf16 v[36:39], v[160:163], v[178:181], v[36:39]
	v_mfma_f32_16x16x32_bf16 v[24:27], v[152:155], v[186:189], v[24:27]
	v_mfma_f32_16x16x32_bf16 v[20:23], v[160:163], v[186:189], v[20:23]
	v_mfma_f32_16x16x32_bf16 v[8:11], v[152:155], v[194:197], v[8:11]
	v_mfma_f32_16x16x32_bf16 v[4:7], v[160:163], v[194:197], v[4:7]
	v_mfma_f32_16x16x32_bf16 v[56:59], v[156:159], v[172:175], v[56:59]
	v_mfma_f32_16x16x32_bf16 v[52:55], v[164:167], v[172:175], v[52:55]
	v_mfma_f32_16x16x32_bf16 v[40:43], v[156:159], v[182:185], v[40:43]
	v_mfma_f32_16x16x32_bf16 v[36:39], v[164:167], v[182:185], v[36:39]
	v_mfma_f32_16x16x32_bf16 v[24:27], v[156:159], v[190:193], v[24:27]
	v_mfma_f32_16x16x32_bf16 v[20:23], v[164:167], v[190:193], v[20:23]
	v_mfma_f32_16x16x32_bf16 v[8:11], v[156:159], v[198:201], v[8:11]
	v_mfma_f32_16x16x32_bf16 v[4:7], v[164:167], v[198:201], v[4:7]
	s_setprio 0
	s_barrier
	v_add_u32_e32 v132, 0x18000, v150
	v_add_u32_e32 v144, 0x1c000, v150
	ds_read_b128 v[112:115], v132
	ds_read_b128 v[116:119], v132 offset:1024
	ds_read_b128 v[128:131], v132 offset:2048
	ds_read_b128 v[132:135], v132 offset:3072
	ds_read_b128 v[152:155], v144
	ds_read_b128 v[156:159], v144 offset:1024
	ds_read_b128 v[160:163], v144 offset:2048
	ds_read_b128 v[164:167], v144 offset:3072
	s_add_i32 s35, s19, 0x80000
	s_mov_b32 m0, s70
	ds_read_b128 v[168:171], v151 offset:32768
	ds_read_b128 v[172:175], v151 offset:33792
	ds_read_b128 v[178:181], v151 offset:34816
	ds_read_b128 v[182:185], v151 offset:35840
	ds_read_b128 v[186:189], v151 offset:36864
	ds_read_b128 v[190:193], v151 offset:37888
	ds_read_b128 v[194:197], v151 offset:38912
	ds_read_b128 v[198:201], v151 offset:39936
	buffer_load_dwordx4 v148, s[44:47], s35 offen lds
	s_mov_b32 m0, s71
	s_nop 0
	buffer_load_dwordx4 v149, s[44:47], s35 offen lds
	s_waitcnt vmcnt(8)
	s_waitcnt lgkmcnt(0)
	s_barrier
	s_setprio 1
	s_waitcnt lgkmcnt(7)
	v_mfma_f32_16x16x32_bf16 v[140:143], v[112:115], v[168:171], v[140:143]
	v_mfma_f32_16x16x32_bf16 v[136:139], v[128:131], v[168:171], v[136:139]
	s_waitcnt lgkmcnt(5)
	v_mfma_f32_16x16x32_bf16 v[108:111], v[112:115], v[178:181], v[108:111]
	v_mfma_f32_16x16x32_bf16 v[104:107], v[128:131], v[178:181], v[104:107]
	s_waitcnt lgkmcnt(3)
	v_mfma_f32_16x16x32_bf16 v[92:95], v[112:115], v[186:189], v[92:95]
	v_mfma_f32_16x16x32_bf16 v[88:91], v[128:131], v[186:189], v[88:91]
	s_waitcnt lgkmcnt(1)
	v_mfma_f32_16x16x32_bf16 v[76:79], v[112:115], v[194:197], v[76:79]
	v_mfma_f32_16x16x32_bf16 v[72:75], v[128:131], v[194:197], v[72:75]
	v_mfma_f32_16x16x32_bf16 v[140:143], v[116:119], v[172:175], v[140:143]
	v_mfma_f32_16x16x32_bf16 v[136:139], v[132:135], v[172:175], v[136:139]
	v_mfma_f32_16x16x32_bf16 v[108:111], v[116:119], v[182:185], v[108:111]
	v_mfma_f32_16x16x32_bf16 v[104:107], v[132:135], v[182:185], v[104:107]
	v_mfma_f32_16x16x32_bf16 v[92:95], v[116:119], v[190:193], v[92:95]
	v_mfma_f32_16x16x32_bf16 v[88:91], v[132:135], v[190:193], v[88:91]
	s_waitcnt lgkmcnt(0)
	v_mfma_f32_16x16x32_bf16 v[76:79], v[116:119], v[198:201], v[76:79]
	v_mfma_f32_16x16x32_bf16 v[72:75], v[132:135], v[198:201], v[72:75]
	v_mfma_f32_16x16x32_bf16 v[124:127], v[152:155], v[168:171], v[124:127]
	v_mfma_f32_16x16x32_bf16 v[120:123], v[160:163], v[168:171], v[120:123]
	v_mfma_f32_16x16x32_bf16 v[100:103], v[152:155], v[178:181], v[100:103]
	v_mfma_f32_16x16x32_bf16 v[96:99], v[160:163], v[178:181], v[96:99]
	v_mfma_f32_16x16x32_bf16 v[84:87], v[152:155], v[186:189], v[84:87]
	v_mfma_f32_16x16x32_bf16 v[80:83], v[160:163], v[186:189], v[80:83]
	v_mfma_f32_16x16x32_bf16 v[68:71], v[152:155], v[194:197], v[68:71]
	v_mfma_f32_16x16x32_bf16 v[64:67], v[160:163], v[194:197], v[64:67]
	v_mfma_f32_16x16x32_bf16 v[124:127], v[156:159], v[172:175], v[124:127]
	v_mfma_f32_16x16x32_bf16 v[120:123], v[164:167], v[172:175], v[120:123]
	v_mfma_f32_16x16x32_bf16 v[100:103], v[156:159], v[182:185], v[100:103]
	v_mfma_f32_16x16x32_bf16 v[96:99], v[164:167], v[182:185], v[96:99]
	v_mfma_f32_16x16x32_bf16 v[84:87], v[156:159], v[190:193], v[84:87]
	v_mfma_f32_16x16x32_bf16 v[80:83], v[164:167], v[190:193], v[80:83]
	v_mfma_f32_16x16x32_bf16 v[68:71], v[156:159], v[198:201], v[68:71]
	v_mfma_f32_16x16x32_bf16 v[64:67], v[164:167], v[198:201], v[64:67]
	s_setprio 0
	s_barrier
	s_mov_b32 m0, s76
	s_or_b32 s35, s19, 0x80
	ds_read_b128 v[168:171], v151 offset:49152
	ds_read_b128 v[172:175], v151 offset:50176
	ds_read_b128 v[178:181], v151 offset:51200
	ds_read_b128 v[182:185], v151 offset:52224
	ds_read_b128 v[186:189], v151 offset:53248
	ds_read_b128 v[190:193], v151 offset:54272
	ds_read_b128 v[194:197], v151 offset:55296
	ds_read_b128 v[198:201], v151 offset:56320
	buffer_load_dwordx4 v146, s[48:51], s35 offen lds
	s_mov_b32 m0, s77
	s_addk_i32 s19, 0x1080
	buffer_load_dwordx4 v147, s[48:51], s35 offen lds
	s_mov_b32 m0, s80
	s_nop 0
	buffer_load_dwordx4 v146, s[48:51], s19 offen lds
	s_mov_b32 m0, s82
	s_nop 0
	buffer_load_dwordx4 v147, s[48:51], s19 offen lds
	s_mov_b32 m0, s78
	s_nop 0
	buffer_load_dwordx4 v148, s[44:47], s35 offen lds
	s_mov_b32 m0, s79
	s_nop 0
	buffer_load_dwordx4 v149, s[44:47], s35 offen lds
	s_waitcnt vmcnt(8)
	s_waitcnt lgkmcnt(0)
	s_barrier
	s_setprio 1
	s_waitcnt lgkmcnt(7)
	v_mfma_f32_16x16x32_bf16 v[60:63], v[112:115], v[168:171], v[60:63]
	v_mfma_f32_16x16x32_bf16 v[0:3], v[128:131], v[168:171], v[0:3]
	s_waitcnt lgkmcnt(5)
	v_mfma_f32_16x16x32_bf16 v[48:51], v[112:115], v[178:181], v[48:51]
	v_mfma_f32_16x16x32_bf16 v[44:47], v[128:131], v[178:181], v[44:47]
	s_waitcnt lgkmcnt(3)
	v_mfma_f32_16x16x32_bf16 v[32:35], v[112:115], v[186:189], v[32:35]
	v_mfma_f32_16x16x32_bf16 v[28:31], v[128:131], v[186:189], v[28:31]
	s_waitcnt lgkmcnt(1)
	v_mfma_f32_16x16x32_bf16 v[16:19], v[112:115], v[194:197], v[16:19]
	v_mfma_f32_16x16x32_bf16 v[12:15], v[128:131], v[194:197], v[12:15]
	v_mfma_f32_16x16x32_bf16 v[60:63], v[116:119], v[172:175], v[60:63]
	v_mfma_f32_16x16x32_bf16 v[0:3], v[132:135], v[172:175], v[0:3]
	v_mfma_f32_16x16x32_bf16 v[48:51], v[116:119], v[182:185], v[48:51]
	v_mfma_f32_16x16x32_bf16 v[44:47], v[132:135], v[182:185], v[44:47]
	v_mfma_f32_16x16x32_bf16 v[32:35], v[116:119], v[190:193], v[32:35]
	v_mfma_f32_16x16x32_bf16 v[28:31], v[132:135], v[190:193], v[28:31]
	s_waitcnt lgkmcnt(0)
	v_mfma_f32_16x16x32_bf16 v[16:19], v[116:119], v[198:201], v[16:19]
	v_mfma_f32_16x16x32_bf16 v[12:15], v[132:135], v[198:201], v[12:15]
	v_mfma_f32_16x16x32_bf16 v[56:59], v[152:155], v[168:171], v[56:59]
	v_mfma_f32_16x16x32_bf16 v[52:55], v[160:163], v[168:171], v[52:55]
	v_mfma_f32_16x16x32_bf16 v[40:43], v[152:155], v[178:181], v[40:43]
	v_mfma_f32_16x16x32_bf16 v[36:39], v[160:163], v[178:181], v[36:39]
	v_mfma_f32_16x16x32_bf16 v[24:27], v[152:155], v[186:189], v[24:27]
	v_mfma_f32_16x16x32_bf16 v[20:23], v[160:163], v[186:189], v[20:23]
	v_mfma_f32_16x16x32_bf16 v[8:11], v[152:155], v[194:197], v[8:11]
	v_mfma_f32_16x16x32_bf16 v[4:7], v[160:163], v[194:197], v[4:7]
	v_mfma_f32_16x16x32_bf16 v[56:59], v[156:159], v[172:175], v[56:59]
	v_mfma_f32_16x16x32_bf16 v[52:55], v[164:167], v[172:175], v[52:55]
	v_mfma_f32_16x16x32_bf16 v[40:43], v[156:159], v[182:185], v[40:43]
	v_mfma_f32_16x16x32_bf16 v[36:39], v[164:167], v[182:185], v[36:39]
	v_mfma_f32_16x16x32_bf16 v[24:27], v[156:159], v[190:193], v[24:27]
	v_mfma_f32_16x16x32_bf16 v[20:23], v[164:167], v[190:193], v[20:23]
	v_mfma_f32_16x16x32_bf16 v[8:11], v[156:159], v[198:201], v[8:11]
	v_mfma_f32_16x16x32_bf16 v[4:7], v[164:167], v[198:201], v[4:7]
	s_setprio 0
	s_barrier
	s_add_i32 s12, s12, 2
	s_addk_i32 s13, 0x100
	s_cmp_gt_u32 s12, 29
	s_cbranch_scc0 .LBB0_1217
	s_and_b64 vcc, exec, s[8:9]
	s_cbranch_vccz .LBB0_1220
	s_barrier

.LBB0_1396:
	v_add_u32_e32 v140, 0x10000, v164
	v_add_u32_e32 v156, 0x14000, v164
	ds_read_b128 v[128:131], v140
	ds_read_b128 v[132:135], v140 offset:1024
	ds_read_b128 v[136:139], v140 offset:2048
	ds_read_b128 v[140:143], v140 offset:3072
	ds_read_b128 v[144:147], v156
	ds_read_b128 v[148:151], v156 offset:1024
	ds_read_b128 v[152:155], v156 offset:2048
	ds_read_b128 v[156:159], v156 offset:3072
	s_add_i32 s2, s83, 0xfff60080
	s_cmp_eq_u32 s88, 38
	s_cselect_b32 s3, 0, s2
	s_cselect_b32 s45, s39, s41
	s_cselect_b32 s44, s38, s40
	s_cselect_b32 s47, s71, s43
	s_cselect_b32 s46, s70, s42
	s_cselect_b32 s49, s73, s53
	s_cselect_b32 s48, s72, s52
	s_cselect_b32 s51, s77, s1
	s_cselect_b32 s50, s76, s0
	s_or_b32 s2, s3, 0x80
	s_mov_b32 m0, s75
	ds_read_b128 v[166:169], v165
	ds_read_b128 v[170:173], v165 offset:1024
	ds_read_b128 v[178:181], v165 offset:2048
	ds_read_b128 v[182:185], v165 offset:3072
	ds_read_b128 v[186:189], v165 offset:4096
	ds_read_b128 v[190:193], v165 offset:5120
	ds_read_b128 v[194:197], v165 offset:6144
	ds_read_b128 v[198:201], v165 offset:7168
	buffer_load_dwordx4 v162, s[40:43], s83 offen lds
	s_mov_b32 m0, s78
	s_nop 0
	buffer_load_dwordx4 v163, s[40:43], s83 offen lds
	s_waitcnt vmcnt(8)
	s_waitcnt lgkmcnt(0)
	s_barrier
	s_setprio 1
	s_waitcnt lgkmcnt(7)
	v_mfma_f32_16x16x32_bf16 v[124:127], v[128:131], v[166:169], v[124:127]
	v_mfma_f32_16x16x32_bf16 v[120:123], v[136:139], v[166:169], v[120:123]
	s_waitcnt lgkmcnt(5)
	v_mfma_f32_16x16x32_bf16 v[108:111], v[128:131], v[178:181], v[108:111]
	v_mfma_f32_16x16x32_bf16 v[104:107], v[136:139], v[178:181], v[104:107]
	s_waitcnt lgkmcnt(3)
	v_mfma_f32_16x16x32_bf16 v[92:95], v[128:131], v[186:189], v[92:95]
	v_mfma_f32_16x16x32_bf16 v[88:91], v[136:139], v[186:189], v[88:91]
	s_waitcnt lgkmcnt(1)
	v_mfma_f32_16x16x32_bf16 v[76:79], v[128:131], v[194:197], v[76:79]
	v_mfma_f32_16x16x32_bf16 v[72:75], v[136:139], v[194:197], v[72:75]
	v_mfma_f32_16x16x32_bf16 v[124:127], v[132:135], v[170:173], v[124:127]
	v_mfma_f32_16x16x32_bf16 v[120:123], v[140:143], v[170:173], v[120:123]
	v_mfma_f32_16x16x32_bf16 v[108:111], v[132:135], v[182:185], v[108:111]
	v_mfma_f32_16x16x32_bf16 v[104:107], v[140:143], v[182:185], v[104:107]
	v_mfma_f32_16x16x32_bf16 v[92:95], v[132:135], v[190:193], v[92:95]
	v_mfma_f32_16x16x32_bf16 v[88:91], v[140:143], v[190:193], v[88:91]
	s_waitcnt lgkmcnt(0)
	v_mfma_f32_16x16x32_bf16 v[76:79], v[132:135], v[198:201], v[76:79]
	v_mfma_f32_16x16x32_bf16 v[72:75], v[140:143], v[198:201], v[72:75]
	v_mfma_f32_16x16x32_bf16 v[116:119], v[144:147], v[166:169], v[116:119]
	v_mfma_f32_16x16x32_bf16 v[112:115], v[152:155], v[166:169], v[112:115]
	v_mfma_f32_16x16x32_bf16 v[100:103], v[144:147], v[178:181], v[100:103]
	v_mfma_f32_16x16x32_bf16 v[96:99], v[152:155], v[178:181], v[96:99]
	v_mfma_f32_16x16x32_bf16 v[84:87], v[144:147], v[186:189], v[84:87]
	v_mfma_f32_16x16x32_bf16 v[80:83], v[152:155], v[186:189], v[80:83]
	v_mfma_f32_16x16x32_bf16 v[68:71], v[144:147], v[194:197], v[68:71]
	v_mfma_f32_16x16x32_bf16 v[64:67], v[152:155], v[194:197], v[64:67]
	v_mfma_f32_16x16x32_bf16 v[116:119], v[148:151], v[170:173], v[116:119]
	v_mfma_f32_16x16x32_bf16 v[112:115], v[156:159], v[170:173], v[112:115]
	v_mfma_f32_16x16x32_bf16 v[100:103], v[148:151], v[182:185], v[100:103]
	v_mfma_f32_16x16x32_bf16 v[96:99], v[156:159], v[182:185], v[96:99]
	v_mfma_f32_16x16x32_bf16 v[84:87], v[148:151], v[190:193], v[84:87]
	v_mfma_f32_16x16x32_bf16 v[80:83], v[156:159], v[190:193], v[80:83]
	v_mfma_f32_16x16x32_bf16 v[68:71], v[148:151], v[198:201], v[68:71]
	v_mfma_f32_16x16x32_bf16 v[64:67], v[156:159], v[198:201], v[64:67]
	s_setprio 0
	s_barrier
	s_mov_b32 m0, s20
	ds_read_b128 v[166:169], v165 offset:16384
	ds_read_b128 v[170:173], v165 offset:17408
	ds_read_b128 v[178:181], v165 offset:18432
	ds_read_b128 v[182:185], v165 offset:19456
	ds_read_b128 v[186:189], v165 offset:20480
	ds_read_b128 v[190:193], v165 offset:21504
	ds_read_b128 v[194:197], v165 offset:22528
	ds_read_b128 v[198:201], v165 offset:23552
	buffer_load_dwordx4 v160, s[48:51], s3 offen lds
	s_mov_b32 m0, s21
	s_add_i32 s80, s3, 0xa0000
	buffer_load_dwordx4 v161, s[48:51], s3 offen lds
	s_mov_b32 m0, s22
	s_nop 0
	buffer_load_dwordx4 v160, s[48:51], s80 offen lds
	s_mov_b32 m0, s23
	s_nop 0
	buffer_load_dwordx4 v161, s[48:51], s80 offen lds
	s_mov_b32 m0, s13
	s_nop 0
	buffer_load_dwordx4 v162, s[44:47], s3 offen lds
	s_mov_b32 m0, s28
	s_nop 0
	buffer_load_dwordx4 v163, s[44:47], s3 offen lds
	s_waitcnt vmcnt(8)
	s_waitcnt lgkmcnt(0)
	s_barrier
	s_setprio 1
	s_waitcnt lgkmcnt(7)
	v_mfma_f32_16x16x32_bf16 v[60:63], v[128:131], v[166:169], v[60:63]
	v_mfma_f32_16x16x32_bf16 v[0:3], v[136:139], v[166:169], v[0:3]
	s_waitcnt lgkmcnt(5)
	v_mfma_f32_16x16x32_bf16 v[48:51], v[128:131], v[178:181], v[48:51]
	v_mfma_f32_16x16x32_bf16 v[44:47], v[136:139], v[178:181], v[44:47]
	s_waitcnt lgkmcnt(3)
	v_mfma_f32_16x16x32_bf16 v[32:35], v[128:131], v[186:189], v[32:35]
	v_mfma_f32_16x16x32_bf16 v[28:31], v[136:139], v[186:189], v[28:31]
	s_waitcnt lgkmcnt(1)
	v_mfma_f32_16x16x32_bf16 v[16:19], v[128:131], v[194:197], v[16:19]
	v_mfma_f32_16x16x32_bf16 v[12:15], v[136:139], v[194:197], v[12:15]
	v_mfma_f32_16x16x32_bf16 v[60:63], v[132:135], v[170:173], v[60:63]
	v_mfma_f32_16x16x32_bf16 v[0:3], v[140:143], v[170:173], v[0:3]
	v_mfma_f32_16x16x32_bf16 v[48:51], v[132:135], v[182:185], v[48:51]
	v_mfma_f32_16x16x32_bf16 v[44:47], v[140:143], v[182:185], v[44:47]
	v_mfma_f32_16x16x32_bf16 v[32:35], v[132:135], v[190:193], v[32:35]
	v_mfma_f32_16x16x32_bf16 v[28:31], v[140:143], v[190:193], v[28:31]
	s_waitcnt lgkmcnt(0)
	v_mfma_f32_16x16x32_bf16 v[16:19], v[132:135], v[198:201], v[16:19]
	v_mfma_f32_16x16x32_bf16 v[12:15], v[140:143], v[198:201], v[12:15]
	v_mfma_f32_16x16x32_bf16 v[56:59], v[144:147], v[166:169], v[56:59]
	v_mfma_f32_16x16x32_bf16 v[52:55], v[152:155], v[166:169], v[52:55]
	v_mfma_f32_16x16x32_bf16 v[40:43], v[144:147], v[178:181], v[40:43]
	v_mfma_f32_16x16x32_bf16 v[36:39], v[152:155], v[178:181], v[36:39]
	v_mfma_f32_16x16x32_bf16 v[24:27], v[144:147], v[186:189], v[24:27]
	v_mfma_f32_16x16x32_bf16 v[20:23], v[152:155], v[186:189], v[20:23]
	v_mfma_f32_16x16x32_bf16 v[8:11], v[144:147], v[194:197], v[8:11]
	v_mfma_f32_16x16x32_bf16 v[4:7], v[152:155], v[194:197], v[4:7]
	v_mfma_f32_16x16x32_bf16 v[56:59], v[148:151], v[170:173], v[56:59]
	v_mfma_f32_16x16x32_bf16 v[52:55], v[156:159], v[170:173], v[52:55]
	v_mfma_f32_16x16x32_bf16 v[40:43], v[148:151], v[182:185], v[40:43]
	v_mfma_f32_16x16x32_bf16 v[36:39], v[156:159], v[182:185], v[36:39]
	v_mfma_f32_16x16x32_bf16 v[24:27], v[148:151], v[190:193], v[24:27]
	v_mfma_f32_16x16x32_bf16 v[20:23], v[156:159], v[190:193], v[20:23]
	v_mfma_f32_16x16x32_bf16 v[8:11], v[148:151], v[198:201], v[8:11]
	v_mfma_f32_16x16x32_bf16 v[4:7], v[156:159], v[198:201], v[4:7]
	s_setprio 0
	s_barrier
	v_add_u32_e32 v140, 0x18000, v164
	v_add_u32_e32 v156, 0x1c000, v164
	ds_read_b128 v[128:131], v140
	ds_read_b128 v[132:135], v140 offset:1024
	ds_read_b128 v[136:139], v140 offset:2048
	ds_read_b128 v[140:143], v140 offset:3072
	ds_read_b128 v[144:147], v156
	ds_read_b128 v[148:151], v156 offset:1024
	ds_read_b128 v[152:155], v156 offset:2048
	ds_read_b128 v[156:159], v156 offset:3072
	s_mov_b32 m0, s29
	ds_read_b128 v[166:169], v165 offset:32768
	ds_read_b128 v[170:173], v165 offset:33792
	ds_read_b128 v[178:181], v165 offset:34816
	ds_read_b128 v[182:185], v165 offset:35840
	ds_read_b128 v[186:189], v165 offset:36864
	ds_read_b128 v[190:193], v165 offset:37888
	ds_read_b128 v[194:197], v165 offset:38912
	ds_read_b128 v[198:201], v165 offset:39936
	buffer_load_dwordx4 v162, s[44:47], s80 offen lds
	s_mov_b32 m0, s30
	s_nop 0
	buffer_load_dwordx4 v163, s[44:47], s80 offen lds
	s_waitcnt vmcnt(8)
	s_waitcnt lgkmcnt(0)
	s_barrier
	s_setprio 1
	s_waitcnt lgkmcnt(7)
	v_mfma_f32_16x16x32_bf16 v[124:127], v[128:131], v[166:169], v[124:127]
	v_mfma_f32_16x16x32_bf16 v[120:123], v[136:139], v[166:169], v[120:123]
	s_waitcnt lgkmcnt(5)
	v_mfma_f32_16x16x32_bf16 v[108:111], v[128:131], v[178:181], v[108:111]
	v_mfma_f32_16x16x32_bf16 v[104:107], v[136:139], v[178:181], v[104:107]
	s_waitcnt lgkmcnt(3)
	v_mfma_f32_16x16x32_bf16 v[92:95], v[128:131], v[186:189], v[92:95]
	v_mfma_f32_16x16x32_bf16 v[88:91], v[136:139], v[186:189], v[88:91]
	s_waitcnt lgkmcnt(1)
	v_mfma_f32_16x16x32_bf16 v[76:79], v[128:131], v[194:197], v[76:79]
	v_mfma_f32_16x16x32_bf16 v[72:75], v[136:139], v[194:197], v[72:75]
	v_mfma_f32_16x16x32_bf16 v[124:127], v[132:135], v[170:173], v[124:127]
	v_mfma_f32_16x16x32_bf16 v[120:123], v[140:143], v[170:173], v[120:123]
	v_mfma_f32_16x16x32_bf16 v[108:111], v[132:135], v[182:185], v[108:111]
	v_mfma_f32_16x16x32_bf16 v[104:107], v[140:143], v[182:185], v[104:107]
	v_mfma_f32_16x16x32_bf16 v[92:95], v[132:135], v[190:193], v[92:95]
	v_mfma_f32_16x16x32_bf16 v[88:91], v[140:143], v[190:193], v[88:91]
	s_waitcnt lgkmcnt(0)
	v_mfma_f32_16x16x32_bf16 v[76:79], v[132:135], v[198:201], v[76:79]
	v_mfma_f32_16x16x32_bf16 v[72:75], v[140:143], v[198:201], v[72:75]
	v_mfma_f32_16x16x32_bf16 v[116:119], v[144:147], v[166:169], v[116:119]
	v_mfma_f32_16x16x32_bf16 v[112:115], v[152:155], v[166:169], v[112:115]
	v_mfma_f32_16x16x32_bf16 v[100:103], v[144:147], v[178:181], v[100:103]
	v_mfma_f32_16x16x32_bf16 v[96:99], v[152:155], v[178:181], v[96:99]
	v_mfma_f32_16x16x32_bf16 v[84:87], v[144:147], v[186:189], v[84:87]
	v_mfma_f32_16x16x32_bf16 v[80:83], v[152:155], v[186:189], v[80:83]
	v_mfma_f32_16x16x32_bf16 v[68:71], v[144:147], v[194:197], v[68:71]
	v_mfma_f32_16x16x32_bf16 v[64:67], v[152:155], v[194:197], v[64:67]
	v_mfma_f32_16x16x32_bf16 v[116:119], v[148:151], v[170:173], v[116:119]
	v_mfma_f32_16x16x32_bf16 v[112:115], v[156:159], v[170:173], v[112:115]
	v_mfma_f32_16x16x32_bf16 v[100:103], v[148:151], v[182:185], v[100:103]
	v_mfma_f32_16x16x32_bf16 v[96:99], v[156:159], v[182:185], v[96:99]
	v_mfma_f32_16x16x32_bf16 v[84:87], v[148:151], v[190:193], v[84:87]
	v_mfma_f32_16x16x32_bf16 v[80:83], v[156:159], v[190:193], v[80:83]
	v_mfma_f32_16x16x32_bf16 v[68:71], v[148:151], v[198:201], v[68:71]
	v_mfma_f32_16x16x32_bf16 v[64:67], v[156:159], v[198:201], v[64:67]
	s_setprio 0
	s_barrier
	s_mov_b32 m0, s31
	ds_read_b128 v[166:169], v165 offset:49152
	ds_read_b128 v[170:173], v165 offset:50176
	ds_read_b128 v[178:181], v165 offset:51200
	ds_read_b128 v[182:185], v165 offset:52224
	ds_read_b128 v[186:189], v165 offset:53248
	ds_read_b128 v[190:193], v165 offset:54272
	ds_read_b128 v[194:197], v165 offset:55296
	ds_read_b128 v[198:201], v165 offset:56320
	buffer_load_dwordx4 v160, s[48:51], s2 offen lds
	s_mov_b32 m0, s33
	s_add_i32 s3, s3, 0xa0080
	buffer_load_dwordx4 v161, s[48:51], s2 offen lds
	s_mov_b32 m0, s62
	s_nop 0
	buffer_load_dwordx4 v160, s[48:51], s3 offen lds
	s_mov_b32 m0, s63
	s_nop 0
	buffer_load_dwordx4 v161, s[48:51], s3 offen lds
	s_mov_b32 m0, s34
	s_nop 0
	buffer_load_dwordx4 v162, s[44:47], s2 offen lds
	s_mov_b32 m0, s35
	s_nop 0
	buffer_load_dwordx4 v163, s[44:47], s2 offen lds
	s_waitcnt vmcnt(8)
	s_waitcnt lgkmcnt(0)
	s_barrier
	s_setprio 1
	s_waitcnt lgkmcnt(7)
	v_mfma_f32_16x16x32_bf16 v[60:63], v[128:131], v[166:169], v[60:63]
	v_mfma_f32_16x16x32_bf16 v[0:3], v[136:139], v[166:169], v[0:3]
	s_waitcnt lgkmcnt(5)
	v_mfma_f32_16x16x32_bf16 v[48:51], v[128:131], v[178:181], v[48:51]
	v_mfma_f32_16x16x32_bf16 v[44:47], v[136:139], v[178:181], v[44:47]
	s_waitcnt lgkmcnt(3)
	v_mfma_f32_16x16x32_bf16 v[32:35], v[128:131], v[186:189], v[32:35]
	v_mfma_f32_16x16x32_bf16 v[28:31], v[136:139], v[186:189], v[28:31]
	s_waitcnt lgkmcnt(1)
	v_mfma_f32_16x16x32_bf16 v[16:19], v[128:131], v[194:197], v[16:19]
	v_mfma_f32_16x16x32_bf16 v[12:15], v[136:139], v[194:197], v[12:15]
	v_mfma_f32_16x16x32_bf16 v[60:63], v[132:135], v[170:173], v[60:63]
	v_mfma_f32_16x16x32_bf16 v[0:3], v[140:143], v[170:173], v[0:3]
	v_mfma_f32_16x16x32_bf16 v[48:51], v[132:135], v[182:185], v[48:51]
	v_mfma_f32_16x16x32_bf16 v[44:47], v[140:143], v[182:185], v[44:47]
	v_mfma_f32_16x16x32_bf16 v[32:35], v[132:135], v[190:193], v[32:35]
	v_mfma_f32_16x16x32_bf16 v[28:31], v[140:143], v[190:193], v[28:31]
	s_waitcnt lgkmcnt(0)
	v_mfma_f32_16x16x32_bf16 v[16:19], v[132:135], v[198:201], v[16:19]
	v_mfma_f32_16x16x32_bf16 v[12:15], v[140:143], v[198:201], v[12:15]
	v_mfma_f32_16x16x32_bf16 v[56:59], v[144:147], v[166:169], v[56:59]
	v_mfma_f32_16x16x32_bf16 v[52:55], v[152:155], v[166:169], v[52:55]
	v_mfma_f32_16x16x32_bf16 v[40:43], v[144:147], v[178:181], v[40:43]
	v_mfma_f32_16x16x32_bf16 v[36:39], v[152:155], v[178:181], v[36:39]
	v_mfma_f32_16x16x32_bf16 v[24:27], v[144:147], v[186:189], v[24:27]
	v_mfma_f32_16x16x32_bf16 v[20:23], v[152:155], v[186:189], v[20:23]
	v_mfma_f32_16x16x32_bf16 v[8:11], v[144:147], v[194:197], v[8:11]
	v_mfma_f32_16x16x32_bf16 v[4:7], v[152:155], v[194:197], v[4:7]
	v_mfma_f32_16x16x32_bf16 v[56:59], v[148:151], v[170:173], v[56:59]
	v_mfma_f32_16x16x32_bf16 v[52:55], v[156:159], v[170:173], v[52:55]
	v_mfma_f32_16x16x32_bf16 v[40:43], v[148:151], v[182:185], v[40:43]
	v_mfma_f32_16x16x32_bf16 v[36:39], v[156:159], v[182:185], v[36:39]
	v_mfma_f32_16x16x32_bf16 v[24:27], v[148:151], v[190:193], v[24:27]
	v_mfma_f32_16x16x32_bf16 v[20:23], v[156:159], v[190:193], v[20:23]
	v_mfma_f32_16x16x32_bf16 v[8:11], v[148:151], v[198:201], v[8:11]
	v_mfma_f32_16x16x32_bf16 v[4:7], v[156:159], v[198:201], v[4:7]
	s_setprio 0
	s_barrier
	s_add_i32 s2, s88, 2
	s_addk_i32 s83, 0x100
	s_cmp_gt_u32 s88, 37
	s_cbranch_scc1 .LBB0_1398
	s_mov_b32 s88, s2
	s_and_b32 s2, s88, 0x7ffffff6
	s_cmp_lg_u32 s2, 16
	s_cbranch_scc0 .LBB0_1395
	s_branch .LBB0_1396

.LBB0_1428:
	v_add_u32_e32 v140, 0x10000, v164
	v_add_u32_e32 v156, 0x14000, v164
	ds_read_b128 v[128:131], v140
	ds_read_b128 v[132:135], v140 offset:1024
	ds_read_b128 v[136:139], v140 offset:2048
	ds_read_b128 v[140:143], v140 offset:3072
	ds_read_b128 v[144:147], v156
	ds_read_b128 v[148:151], v156 offset:1024
	ds_read_b128 v[152:155], v156 offset:2048
	ds_read_b128 v[156:159], v156 offset:3072
	s_add_i32 s2, s83, 0xfff60080
	s_cmp_eq_u32 s88, 38
	s_cselect_b32 s3, 0, s2
	s_cselect_b32 s45, s39, s41
	s_cselect_b32 s44, s38, s40
	s_cselect_b32 s47, s71, s43
	s_cselect_b32 s46, s70, s42
	s_cselect_b32 s49, s73, s53
	s_cselect_b32 s48, s72, s52
	s_cselect_b32 s51, s77, s1
	s_cselect_b32 s50, s76, s0
	s_or_b32 s2, s3, 0x80
	s_mov_b32 m0, s21
	ds_read_b128 v[166:169], v165
	ds_read_b128 v[170:173], v165 offset:1024
	ds_read_b128 v[178:181], v165 offset:2048
	ds_read_b128 v[182:185], v165 offset:3072
	ds_read_b128 v[186:189], v165 offset:4096
	ds_read_b128 v[190:193], v165 offset:5120
	ds_read_b128 v[194:197], v165 offset:6144
	ds_read_b128 v[198:201], v165 offset:7168
	buffer_load_dwordx4 v162, s[40:43], s83 offen lds
	s_mov_b32 m0, s75
	s_nop 0
	buffer_load_dwordx4 v163, s[40:43], s83 offen lds
	s_waitcnt vmcnt(8)
	s_waitcnt lgkmcnt(0)
	s_barrier
	s_setprio 1
	s_waitcnt lgkmcnt(7)
	v_mfma_f32_16x16x32_bf16 v[124:127], v[128:131], v[166:169], v[124:127]
	v_mfma_f32_16x16x32_bf16 v[120:123], v[136:139], v[166:169], v[120:123]
	s_waitcnt lgkmcnt(5)
	v_mfma_f32_16x16x32_bf16 v[108:111], v[128:131], v[178:181], v[108:111]
	v_mfma_f32_16x16x32_bf16 v[104:107], v[136:139], v[178:181], v[104:107]
	s_waitcnt lgkmcnt(3)
	v_mfma_f32_16x16x32_bf16 v[92:95], v[128:131], v[186:189], v[92:95]
	v_mfma_f32_16x16x32_bf16 v[88:91], v[136:139], v[186:189], v[88:91]
	s_waitcnt lgkmcnt(1)
	v_mfma_f32_16x16x32_bf16 v[76:79], v[128:131], v[194:197], v[76:79]
	v_mfma_f32_16x16x32_bf16 v[72:75], v[136:139], v[194:197], v[72:75]
	v_mfma_f32_16x16x32_bf16 v[124:127], v[132:135], v[170:173], v[124:127]
	v_mfma_f32_16x16x32_bf16 v[120:123], v[140:143], v[170:173], v[120:123]
	v_mfma_f32_16x16x32_bf16 v[108:111], v[132:135], v[182:185], v[108:111]
	v_mfma_f32_16x16x32_bf16 v[104:107], v[140:143], v[182:185], v[104:107]
	v_mfma_f32_16x16x32_bf16 v[92:95], v[132:135], v[190:193], v[92:95]
	v_mfma_f32_16x16x32_bf16 v[88:91], v[140:143], v[190:193], v[88:91]
	s_waitcnt lgkmcnt(0)
	v_mfma_f32_16x16x32_bf16 v[76:79], v[132:135], v[198:201], v[76:79]
	v_mfma_f32_16x16x32_bf16 v[72:75], v[140:143], v[198:201], v[72:75]
	v_mfma_f32_16x16x32_bf16 v[116:119], v[144:147], v[166:169], v[116:119]
	v_mfma_f32_16x16x32_bf16 v[112:115], v[152:155], v[166:169], v[112:115]
	v_mfma_f32_16x16x32_bf16 v[100:103], v[144:147], v[178:181], v[100:103]
	v_mfma_f32_16x16x32_bf16 v[96:99], v[152:155], v[178:181], v[96:99]
	v_mfma_f32_16x16x32_bf16 v[84:87], v[144:147], v[186:189], v[84:87]
	v_mfma_f32_16x16x32_bf16 v[80:83], v[152:155], v[186:189], v[80:83]
	v_mfma_f32_16x16x32_bf16 v[68:71], v[144:147], v[194:197], v[68:71]
	v_mfma_f32_16x16x32_bf16 v[64:67], v[152:155], v[194:197], v[64:67]
	v_mfma_f32_16x16x32_bf16 v[116:119], v[148:151], v[170:173], v[116:119]
	v_mfma_f32_16x16x32_bf16 v[112:115], v[156:159], v[170:173], v[112:115]
	v_mfma_f32_16x16x32_bf16 v[100:103], v[148:151], v[182:185], v[100:103]
	v_mfma_f32_16x16x32_bf16 v[96:99], v[156:159], v[182:185], v[96:99]
	v_mfma_f32_16x16x32_bf16 v[84:87], v[148:151], v[190:193], v[84:87]
	v_mfma_f32_16x16x32_bf16 v[80:83], v[156:159], v[190:193], v[80:83]
	v_mfma_f32_16x16x32_bf16 v[68:71], v[148:151], v[198:201], v[68:71]
	v_mfma_f32_16x16x32_bf16 v[64:67], v[156:159], v[198:201], v[64:67]
	s_setprio 0
	s_barrier
	s_mov_b32 m0, s22
	ds_read_b128 v[166:169], v165 offset:16384
	ds_read_b128 v[170:173], v165 offset:17408
	ds_read_b128 v[178:181], v165 offset:18432
	ds_read_b128 v[182:185], v165 offset:19456
	ds_read_b128 v[186:189], v165 offset:20480
	ds_read_b128 v[190:193], v165 offset:21504
	ds_read_b128 v[194:197], v165 offset:22528
	ds_read_b128 v[198:201], v165 offset:23552
	buffer_load_dwordx4 v160, s[48:51], s3 offen lds
	s_mov_b32 m0, s23
	s_add_i32 s80, s3, 0xa0000
	buffer_load_dwordx4 v161, s[48:51], s3 offen lds
	s_mov_b32 m0, s28
	s_nop 0
	buffer_load_dwordx4 v160, s[48:51], s80 offen lds
	s_mov_b32 m0, s29
	s_nop 0
	buffer_load_dwordx4 v161, s[48:51], s80 offen lds
	s_mov_b32 m0, s74
	s_nop 0
	buffer_load_dwordx4 v162, s[44:47], s3 offen lds
	s_mov_b32 m0, s30
	s_nop 0
	buffer_load_dwordx4 v163, s[44:47], s3 offen lds
	s_waitcnt vmcnt(8)
	s_waitcnt lgkmcnt(0)
	s_barrier
	s_setprio 1
	s_waitcnt lgkmcnt(7)
	v_mfma_f32_16x16x32_bf16 v[60:63], v[128:131], v[166:169], v[60:63]
	v_mfma_f32_16x16x32_bf16 v[8:11], v[136:139], v[166:169], v[8:11]
	s_waitcnt lgkmcnt(5)
	v_mfma_f32_16x16x32_bf16 v[48:51], v[128:131], v[178:181], v[48:51]
	v_mfma_f32_16x16x32_bf16 v[44:47], v[136:139], v[178:181], v[44:47]
	s_waitcnt lgkmcnt(3)
	v_mfma_f32_16x16x32_bf16 v[32:35], v[128:131], v[186:189], v[32:35]
	v_mfma_f32_16x16x32_bf16 v[28:31], v[136:139], v[186:189], v[28:31]
	s_waitcnt lgkmcnt(1)
	v_mfma_f32_16x16x32_bf16 v[16:19], v[128:131], v[194:197], v[16:19]
	v_mfma_f32_16x16x32_bf16 v[12:15], v[136:139], v[194:197], v[12:15]
	v_mfma_f32_16x16x32_bf16 v[60:63], v[132:135], v[170:173], v[60:63]
	v_mfma_f32_16x16x32_bf16 v[8:11], v[140:143], v[170:173], v[8:11]
	v_mfma_f32_16x16x32_bf16 v[48:51], v[132:135], v[182:185], v[48:51]
	v_mfma_f32_16x16x32_bf16 v[44:47], v[140:143], v[182:185], v[44:47]
	v_mfma_f32_16x16x32_bf16 v[32:35], v[132:135], v[190:193], v[32:35]
	v_mfma_f32_16x16x32_bf16 v[28:31], v[140:143], v[190:193], v[28:31]
	s_waitcnt lgkmcnt(0)
	v_mfma_f32_16x16x32_bf16 v[16:19], v[132:135], v[198:201], v[16:19]
	v_mfma_f32_16x16x32_bf16 v[12:15], v[140:143], v[198:201], v[12:15]
	v_mfma_f32_16x16x32_bf16 v[56:59], v[144:147], v[166:169], v[56:59]
	v_mfma_f32_16x16x32_bf16 v[52:55], v[152:155], v[166:169], v[52:55]
	v_mfma_f32_16x16x32_bf16 v[40:43], v[144:147], v[178:181], v[40:43]
	v_mfma_f32_16x16x32_bf16 v[36:39], v[152:155], v[178:181], v[36:39]
	v_mfma_f32_16x16x32_bf16 v[24:27], v[144:147], v[186:189], v[24:27]
	v_mfma_f32_16x16x32_bf16 v[20:23], v[152:155], v[186:189], v[20:23]
	v_mfma_f32_16x16x32_bf16 v[4:7], v[144:147], v[194:197], v[4:7]
	v_mfma_f32_16x16x32_bf16 v[0:3], v[152:155], v[194:197], v[0:3]
	v_mfma_f32_16x16x32_bf16 v[56:59], v[148:151], v[170:173], v[56:59]
	v_mfma_f32_16x16x32_bf16 v[52:55], v[156:159], v[170:173], v[52:55]
	v_mfma_f32_16x16x32_bf16 v[40:43], v[148:151], v[182:185], v[40:43]
	v_mfma_f32_16x16x32_bf16 v[36:39], v[156:159], v[182:185], v[36:39]
	v_mfma_f32_16x16x32_bf16 v[24:27], v[148:151], v[190:193], v[24:27]
	v_mfma_f32_16x16x32_bf16 v[20:23], v[156:159], v[190:193], v[20:23]
	v_mfma_f32_16x16x32_bf16 v[4:7], v[148:151], v[198:201], v[4:7]
	v_mfma_f32_16x16x32_bf16 v[0:3], v[156:159], v[198:201], v[0:3]
	s_setprio 0
	s_barrier
	v_add_u32_e32 v140, 0x18000, v164
	v_add_u32_e32 v156, 0x1c000, v164
	ds_read_b128 v[128:131], v140
	ds_read_b128 v[132:135], v140 offset:1024
	ds_read_b128 v[136:139], v140 offset:2048
	ds_read_b128 v[140:143], v140 offset:3072
	ds_read_b128 v[144:147], v156
	ds_read_b128 v[148:151], v156 offset:1024
	ds_read_b128 v[152:155], v156 offset:2048
	ds_read_b128 v[156:159], v156 offset:3072
	s_mov_b32 m0, s31
	ds_read_b128 v[166:169], v165 offset:32768
	ds_read_b128 v[170:173], v165 offset:33792
	ds_read_b128 v[178:181], v165 offset:34816
	ds_read_b128 v[182:185], v165 offset:35840
	ds_read_b128 v[186:189], v165 offset:36864
	ds_read_b128 v[190:193], v165 offset:37888
	ds_read_b128 v[194:197], v165 offset:38912
	ds_read_b128 v[198:201], v165 offset:39936
	buffer_load_dwordx4 v162, s[44:47], s80 offen lds
	s_mov_b32 m0, s33
	s_nop 0
	buffer_load_dwordx4 v163, s[44:47], s80 offen lds
	s_waitcnt vmcnt(8)
	s_waitcnt lgkmcnt(0)
	s_barrier
	s_setprio 1
	s_waitcnt lgkmcnt(7)
	v_mfma_f32_16x16x32_bf16 v[124:127], v[128:131], v[166:169], v[124:127]
	v_mfma_f32_16x16x32_bf16 v[120:123], v[136:139], v[166:169], v[120:123]
	s_waitcnt lgkmcnt(5)
	v_mfma_f32_16x16x32_bf16 v[108:111], v[128:131], v[178:181], v[108:111]
	v_mfma_f32_16x16x32_bf16 v[104:107], v[136:139], v[178:181], v[104:107]
	s_waitcnt lgkmcnt(3)
	v_mfma_f32_16x16x32_bf16 v[92:95], v[128:131], v[186:189], v[92:95]
	v_mfma_f32_16x16x32_bf16 v[88:91], v[136:139], v[186:189], v[88:91]
	s_waitcnt lgkmcnt(1)
	v_mfma_f32_16x16x32_bf16 v[76:79], v[128:131], v[194:197], v[76:79]
	v_mfma_f32_16x16x32_bf16 v[72:75], v[136:139], v[194:197], v[72:75]
	v_mfma_f32_16x16x32_bf16 v[124:127], v[132:135], v[170:173], v[124:127]
	v_mfma_f32_16x16x32_bf16 v[120:123], v[140:143], v[170:173], v[120:123]
	v_mfma_f32_16x16x32_bf16 v[108:111], v[132:135], v[182:185], v[108:111]
	v_mfma_f32_16x16x32_bf16 v[104:107], v[140:143], v[182:185], v[104:107]
	v_mfma_f32_16x16x32_bf16 v[92:95], v[132:135], v[190:193], v[92:95]
	v_mfma_f32_16x16x32_bf16 v[88:91], v[140:143], v[190:193], v[88:91]
	s_waitcnt lgkmcnt(0)
	v_mfma_f32_16x16x32_bf16 v[76:79], v[132:135], v[198:201], v[76:79]
	v_mfma_f32_16x16x32_bf16 v[72:75], v[140:143], v[198:201], v[72:75]
	v_mfma_f32_16x16x32_bf16 v[116:119], v[144:147], v[166:169], v[116:119]
	v_mfma_f32_16x16x32_bf16 v[112:115], v[152:155], v[166:169], v[112:115]
	v_mfma_f32_16x16x32_bf16 v[100:103], v[144:147], v[178:181], v[100:103]
	v_mfma_f32_16x16x32_bf16 v[96:99], v[152:155], v[178:181], v[96:99]
	v_mfma_f32_16x16x32_bf16 v[84:87], v[144:147], v[186:189], v[84:87]
	v_mfma_f32_16x16x32_bf16 v[80:83], v[152:155], v[186:189], v[80:83]
	v_mfma_f32_16x16x32_bf16 v[68:71], v[144:147], v[194:197], v[68:71]
	v_mfma_f32_16x16x32_bf16 v[64:67], v[152:155], v[194:197], v[64:67]
	v_mfma_f32_16x16x32_bf16 v[116:119], v[148:151], v[170:173], v[116:119]
	v_mfma_f32_16x16x32_bf16 v[112:115], v[156:159], v[170:173], v[112:115]
	v_mfma_f32_16x16x32_bf16 v[100:103], v[148:151], v[182:185], v[100:103]
	v_mfma_f32_16x16x32_bf16 v[96:99], v[156:159], v[182:185], v[96:99]
	v_mfma_f32_16x16x32_bf16 v[84:87], v[148:151], v[190:193], v[84:87]
	v_mfma_f32_16x16x32_bf16 v[80:83], v[156:159], v[190:193], v[80:83]
	v_mfma_f32_16x16x32_bf16 v[68:71], v[148:151], v[198:201], v[68:71]
	v_mfma_f32_16x16x32_bf16 v[64:67], v[156:159], v[198:201], v[64:67]
	s_setprio 0
	s_barrier
	s_mov_b32 m0, s34
	ds_read_b128 v[166:169], v165 offset:49152
	ds_read_b128 v[170:173], v165 offset:50176
	ds_read_b128 v[178:181], v165 offset:51200
	ds_read_b128 v[182:185], v165 offset:52224
	ds_read_b128 v[186:189], v165 offset:53248
	ds_read_b128 v[190:193], v165 offset:54272
	ds_read_b128 v[194:197], v165 offset:55296
	ds_read_b128 v[198:201], v165 offset:56320
	buffer_load_dwordx4 v160, s[48:51], s2 offen lds
	s_mov_b32 m0, s35
	s_add_i32 s3, s3, 0xa0080
	buffer_load_dwordx4 v161, s[48:51], s2 offen lds
	s_mov_b32 m0, s64
	s_nop 0
	buffer_load_dwordx4 v160, s[48:51], s3 offen lds
	s_mov_b32 m0, s65
	s_nop 0
	buffer_load_dwordx4 v161, s[48:51], s3 offen lds
	s_mov_b32 m0, s62
	s_nop 0
	buffer_load_dwordx4 v162, s[44:47], s2 offen lds
	s_mov_b32 m0, s63
	s_nop 0
	buffer_load_dwordx4 v163, s[44:47], s2 offen lds
	s_waitcnt vmcnt(8)
	s_waitcnt lgkmcnt(0)
	s_barrier
	s_setprio 1
	s_waitcnt lgkmcnt(7)
	v_mfma_f32_16x16x32_bf16 v[60:63], v[128:131], v[166:169], v[60:63]
	v_mfma_f32_16x16x32_bf16 v[8:11], v[136:139], v[166:169], v[8:11]
	s_waitcnt lgkmcnt(5)
	v_mfma_f32_16x16x32_bf16 v[48:51], v[128:131], v[178:181], v[48:51]
	v_mfma_f32_16x16x32_bf16 v[44:47], v[136:139], v[178:181], v[44:47]
	s_waitcnt lgkmcnt(3)
	v_mfma_f32_16x16x32_bf16 v[32:35], v[128:131], v[186:189], v[32:35]
	v_mfma_f32_16x16x32_bf16 v[28:31], v[136:139], v[186:189], v[28:31]
	s_waitcnt lgkmcnt(1)
	v_mfma_f32_16x16x32_bf16 v[16:19], v[128:131], v[194:197], v[16:19]
	v_mfma_f32_16x16x32_bf16 v[12:15], v[136:139], v[194:197], v[12:15]
	v_mfma_f32_16x16x32_bf16 v[60:63], v[132:135], v[170:173], v[60:63]
	v_mfma_f32_16x16x32_bf16 v[8:11], v[140:143], v[170:173], v[8:11]
	v_mfma_f32_16x16x32_bf16 v[48:51], v[132:135], v[182:185], v[48:51]
	v_mfma_f32_16x16x32_bf16 v[44:47], v[140:143], v[182:185], v[44:47]
	v_mfma_f32_16x16x32_bf16 v[32:35], v[132:135], v[190:193], v[32:35]
	v_mfma_f32_16x16x32_bf16 v[28:31], v[140:143], v[190:193], v[28:31]
	s_waitcnt lgkmcnt(0)
	v_mfma_f32_16x16x32_bf16 v[16:19], v[132:135], v[198:201], v[16:19]
	v_mfma_f32_16x16x32_bf16 v[12:15], v[140:143], v[198:201], v[12:15]
	v_mfma_f32_16x16x32_bf16 v[56:59], v[144:147], v[166:169], v[56:59]
	v_mfma_f32_16x16x32_bf16 v[52:55], v[152:155], v[166:169], v[52:55]
	v_mfma_f32_16x16x32_bf16 v[40:43], v[144:147], v[178:181], v[40:43]
	v_mfma_f32_16x16x32_bf16 v[36:39], v[152:155], v[178:181], v[36:39]
	v_mfma_f32_16x16x32_bf16 v[24:27], v[144:147], v[186:189], v[24:27]
	v_mfma_f32_16x16x32_bf16 v[20:23], v[152:155], v[186:189], v[20:23]
	v_mfma_f32_16x16x32_bf16 v[4:7], v[144:147], v[194:197], v[4:7]
	v_mfma_f32_16x16x32_bf16 v[0:3], v[152:155], v[194:197], v[0:3]
	v_mfma_f32_16x16x32_bf16 v[56:59], v[148:151], v[170:173], v[56:59]
	v_mfma_f32_16x16x32_bf16 v[52:55], v[156:159], v[170:173], v[52:55]
	v_mfma_f32_16x16x32_bf16 v[40:43], v[148:151], v[182:185], v[40:43]
	v_mfma_f32_16x16x32_bf16 v[36:39], v[156:159], v[182:185], v[36:39]
	v_mfma_f32_16x16x32_bf16 v[24:27], v[148:151], v[190:193], v[24:27]
	v_mfma_f32_16x16x32_bf16 v[20:23], v[156:159], v[190:193], v[20:23]
	v_mfma_f32_16x16x32_bf16 v[4:7], v[148:151], v[198:201], v[4:7]
	v_mfma_f32_16x16x32_bf16 v[0:3], v[156:159], v[198:201], v[0:3]
	s_setprio 0
	s_barrier
	s_add_i32 s2, s88, 2
	s_addk_i32 s83, 0x100
	s_cmp_gt_u32 s88, 37
	s_cbranch_scc1 .LBB0_1430
	s_mov_b32 s88, s2
	s_and_b32 s2, s88, 0x7ffffff6
	s_cmp_lg_u32 s2, 16
	s_cbranch_scc0 .LBB0_1427
	s_branch .LBB0_1428

.LBB0_1507:
	v_add_u32_e32 v116, 0x10000, v176
	v_add_u32_e32 v120, 0x14000, v176
	ds_read_b128 v[104:107], v116
	ds_read_b128 v[108:111], v116 offset:1024
	ds_read_b128 v[112:115], v116 offset:2048
	ds_read_b128 v[116:119], v116 offset:3072
	ds_read_b128 v[148:151], v120
	ds_read_b128 v[152:155], v120 offset:1024
	ds_read_b128 v[156:159], v120 offset:2048
	ds_read_b128 v[160:163], v120 offset:3072
	s_add_i32 s21, s13, 0xfffc0080
	s_cmp_eq_u32 s12, 12
	s_cselect_b32 s45, s29, s41
	s_cselect_b32 s44, s28, s40
	s_cselect_b32 s47, s31, s43
	s_cselect_b32 s46, s30, s42
	s_cselect_b32 s21, 0, s21
	s_cselect_b32 s49, s35, s53
	s_cselect_b32 s48, s34, s52
	s_cselect_b32 s51, s39, s5
	s_cselect_b32 s50, s38, s4
	s_mov_b32 m0, s90
	ds_read_b128 v[164:167], v198
	ds_read_b128 v[168:171], v198 offset:1024
	ds_read_b128 v[200:203], v198 offset:2048
	ds_read_b128 v[204:207], v198 offset:3072
	ds_read_b128 v[208:211], v198 offset:4096
	ds_read_b128 v[212:215], v198 offset:5120
	ds_read_b128 v[216:219], v198 offset:6144
	ds_read_b128 v[220:223], v198 offset:7168
	buffer_load_dwordx4 v229, s[40:43], s13 offen lds
	s_mov_b32 m0, s92
	s_nop 0
	buffer_load_dwordx4 v252, s[40:43], s13 offen lds
	s_waitcnt vmcnt(8)
	s_waitcnt lgkmcnt(0)
	s_barrier
	s_setprio 1
	s_waitcnt lgkmcnt(6)
	v_mfma_f32_16x16x128_f8f6f4 v[140:143], v[112:119], v[164:171], v[140:143]
	s_waitcnt lgkmcnt(4)
	v_mfma_f32_16x16x128_f8f6f4 v[128:131], v[104:111], v[200:207], v[128:131]
	v_mfma_f32_16x16x128_f8f6f4 v[124:127], v[112:119], v[200:207], v[124:127]
	v_mfma_f32_16x16x128_f8f6f4 v[120:123], v[104:111], v[164:171], v[144:147]
	s_waitcnt lgkmcnt(2)
	v_mfma_f32_16x16x128_f8f6f4 v[178:181], v[104:111], v[208:215], v[92:95]
	v_mfma_f32_16x16x128_f8f6f4 v[182:185], v[112:119], v[208:215], v[88:91]
	s_waitcnt lgkmcnt(0)
	v_mfma_f32_16x16x128_f8f6f4 v[186:189], v[104:111], v[216:223], v[76:79]
	v_mfma_f32_16x16x128_f8f6f4 v[190:193], v[112:119], v[216:223], v[72:75]
	v_mfma_f32_16x16x128_f8f6f4 v[136:139], v[148:155], v[164:171], v[136:139]
	v_mfma_f32_16x16x128_f8f6f4 v[132:135], v[156:163], v[164:171], v[132:135]
	v_mfma_f32_16x16x128_f8f6f4 v[100:103], v[148:155], v[200:207], v[100:103]
	v_mfma_f32_16x16x128_f8f6f4 v[96:99], v[156:163], v[200:207], v[96:99]
	v_mfma_f32_16x16x128_f8f6f4 v[164:167], v[148:155], v[208:215], v[84:87]
	v_mfma_f32_16x16x128_f8f6f4 v[168:171], v[156:163], v[208:215], v[80:83]
	v_mfma_f32_16x16x128_f8f6f4 v[194:197], v[148:155], v[216:223], v[68:71]
	v_mfma_f32_16x16x128_f8f6f4 v[200:203], v[156:163], v[216:223], v[64:67]
	s_setprio 0
	s_barrier
	s_mov_b32 m0, s63
	s_nop 3
	ds_read_b128 v[64:67], v198 offset:16384
	ds_read_b128 v[68:71], v198 offset:17408
	ds_read_b128 v[72:75], v198 offset:18432
	ds_read_b128 v[76:79], v198 offset:19456
	ds_read_b128 v[80:83], v198 offset:20480
	ds_read_b128 v[84:87], v198 offset:21504
	ds_read_b128 v[88:91], v198 offset:22528
	ds_read_b128 v[92:95], v198 offset:23552
	buffer_load_dwordx4 v199, s[48:51], s21 offen lds
	s_mov_b32 m0, s69
	s_add_i32 s23, s21, 0x40000
	buffer_load_dwordx4 v228, s[48:51], s21 offen lds
	s_mov_b32 m0, s70
	s_nop 0
	buffer_load_dwordx4 v199, s[48:51], s23 offen lds
	s_mov_b32 m0, s71
	s_nop 0
	buffer_load_dwordx4 v228, s[48:51], s23 offen lds
	s_mov_b32 m0, s62
	s_nop 0
	buffer_load_dwordx4 v229, s[44:47], s21 offen lds
	s_mov_b32 m0, s72
	s_nop 0
	buffer_load_dwordx4 v252, s[44:47], s21 offen lds
	s_waitcnt vmcnt(8)
	s_waitcnt lgkmcnt(0)
	s_barrier
	s_setprio 1
	s_waitcnt lgkmcnt(6)
	v_mfma_f32_16x16x128_f8f6f4 v[60:63], v[104:111], v[64:71], v[60:63]
	s_waitcnt lgkmcnt(0)
	v_mfma_f32_16x16x128_f8f6f4 v[16:19], v[104:111], v[88:95], v[16:19]
	v_mfma_f32_16x16x128_f8f6f4 v[204:207], v[112:119], v[64:71], v[8:11]
	v_mfma_f32_16x16x128_f8f6f4 v[208:211], v[104:111], v[72:79], v[48:51]
	v_mfma_f32_16x16x128_f8f6f4 v[212:215], v[112:119], v[72:79], v[44:47]
	v_mfma_f32_16x16x128_f8f6f4 v[216:219], v[104:111], v[80:87], v[32:35]
	v_mfma_f32_16x16x128_f8f6f4 v[220:223], v[112:119], v[80:87], v[28:31]
	v_mfma_f32_16x16x128_f8f6f4 v[224:227], v[112:119], v[88:95], v[12:15]
	v_mfma_f32_16x16x128_f8f6f4 v[56:59], v[148:155], v[64:71], v[56:59]
	v_mfma_f32_16x16x128_f8f6f4 v[52:55], v[156:163], v[64:71], v[52:55]
	v_mfma_f32_16x16x128_f8f6f4 v[232:235], v[148:155], v[72:79], v[40:43]
	v_mfma_f32_16x16x128_f8f6f4 v[236:239], v[156:163], v[72:79], v[36:39]
	v_mfma_f32_16x16x128_f8f6f4 v[240:243], v[148:155], v[80:87], v[24:27]
	v_mfma_f32_16x16x128_f8f6f4 v[244:247], v[156:163], v[80:87], v[20:23]
	v_mfma_f32_16x16x128_f8f6f4 v[248:251], v[148:155], v[88:95], v[4:7]
	v_mfma_f32_16x16x128_f8f6f4 v[172:175], v[156:163], v[88:95], v[0:3]
	s_setprio 0
	s_barrier
	v_add_u32_e32 v8, 0x18000, v176
	s_nop 3
	ds_read_b128 v[0:3], v8
	ds_read_b128 v[4:7], v8 offset:1024
	ds_read_b128 v[20:23], v8 offset:2048
	ds_read_b128 v[24:27], v8 offset:3072
	v_add_u32_e32 v8, 0x1c000, v176
	ds_read_b128 v[104:107], v8
	ds_read_b128 v[108:111], v8 offset:1024
	ds_read_b128 v[112:115], v8 offset:2048
	ds_read_b128 v[116:119], v8 offset:3072
	s_mov_b32 m0, s73
	ds_read_b128 v[8:11], v198 offset:32768
	ds_read_b128 v[12:15], v198 offset:33792
	ds_read_b128 v[28:31], v198 offset:34816
	ds_read_b128 v[32:35], v198 offset:35840
	ds_read_b128 v[36:39], v198 offset:36864
	ds_read_b128 v[40:43], v198 offset:37888
	ds_read_b128 v[44:47], v198 offset:38912
	ds_read_b128 v[48:51], v198 offset:39936
	buffer_load_dwordx4 v229, s[44:47], s23 offen lds
	s_mov_b32 m0, s74
	s_nop 0
	buffer_load_dwordx4 v252, s[44:47], s23 offen lds
	s_waitcnt vmcnt(8)
	s_waitcnt lgkmcnt(0)
	s_barrier
	s_setprio 1
	s_waitcnt lgkmcnt(6)
	v_mfma_f32_16x16x128_f8f6f4 v[144:147], v[0:7], v[8:15], v[120:123]
	v_mfma_f32_16x16x128_f8f6f4 v[140:143], v[20:27], v[8:15], v[140:143]
	s_waitcnt lgkmcnt(4)
	v_mfma_f32_16x16x128_f8f6f4 v[128:131], v[0:7], v[28:35], v[128:131]
	v_mfma_f32_16x16x128_f8f6f4 v[124:127], v[20:27], v[28:35], v[124:127]
	s_waitcnt lgkmcnt(2)
	v_mfma_f32_16x16x128_f8f6f4 v[92:95], v[0:7], v[36:43], v[178:181]
	v_mfma_f32_16x16x128_f8f6f4 v[88:91], v[20:27], v[36:43], v[182:185]
	s_waitcnt lgkmcnt(0)
	v_mfma_f32_16x16x128_f8f6f4 v[76:79], v[0:7], v[44:51], v[186:189]
	v_mfma_f32_16x16x128_f8f6f4 v[72:75], v[20:27], v[44:51], v[190:193]
	v_mfma_f32_16x16x128_f8f6f4 v[136:139], v[104:111], v[8:15], v[136:139]
	v_mfma_f32_16x16x128_f8f6f4 v[132:135], v[112:119], v[8:15], v[132:135]
	v_mfma_f32_16x16x128_f8f6f4 v[100:103], v[104:111], v[28:35], v[100:103]
	v_mfma_f32_16x16x128_f8f6f4 v[96:99], v[112:119], v[28:35], v[96:99]
	v_mfma_f32_16x16x128_f8f6f4 v[84:87], v[104:111], v[36:43], v[164:167]
	v_mfma_f32_16x16x128_f8f6f4 v[80:83], v[112:119], v[36:43], v[168:171]
	v_mfma_f32_16x16x128_f8f6f4 v[68:71], v[104:111], v[44:51], v[194:197]
	v_mfma_f32_16x16x128_f8f6f4 v[64:67], v[112:119], v[44:51], v[200:203]
	s_setprio 0
	s_barrier
	s_mov_b32 m0, s75
	s_or_b32 s23, s21, 0x80
	ds_read_b128 v[36:39], v198 offset:49152
	ds_read_b128 v[40:43], v198 offset:50176
	ds_read_b128 v[148:151], v198 offset:51200
	ds_read_b128 v[152:155], v198 offset:52224
	ds_read_b128 v[156:159], v198 offset:53248
	ds_read_b128 v[160:163], v198 offset:54272
	ds_read_b128 v[164:167], v198 offset:55296
	ds_read_b128 v[168:171], v198 offset:56320
	buffer_load_dwordx4 v199, s[48:51], s23 offen lds
	s_mov_b32 m0, s76
	s_add_i32 s21, s21, 0x40080
	buffer_load_dwordx4 v228, s[48:51], s23 offen lds
	s_mov_b32 m0, s82
	s_nop 0
	buffer_load_dwordx4 v199, s[48:51], s21 offen lds
	s_mov_b32 m0, s83
	s_nop 0
	buffer_load_dwordx4 v228, s[48:51], s21 offen lds
	s_mov_b32 m0, s77
	s_nop 0
	buffer_load_dwordx4 v229, s[44:47], s23 offen lds
	s_mov_b32 m0, s80
	s_nop 0
	buffer_load_dwordx4 v252, s[44:47], s23 offen lds
	s_waitcnt vmcnt(8)
	s_waitcnt lgkmcnt(0)
	s_barrier
	s_setprio 1
	s_waitcnt lgkmcnt(6)
	v_mfma_f32_16x16x128_f8f6f4 v[60:63], v[0:7], v[36:43], v[60:63]
	v_mfma_f32_16x16x128_f8f6f4 v[8:11], v[20:27], v[36:43], v[204:207]
	s_waitcnt lgkmcnt(4)
	v_mfma_f32_16x16x128_f8f6f4 v[48:51], v[0:7], v[148:155], v[208:211]
	v_mfma_f32_16x16x128_f8f6f4 v[44:47], v[20:27], v[148:155], v[212:215]
	s_waitcnt lgkmcnt(2)
	v_mfma_f32_16x16x128_f8f6f4 v[32:35], v[0:7], v[156:163], v[216:219]
	v_mfma_f32_16x16x128_f8f6f4 v[28:31], v[20:27], v[156:163], v[220:223]
	s_waitcnt lgkmcnt(0)
	v_mfma_f32_16x16x128_f8f6f4 v[16:19], v[0:7], v[164:171], v[16:19]
	v_mfma_f32_16x16x128_f8f6f4 v[12:15], v[20:27], v[164:171], v[224:227]
	v_mfma_f32_16x16x128_f8f6f4 v[56:59], v[104:111], v[36:43], v[56:59]
	v_mfma_f32_16x16x128_f8f6f4 v[52:55], v[112:119], v[36:43], v[52:55]
	v_mfma_f32_16x16x128_f8f6f4 v[40:43], v[104:111], v[148:155], v[232:235]
	v_mfma_f32_16x16x128_f8f6f4 v[36:39], v[112:119], v[148:155], v[236:239]
	v_mfma_f32_16x16x128_f8f6f4 v[24:27], v[104:111], v[156:163], v[240:243]
	v_mfma_f32_16x16x128_f8f6f4 v[20:23], v[112:119], v[156:163], v[244:247]
	v_mfma_f32_16x16x128_f8f6f4 v[4:7], v[104:111], v[164:171], v[248:251]
	v_mfma_f32_16x16x128_f8f6f4 v[0:3], v[112:119], v[164:171], v[172:175]
	s_setprio 0
	s_barrier
	s_add_i32 s12, s12, 2
	s_addk_i32 s13, 0x100
	s_cmp_gt_u32 s12, 13
	s_cbranch_scc0 .LBB0_1507
	s_and_b64 vcc, exec, s[18:19]
	s_cbranch_vccz .LBB0_1510
	s_barrier

.LBB0_1539:
	v_add_u32_e32 v124, 0x10000, v174
	v_add_u32_e32 v156, 0x14000, v174
	ds_read_b128 v[104:107], v124
	ds_read_b128 v[116:119], v124 offset:1024
	ds_read_b128 v[120:123], v124 offset:2048
	ds_read_b128 v[124:127], v124 offset:3072
	ds_read_b128 v[128:131], v156
	ds_read_b128 v[136:139], v156 offset:1024
	ds_read_b128 v[152:155], v156 offset:2048
	ds_read_b128 v[156:159], v156 offset:3072
	s_add_i32 s19, s13, 0xfff80080
	s_cmp_eq_u32 s12, 28
	s_cselect_b32 s45, s23, s41
	s_cselect_b32 s44, s22, s40
	s_cselect_b32 s47, s29, s43
	s_cselect_b32 s46, s28, s42
	s_cselect_b32 s19, 0, s19
	s_cselect_b32 s49, s31, s53
	s_cselect_b32 s48, s30, s52
	s_cselect_b32 s51, s35, s5
	s_cselect_b32 s50, s34, s4
	s_mov_b32 m0, s92
	ds_read_b128 v[160:163], v175
	ds_read_b128 v[164:167], v175 offset:1024
	ds_read_b128 v[178:181], v175 offset:2048
	ds_read_b128 v[182:185], v175 offset:3072
	ds_read_b128 v[186:189], v175 offset:4096
	ds_read_b128 v[190:193], v175 offset:5120
	ds_read_b128 v[194:197], v175 offset:6144
	ds_read_b128 v[198:201], v175 offset:7168
	buffer_load_dwordx4 v172, s[40:43], s13 offen lds
	s_mov_b32 m0, s94
	s_nop 0
	buffer_load_dwordx4 v173, s[40:43], s13 offen lds
	s_waitcnt vmcnt(8)
	s_waitcnt lgkmcnt(0)
	s_barrier
	s_setprio 1
	s_waitcnt lgkmcnt(7)
	v_mfma_f32_16x16x32_bf16 v[148:151], v[104:107], v[160:163], v[148:151]
	v_mfma_f32_16x16x32_bf16 v[144:147], v[120:123], v[160:163], v[144:147]
	s_waitcnt lgkmcnt(5)
	v_mfma_f32_16x16x32_bf16 v[112:115], v[104:107], v[178:181], v[112:115]
	v_mfma_f32_16x16x32_bf16 v[108:111], v[120:123], v[178:181], v[108:111]
	s_waitcnt lgkmcnt(3)
	v_mfma_f32_16x16x32_bf16 v[92:95], v[104:107], v[186:189], v[92:95]
	v_mfma_f32_16x16x32_bf16 v[88:91], v[120:123], v[186:189], v[88:91]
	s_waitcnt lgkmcnt(1)
	v_mfma_f32_16x16x32_bf16 v[76:79], v[104:107], v[194:197], v[76:79]
	v_mfma_f32_16x16x32_bf16 v[72:75], v[120:123], v[194:197], v[72:75]
	v_mfma_f32_16x16x32_bf16 v[148:151], v[116:119], v[164:167], v[148:151]
	v_mfma_f32_16x16x32_bf16 v[144:147], v[124:127], v[164:167], v[144:147]
	v_mfma_f32_16x16x32_bf16 v[112:115], v[116:119], v[182:185], v[112:115]
	v_mfma_f32_16x16x32_bf16 v[108:111], v[124:127], v[182:185], v[108:111]
	v_mfma_f32_16x16x32_bf16 v[92:95], v[116:119], v[190:193], v[92:95]
	v_mfma_f32_16x16x32_bf16 v[88:91], v[124:127], v[190:193], v[88:91]
	s_waitcnt lgkmcnt(0)
	v_mfma_f32_16x16x32_bf16 v[76:79], v[116:119], v[198:201], v[76:79]
	v_mfma_f32_16x16x32_bf16 v[72:75], v[124:127], v[198:201], v[72:75]
	v_mfma_f32_16x16x32_bf16 v[140:143], v[128:131], v[160:163], v[140:143]
	v_mfma_f32_16x16x32_bf16 v[132:135], v[152:155], v[160:163], v[132:135]
	v_mfma_f32_16x16x32_bf16 v[100:103], v[128:131], v[178:181], v[100:103]
	v_mfma_f32_16x16x32_bf16 v[96:99], v[152:155], v[178:181], v[96:99]
	v_mfma_f32_16x16x32_bf16 v[84:87], v[128:131], v[186:189], v[84:87]
	v_mfma_f32_16x16x32_bf16 v[80:83], v[152:155], v[186:189], v[80:83]
	v_mfma_f32_16x16x32_bf16 v[68:71], v[128:131], v[194:197], v[68:71]
	v_mfma_f32_16x16x32_bf16 v[64:67], v[152:155], v[194:197], v[64:67]
	v_mfma_f32_16x16x32_bf16 v[140:143], v[136:139], v[164:167], v[140:143]
	v_mfma_f32_16x16x32_bf16 v[132:135], v[156:159], v[164:167], v[132:135]
	v_mfma_f32_16x16x32_bf16 v[100:103], v[136:139], v[182:185], v[100:103]
	v_mfma_f32_16x16x32_bf16 v[96:99], v[156:159], v[182:185], v[96:99]
	v_mfma_f32_16x16x32_bf16 v[84:87], v[136:139], v[190:193], v[84:87]
	v_mfma_f32_16x16x32_bf16 v[80:83], v[156:159], v[190:193], v[80:83]
	v_mfma_f32_16x16x32_bf16 v[68:71], v[136:139], v[198:201], v[68:71]
	v_mfma_f32_16x16x32_bf16 v[64:67], v[156:159], v[198:201], v[64:67]
	s_setprio 0
	s_barrier
	s_mov_b32 m0, s61
	ds_read_b128 v[160:163], v175 offset:16384
	ds_read_b128 v[164:167], v175 offset:17408
	ds_read_b128 v[178:181], v175 offset:18432
	ds_read_b128 v[182:185], v175 offset:19456
	ds_read_b128 v[186:189], v175 offset:20480
	ds_read_b128 v[190:193], v175 offset:21504
	ds_read_b128 v[194:197], v175 offset:22528
	ds_read_b128 v[198:201], v175 offset:23552
	buffer_load_dwordx4 v170, s[48:51], s19 offen lds
	s_mov_b32 m0, s69
	s_add_i32 s21, s19, 0x80000
	buffer_load_dwordx4 v171, s[48:51], s19 offen lds
	s_mov_b32 m0, s70
	s_nop 0
	buffer_load_dwordx4 v170, s[48:51], s21 offen lds
	s_mov_b32 m0, s71
	s_nop 0
	buffer_load_dwordx4 v171, s[48:51], s21 offen lds
	s_mov_b32 m0, s59
	s_nop 0
	buffer_load_dwordx4 v172, s[44:47], s19 offen lds
	s_mov_b32 m0, s72
	s_nop 0
	buffer_load_dwordx4 v173, s[44:47], s19 offen lds
	s_waitcnt vmcnt(8)
	s_waitcnt lgkmcnt(0)
	s_barrier
	s_setprio 1
	s_waitcnt lgkmcnt(7)
	v_mfma_f32_16x16x32_bf16 v[60:63], v[104:107], v[160:163], v[60:63]
	v_mfma_f32_16x16x32_bf16 v[48:51], v[120:123], v[160:163], v[48:51]
	s_waitcnt lgkmcnt(5)
	v_mfma_f32_16x16x32_bf16 v[44:47], v[104:107], v[178:181], v[44:47]
	v_mfma_f32_16x16x32_bf16 v[40:43], v[120:123], v[178:181], v[40:43]
	s_waitcnt lgkmcnt(3)
	v_mfma_f32_16x16x32_bf16 v[28:31], v[104:107], v[186:189], v[28:31]
	v_mfma_f32_16x16x32_bf16 v[24:27], v[120:123], v[186:189], v[24:27]
	s_waitcnt lgkmcnt(1)
	v_mfma_f32_16x16x32_bf16 v[12:15], v[104:107], v[194:197], v[12:15]
	v_mfma_f32_16x16x32_bf16 v[8:11], v[120:123], v[194:197], v[8:11]
	v_mfma_f32_16x16x32_bf16 v[60:63], v[116:119], v[164:167], v[60:63]
	v_mfma_f32_16x16x32_bf16 v[48:51], v[124:127], v[164:167], v[48:51]
	v_mfma_f32_16x16x32_bf16 v[44:47], v[116:119], v[182:185], v[44:47]
	v_mfma_f32_16x16x32_bf16 v[40:43], v[124:127], v[182:185], v[40:43]
	v_mfma_f32_16x16x32_bf16 v[28:31], v[116:119], v[190:193], v[28:31]
	v_mfma_f32_16x16x32_bf16 v[24:27], v[124:127], v[190:193], v[24:27]
	s_waitcnt lgkmcnt(0)
	v_mfma_f32_16x16x32_bf16 v[12:15], v[116:119], v[198:201], v[12:15]
	v_mfma_f32_16x16x32_bf16 v[8:11], v[124:127], v[198:201], v[8:11]
	v_mfma_f32_16x16x32_bf16 v[56:59], v[128:131], v[160:163], v[56:59]
	v_mfma_f32_16x16x32_bf16 v[52:55], v[152:155], v[160:163], v[52:55]
	v_mfma_f32_16x16x32_bf16 v[36:39], v[128:131], v[178:181], v[36:39]
	v_mfma_f32_16x16x32_bf16 v[32:35], v[152:155], v[178:181], v[32:35]
	v_mfma_f32_16x16x32_bf16 v[20:23], v[128:131], v[186:189], v[20:23]
	v_mfma_f32_16x16x32_bf16 v[16:19], v[152:155], v[186:189], v[16:19]
	v_mfma_f32_16x16x32_bf16 v[4:7], v[128:131], v[194:197], v[4:7]
	v_mfma_f32_16x16x32_bf16 v[0:3], v[152:155], v[194:197], v[0:3]
	v_mfma_f32_16x16x32_bf16 v[56:59], v[136:139], v[164:167], v[56:59]
	v_mfma_f32_16x16x32_bf16 v[52:55], v[156:159], v[164:167], v[52:55]
	v_mfma_f32_16x16x32_bf16 v[36:39], v[136:139], v[182:185], v[36:39]
	v_mfma_f32_16x16x32_bf16 v[32:35], v[156:159], v[182:185], v[32:35]
	v_mfma_f32_16x16x32_bf16 v[20:23], v[136:139], v[190:193], v[20:23]
	v_mfma_f32_16x16x32_bf16 v[16:19], v[156:159], v[190:193], v[16:19]
	v_mfma_f32_16x16x32_bf16 v[4:7], v[136:139], v[198:201], v[4:7]
	v_mfma_f32_16x16x32_bf16 v[0:3], v[156:159], v[198:201], v[0:3]
	s_setprio 0
	s_barrier
	v_add_u32_e32 v124, 0x18000, v174
	v_add_u32_e32 v156, 0x1c000, v174
	ds_read_b128 v[104:107], v124
	ds_read_b128 v[116:119], v124 offset:1024
	ds_read_b128 v[120:123], v124 offset:2048
	ds_read_b128 v[124:127], v124 offset:3072
	ds_read_b128 v[128:131], v156
	ds_read_b128 v[136:139], v156 offset:1024
	ds_read_b128 v[152:155], v156 offset:2048
	ds_read_b128 v[156:159], v156 offset:3072
	s_mov_b32 m0, s73
	ds_read_b128 v[160:163], v175 offset:32768
	ds_read_b128 v[164:167], v175 offset:33792
	ds_read_b128 v[178:181], v175 offset:34816
	ds_read_b128 v[182:185], v175 offset:35840
	ds_read_b128 v[186:189], v175 offset:36864
	ds_read_b128 v[190:193], v175 offset:37888
	ds_read_b128 v[194:197], v175 offset:38912
	ds_read_b128 v[198:201], v175 offset:39936
	buffer_load_dwordx4 v172, s[44:47], s21 offen lds
	s_mov_b32 m0, s74
	s_nop 0
	buffer_load_dwordx4 v173, s[44:47], s21 offen lds
	s_waitcnt vmcnt(8)
	s_waitcnt lgkmcnt(0)
	s_barrier
	s_setprio 1
	s_waitcnt lgkmcnt(7)
	v_mfma_f32_16x16x32_bf16 v[148:151], v[104:107], v[160:163], v[148:151]
	v_mfma_f32_16x16x32_bf16 v[144:147], v[120:123], v[160:163], v[144:147]
	s_waitcnt lgkmcnt(5)
	v_mfma_f32_16x16x32_bf16 v[112:115], v[104:107], v[178:181], v[112:115]
	v_mfma_f32_16x16x32_bf16 v[108:111], v[120:123], v[178:181], v[108:111]
	s_waitcnt lgkmcnt(3)
	v_mfma_f32_16x16x32_bf16 v[92:95], v[104:107], v[186:189], v[92:95]
	v_mfma_f32_16x16x32_bf16 v[88:91], v[120:123], v[186:189], v[88:91]
	s_waitcnt lgkmcnt(1)
	v_mfma_f32_16x16x32_bf16 v[76:79], v[104:107], v[194:197], v[76:79]
	v_mfma_f32_16x16x32_bf16 v[72:75], v[120:123], v[194:197], v[72:75]
	v_mfma_f32_16x16x32_bf16 v[148:151], v[116:119], v[164:167], v[148:151]
	v_mfma_f32_16x16x32_bf16 v[144:147], v[124:127], v[164:167], v[144:147]
	v_mfma_f32_16x16x32_bf16 v[112:115], v[116:119], v[182:185], v[112:115]
	v_mfma_f32_16x16x32_bf16 v[108:111], v[124:127], v[182:185], v[108:111]
	v_mfma_f32_16x16x32_bf16 v[92:95], v[116:119], v[190:193], v[92:95]
	v_mfma_f32_16x16x32_bf16 v[88:91], v[124:127], v[190:193], v[88:91]
	s_waitcnt lgkmcnt(0)
	v_mfma_f32_16x16x32_bf16 v[76:79], v[116:119], v[198:201], v[76:79]
	v_mfma_f32_16x16x32_bf16 v[72:75], v[124:127], v[198:201], v[72:75]
	v_mfma_f32_16x16x32_bf16 v[140:143], v[128:131], v[160:163], v[140:143]
	v_mfma_f32_16x16x32_bf16 v[132:135], v[152:155], v[160:163], v[132:135]
	v_mfma_f32_16x16x32_bf16 v[100:103], v[128:131], v[178:181], v[100:103]
	v_mfma_f32_16x16x32_bf16 v[96:99], v[152:155], v[178:181], v[96:99]
	v_mfma_f32_16x16x32_bf16 v[84:87], v[128:131], v[186:189], v[84:87]
	v_mfma_f32_16x16x32_bf16 v[80:83], v[152:155], v[186:189], v[80:83]
	v_mfma_f32_16x16x32_bf16 v[68:71], v[128:131], v[194:197], v[68:71]
	v_mfma_f32_16x16x32_bf16 v[64:67], v[152:155], v[194:197], v[64:67]
	v_mfma_f32_16x16x32_bf16 v[140:143], v[136:139], v[164:167], v[140:143]
	v_mfma_f32_16x16x32_bf16 v[132:135], v[156:159], v[164:167], v[132:135]
	v_mfma_f32_16x16x32_bf16 v[100:103], v[136:139], v[182:185], v[100:103]
	v_mfma_f32_16x16x32_bf16 v[96:99], v[156:159], v[182:185], v[96:99]
	v_mfma_f32_16x16x32_bf16 v[84:87], v[136:139], v[190:193], v[84:87]
	v_mfma_f32_16x16x32_bf16 v[80:83], v[156:159], v[190:193], v[80:83]
	v_mfma_f32_16x16x32_bf16 v[68:71], v[136:139], v[198:201], v[68:71]
	v_mfma_f32_16x16x32_bf16 v[64:67], v[156:159], v[198:201], v[64:67]
	s_setprio 0
	s_barrier
	s_mov_b32 m0, s75
	s_or_b32 s21, s19, 0x80
	ds_read_b128 v[160:163], v175 offset:49152
	ds_read_b128 v[164:167], v175 offset:50176
	ds_read_b128 v[178:181], v175 offset:51200
	ds_read_b128 v[182:185], v175 offset:52224
	ds_read_b128 v[186:189], v175 offset:53248
	ds_read_b128 v[190:193], v175 offset:54272
	ds_read_b128 v[194:197], v175 offset:55296
	ds_read_b128 v[198:201], v175 offset:56320
	buffer_load_dwordx4 v170, s[48:51], s21 offen lds
	s_mov_b32 m0, s76
	s_add_i32 s19, s19, 0x80080
	buffer_load_dwordx4 v171, s[48:51], s21 offen lds
	s_mov_b32 m0, s83
	s_nop 0
	buffer_load_dwordx4 v170, s[48:51], s19 offen lds
	s_mov_b32 m0, s88
	s_nop 0
	buffer_load_dwordx4 v171, s[48:51], s19 offen lds
	s_mov_b32 m0, s77
	s_nop 0
	buffer_load_dwordx4 v172, s[44:47], s21 offen lds
	s_mov_b32 m0, s82
	s_nop 0
	buffer_load_dwordx4 v173, s[44:47], s21 offen lds
	s_waitcnt vmcnt(8)
	s_waitcnt lgkmcnt(0)
	s_barrier
	s_setprio 1
	s_waitcnt lgkmcnt(7)
	v_mfma_f32_16x16x32_bf16 v[60:63], v[104:107], v[160:163], v[60:63]
	v_mfma_f32_16x16x32_bf16 v[48:51], v[120:123], v[160:163], v[48:51]
	s_waitcnt lgkmcnt(5)
	v_mfma_f32_16x16x32_bf16 v[44:47], v[104:107], v[178:181], v[44:47]
	v_mfma_f32_16x16x32_bf16 v[40:43], v[120:123], v[178:181], v[40:43]
	s_waitcnt lgkmcnt(3)
	v_mfma_f32_16x16x32_bf16 v[28:31], v[104:107], v[186:189], v[28:31]
	v_mfma_f32_16x16x32_bf16 v[24:27], v[120:123], v[186:189], v[24:27]
	s_waitcnt lgkmcnt(1)
	v_mfma_f32_16x16x32_bf16 v[12:15], v[104:107], v[194:197], v[12:15]
	v_mfma_f32_16x16x32_bf16 v[8:11], v[120:123], v[194:197], v[8:11]
	v_mfma_f32_16x16x32_bf16 v[60:63], v[116:119], v[164:167], v[60:63]
	v_mfma_f32_16x16x32_bf16 v[48:51], v[124:127], v[164:167], v[48:51]
	v_mfma_f32_16x16x32_bf16 v[44:47], v[116:119], v[182:185], v[44:47]
	v_mfma_f32_16x16x32_bf16 v[40:43], v[124:127], v[182:185], v[40:43]
	v_mfma_f32_16x16x32_bf16 v[28:31], v[116:119], v[190:193], v[28:31]
	v_mfma_f32_16x16x32_bf16 v[24:27], v[124:127], v[190:193], v[24:27]
	s_waitcnt lgkmcnt(0)
	v_mfma_f32_16x16x32_bf16 v[12:15], v[116:119], v[198:201], v[12:15]
	v_mfma_f32_16x16x32_bf16 v[8:11], v[124:127], v[198:201], v[8:11]
	v_mfma_f32_16x16x32_bf16 v[56:59], v[128:131], v[160:163], v[56:59]
	v_mfma_f32_16x16x32_bf16 v[52:55], v[152:155], v[160:163], v[52:55]
	v_mfma_f32_16x16x32_bf16 v[36:39], v[128:131], v[178:181], v[36:39]
	v_mfma_f32_16x16x32_bf16 v[32:35], v[152:155], v[178:181], v[32:35]
	v_mfma_f32_16x16x32_bf16 v[20:23], v[128:131], v[186:189], v[20:23]
	v_mfma_f32_16x16x32_bf16 v[16:19], v[152:155], v[186:189], v[16:19]
	v_mfma_f32_16x16x32_bf16 v[4:7], v[128:131], v[194:197], v[4:7]
	v_mfma_f32_16x16x32_bf16 v[0:3], v[152:155], v[194:197], v[0:3]
	v_mfma_f32_16x16x32_bf16 v[56:59], v[136:139], v[164:167], v[56:59]
	v_mfma_f32_16x16x32_bf16 v[52:55], v[156:159], v[164:167], v[52:55]
	v_mfma_f32_16x16x32_bf16 v[36:39], v[136:139], v[182:185], v[36:39]
	v_mfma_f32_16x16x32_bf16 v[32:35], v[156:159], v[182:185], v[32:35]
	v_mfma_f32_16x16x32_bf16 v[20:23], v[136:139], v[190:193], v[20:23]
	v_mfma_f32_16x16x32_bf16 v[16:19], v[156:159], v[190:193], v[16:19]
	v_mfma_f32_16x16x32_bf16 v[4:7], v[136:139], v[198:201], v[4:7]
	v_mfma_f32_16x16x32_bf16 v[0:3], v[156:159], v[198:201], v[0:3]
	s_setprio 0
	s_barrier
	s_add_i32 s12, s12, 2
	s_addk_i32 s13, 0x100
	s_cmp_gt_u32 s12, 29
	s_cbranch_scc0 .LBB0_1539
	s_and_b64 vcc, exec, s[8:9]
	s_cbranch_vccz .LBB0_1542
	s_barrier

.LBB0_1723:
	s_nop 0
	v_add_u32_e32 v64, 0x10000, v138
	ds_read_b128 v[140:143], v64
	ds_read_b128 v[144:147], v64 offset:1024
	ds_read_b128 v[148:151], v64 offset:2048
	ds_read_b128 v[152:155], v64 offset:3072
	v_add_u32_e32 v64, 0x14000, v138
	ds_read_b128 v[156:159], v64
	ds_read_b128 v[160:163], v64 offset:1024
	ds_read_b128 v[164:167], v64 offset:2048
	ds_read_b128 v[168:171], v64 offset:3072
	s_cmp_eq_u32 s12, 12
	s_cselect_b64 s[4:5], -1, 0
	s_and_b64 s[48:49], s[4:5], exec
	s_cselect_b32 s31, 0, s13
	s_cselect_b32 s49, s35, s45
	s_cselect_b32 s48, s34, s44
	s_cselect_b32 s51, s43, s47
	s_cselect_b32 s50, s42, s46
	s_cselect_b32 s56, s62, s40
	s_cselect_b32 s57, s63, s41
	s_cselect_b32 s58, s64, s66
	s_cselect_b32 s59, s65, s67
	s_or_b32 vcc_lo, s31, 0x80
	s_add_i32 vcc_hi, s13, 0xffffff80
	ds_read_b128 v[198:201], v139
	ds_read_b128 v[202:205], v139 offset:1024
	ds_read_b128 v[206:209], v139 offset:2048
	ds_read_b128 v[210:213], v139 offset:3072
	ds_read_b128 v[214:217], v139 offset:4096
	ds_read_b128 v[218:221], v139 offset:5120
	ds_read_b128 v[222:225], v139 offset:6144
	ds_read_b128 v[226:229], v139 offset:7168
	v_mbcnt_lo_u32_b32 v64, -1, 0
	v_mbcnt_hi_u32_b32 v64, -1, v64
	s_mov_b32 m0, s93
	v_lshl_add_u32 v64, v64, 4, s71
	ds_read_b64 v[64:65], v64 offset:8
	s_waitcnt lgkmcnt(0)
	buffer_load_dwordx4 v64, s[44:47], vcc_hi offen lds
	s_mov_b32 m0, s96
	s_nop 0
	buffer_load_dwordx4 v65, s[44:47], vcc_hi offen lds
	s_waitcnt vmcnt(8)
	s_waitcnt lgkmcnt(0)
	s_barrier
	s_setprio 1
	v_mfma_f32_16x16x128_f8f6f4 v[128:131], v[148:155], v[198:205], v[128:131]
	v_mfma_f32_16x16x128_f8f6f4 v[108:111], v[140:147], v[206:213], v[108:111]
	v_mfma_f32_16x16x128_f8f6f4 v[104:107], v[148:155], v[206:213], v[104:107]
	v_mfma_f32_16x16x128_f8f6f4 v[112:115], v[140:147], v[198:205], v[124:127]
	v_mfma_f32_16x16x128_f8f6f4 v[132:135], v[140:147], v[214:221], v[92:95]
	v_mfma_f32_16x16x128_f8f6f4 v[172:175], v[148:155], v[214:221], v[88:91]
	v_mfma_f32_16x16x128_f8f6f4 v[178:181], v[140:147], v[222:229], v[76:79]
	v_mfma_f32_16x16x128_f8f6f4 v[182:185], v[148:155], v[222:229], v[72:75]
	v_mfma_f32_16x16x128_f8f6f4 v[120:123], v[156:163], v[198:205], v[120:123]
	v_mfma_f32_16x16x128_f8f6f4 v[116:119], v[164:171], v[198:205], v[116:119]
	v_mfma_f32_16x16x128_f8f6f4 v[100:103], v[156:163], v[206:213], v[100:103]
	v_mfma_f32_16x16x128_f8f6f4 v[96:99], v[164:171], v[206:213], v[96:99]
	v_mfma_f32_16x16x128_f8f6f4 v[186:189], v[156:163], v[214:221], v[84:87]
	v_mfma_f32_16x16x128_f8f6f4 v[190:193], v[164:171], v[214:221], v[80:83]
	v_mfma_f32_16x16x128_f8f6f4 v[194:197], v[156:163], v[222:229], v[68:71]
	v_mfma_f32_16x16x128_f8f6f4 v[198:201], v[164:171], v[222:229], v[24:27]
	s_setprio 0
	s_barrier
	s_mov_b32 m0, s74
	s_add_i32 vcc_hi, s31, 0x40000
	s_and_b64 s[4:5], s[38:39], s[4:5]
	ds_read_b128 v[64:67], v139 offset:16384
	ds_read_b128 v[68:71], v139 offset:17408
	ds_read_b128 v[72:75], v139 offset:18432
	ds_read_b128 v[76:79], v139 offset:19456
	ds_read_b128 v[80:83], v139 offset:20480
	ds_read_b128 v[84:87], v139 offset:21504
	ds_read_b128 v[88:91], v139 offset:22528
	ds_read_b128 v[92:95], v139 offset:23552
	buffer_load_dwordx4 v136, s[56:59], s31 offen lds
	s_mov_b32 m0, s75
	s_and_b64 s[4:5], s[4:5], exec
	buffer_load_dwordx4 v137, s[56:59], s31 offen lds
	s_mov_b32 m0, s76
	s_mov_b32 s4, 0x24000
	buffer_load_dwordx4 v136, s[56:59], vcc_hi offen lds
	s_mov_b32 m0, s77
	s_cselect_b32 s4, s4, 0x20500
	buffer_load_dwordx4 v137, s[56:59], vcc_hi offen lds
	v_mbcnt_lo_u32_b32 v24, -1, 0
	v_mbcnt_hi_u32_b32 v24, -1, v24
	s_add_i32 s4, s70, s4
	v_lshl_add_u32 v24, v24, 4, s4
	ds_read_b64 v[24:25], v24
	s_mov_b32 m0, s70
	s_waitcnt lgkmcnt(0)
	buffer_load_dwordx4 v24, s[48:51], s31 offen lds
	s_mov_b32 m0, s78
	s_nop 0
	buffer_load_dwordx4 v25, s[48:51], s31 offen lds
	s_waitcnt vmcnt(8)
	s_waitcnt lgkmcnt(0)
	s_barrier
	s_setprio 1
	v_mfma_f32_16x16x128_f8f6f4 v[60:63], v[140:147], v[64:71], v[60:63]
	v_mfma_f32_16x16x128_f8f6f4 v[0:3], v[148:155], v[64:71], v[0:3]
	v_mfma_f32_16x16x128_f8f6f4 v[12:15], v[140:147], v[88:95], v[12:15]
	v_mfma_f32_16x16x128_f8f6f4 v[206:209], v[140:147], v[72:79], v[44:47]
	v_mfma_f32_16x16x128_f8f6f4 v[210:213], v[148:155], v[72:79], v[48:51]
	v_mfma_f32_16x16x128_f8f6f4 v[214:217], v[140:147], v[80:87], v[28:31]
	v_mfma_f32_16x16x128_f8f6f4 v[218:221], v[148:155], v[80:87], v[32:35]
	v_mfma_f32_16x16x128_f8f6f4 v[222:225], v[148:155], v[88:95], v[16:19]
	v_mfma_f32_16x16x128_f8f6f4 v[56:59], v[164:171], v[64:71], v[56:59]
	v_mfma_f32_16x16x128_f8f6f4 v[244:247], v[164:171], v[80:87], v[244:247]
	v_mfma_f32_16x16x128_f8f6f4 v[226:229], v[156:163], v[64:71], v[52:55]
	v_mfma_f32_16x16x128_f8f6f4 v[232:235], v[156:163], v[72:79], v[36:39]
	v_mfma_f32_16x16x128_f8f6f4 v[236:239], v[164:171], v[72:79], v[40:43]
	v_mfma_f32_16x16x128_f8f6f4 v[240:243], v[156:163], v[80:87], v[20:23]
	v_mfma_f32_16x16x128_f8f6f4 v[248:251], v[156:163], v[88:95], v[4:7]
	v_mfma_f32_16x16x128_f8f6f4 v[64:67], v[164:171], v[88:95], v[8:11]
	s_setprio 0
	s_barrier
	s_nop 2
	v_add_u32_e32 v20, 0x18000, v138
	v_add_u32_e32 v24, 0x1c000, v138
	ds_read_b128 v[4:7], v20
	ds_read_b128 v[8:11], v20 offset:1024
	ds_read_b128 v[16:19], v20 offset:2048
	ds_read_b128 v[20:23], v20 offset:3072
	ds_read_b128 v[140:143], v24
	ds_read_b128 v[144:147], v24 offset:1024
	ds_read_b128 v[148:151], v24 offset:2048
	ds_read_b128 v[152:155], v24 offset:3072
	ds_read_b128 v[24:27], v139 offset:32768
	ds_read_b128 v[28:31], v139 offset:33792
	ds_read_b128 v[32:35], v139 offset:34816
	ds_read_b128 v[36:39], v139 offset:35840
	ds_read_b128 v[40:43], v139 offset:36864
	ds_read_b128 v[44:47], v139 offset:37888
	ds_read_b128 v[48:51], v139 offset:38912
	ds_read_b128 v[52:55], v139 offset:39936
	v_mbcnt_lo_u32_b32 v68, -1, 0
	v_mbcnt_hi_u32_b32 v68, -1, v68
	s_mov_b32 m0, s79
	v_lshl_add_u32 v68, v68, 4, s4
	ds_read_b64 v[68:69], v68 offset:8
	s_waitcnt lgkmcnt(0)
	buffer_load_dwordx4 v68, s[48:51], s31 offen lds
	s_mov_b32 m0, s80
	s_nop 0
	buffer_load_dwordx4 v69, s[48:51], s31 offen lds
	s_waitcnt vmcnt(8)
	s_waitcnt lgkmcnt(0)
	s_barrier
	s_setprio 1
	v_mfma_f32_16x16x128_f8f6f4 v[124:127], v[4:11], v[24:31], v[112:115]
	v_mfma_f32_16x16x128_f8f6f4 v[128:131], v[16:23], v[24:31], v[128:131]
	v_mfma_f32_16x16x128_f8f6f4 v[108:111], v[4:11], v[32:39], v[108:111]
	v_mfma_f32_16x16x128_f8f6f4 v[104:107], v[16:23], v[32:39], v[104:107]
	v_mfma_f32_16x16x128_f8f6f4 v[92:95], v[4:11], v[40:47], v[132:135]
	v_mfma_f32_16x16x128_f8f6f4 v[88:91], v[16:23], v[40:47], v[172:175]
	v_mfma_f32_16x16x128_f8f6f4 v[76:79], v[4:11], v[48:55], v[178:181]
	v_mfma_f32_16x16x128_f8f6f4 v[72:75], v[16:23], v[48:55], v[182:185]
	v_mfma_f32_16x16x128_f8f6f4 v[120:123], v[140:147], v[24:31], v[120:123]
	v_mfma_f32_16x16x128_f8f6f4 v[116:119], v[148:155], v[24:31], v[116:119]
	v_mfma_f32_16x16x128_f8f6f4 v[100:103], v[140:147], v[32:39], v[100:103]
	v_mfma_f32_16x16x128_f8f6f4 v[96:99], v[148:155], v[32:39], v[96:99]
	v_mfma_f32_16x16x128_f8f6f4 v[84:87], v[140:147], v[40:47], v[186:189]
	v_mfma_f32_16x16x128_f8f6f4 v[80:83], v[148:155], v[40:47], v[190:193]
	v_mfma_f32_16x16x128_f8f6f4 v[68:71], v[140:147], v[48:55], v[194:197]
	v_mfma_f32_16x16x128_f8f6f4 v[24:27], v[148:155], v[48:55], v[198:201]
	s_setprio 0
	s_barrier
	s_mov_b32 m0, s83
	ds_read_b128 v[36:39], v139 offset:49152
	ds_read_b128 v[40:43], v139 offset:50176
	ds_read_b128 v[156:159], v139 offset:51200
	ds_read_b128 v[160:163], v139 offset:52224
	ds_read_b128 v[164:167], v139 offset:53248
	ds_read_b128 v[168:171], v139 offset:54272
	ds_read_b128 v[198:201], v139 offset:55296
	ds_read_b128 v[202:205], v139 offset:56320
	buffer_load_dwordx4 v136, s[56:59], vcc_lo offen lds
	s_mov_b32 m0, s88
	s_add_i32 s31, s31, 0x40080
	buffer_load_dwordx4 v137, s[56:59], vcc_lo offen lds
	s_mov_b32 m0, s91
	s_nop 0
	buffer_load_dwordx4 v136, s[56:59], s31 offen lds
	s_mov_b32 m0, s92
	s_nop 0
	buffer_load_dwordx4 v137, s[56:59], s31 offen lds
	v_mbcnt_lo_u32_b32 v28, -1, 0
	v_mbcnt_hi_u32_b32 v28, -1, v28
	s_mov_b32 m0, s89
	v_lshl_add_u32 v28, v28, 4, s4
	ds_read_b64 v[28:29], v28
	s_waitcnt lgkmcnt(0)
	buffer_load_dwordx4 v28, s[48:51], vcc_lo offen lds
	s_mov_b32 m0, s90
	s_nop 0
	buffer_load_dwordx4 v29, s[48:51], vcc_lo offen lds
	s_waitcnt vmcnt(8)
	s_waitcnt lgkmcnt(0)
	s_barrier
	s_setprio 1
	v_mfma_f32_16x16x128_f8f6f4 v[60:63], v[4:11], v[36:43], v[60:63]
	v_mfma_f32_16x16x128_f8f6f4 v[0:3], v[16:23], v[36:43], v[0:3]
	v_mfma_f32_16x16x128_f8f6f4 v[44:47], v[4:11], v[156:163], v[206:209]
	v_mfma_f32_16x16x128_f8f6f4 v[48:51], v[16:23], v[156:163], v[210:213]
	v_mfma_f32_16x16x128_f8f6f4 v[28:31], v[4:11], v[164:171], v[214:217]
	v_mfma_f32_16x16x128_f8f6f4 v[32:35], v[16:23], v[164:171], v[218:221]
	v_mfma_f32_16x16x128_f8f6f4 v[12:15], v[4:11], v[198:205], v[12:15]
	v_mfma_f32_16x16x128_f8f6f4 v[16:19], v[16:23], v[198:205], v[222:225]
	v_mfma_f32_16x16x128_f8f6f4 v[52:55], v[140:147], v[36:43], v[226:229]
	v_mfma_f32_16x16x128_f8f6f4 v[56:59], v[148:155], v[36:43], v[56:59]
	v_mfma_f32_16x16x128_f8f6f4 v[36:39], v[140:147], v[156:163], v[232:235]
	v_mfma_f32_16x16x128_f8f6f4 v[40:43], v[148:155], v[156:163], v[236:239]
	v_mfma_f32_16x16x128_f8f6f4 v[20:23], v[140:147], v[164:171], v[240:243]
	v_mfma_f32_16x16x128_f8f6f4 v[244:247], v[148:155], v[164:171], v[244:247]
	v_mfma_f32_16x16x128_f8f6f4 v[4:7], v[140:147], v[198:205], v[248:251]
	v_mfma_f32_16x16x128_f8f6f4 v[8:11], v[148:155], v[198:205], v[64:67]
	s_setprio 0
	s_barrier
	s_add_i32 s12, s12, 2
	s_addk_i32 s13, 0x100
	s_cmp_gt_u32 s12, 13
	s_cbranch_scc0 .LBB0_1723
	s_mov_b64 s[4:5], 0
	s_and_b64 vcc, exec, s[38:39]
	s_cbranch_vccz .LBB0_1731
	v_readlane_b32 s4, v255, 9
	v_mov_b32_e32 v222, v176
	s_nop 0
	v_mov_b32_e32 v64, s4
	ds_read_b32 v64, v64
	s_add_i32 s4, s3, 2
	s_mul_i32 s3, s4, s72
	s_mul_hi_u32 s5, s4, s33
	s_add_i32 s5, s5, s3
	s_waitcnt lgkmcnt(0)
	v_readfirstlane_b32 s3, v64
	s_mul_i32 s4, s4, s33
	s_mul_i32 s31, s3, 44
	s_add_u32 s12, s4, s61
	s_addc_u32 s13, s5, s73
	s_ashr_i32 s38, s31, 31
	v_mov_b32_e32 v64, s31
	v_mov_b32_e32 v65, s38
	v_cmp_ge_i64_e32 vcc, s[12:13], v[64:65]
	s_mov_b64 s[4:5], 0
	s_cbranch_vccnz .LBB0_1732
	s_lshr_b32 s4, s38, 29
	s_add_i32 s4, s31, s4
	s_ashr_i32 s38, s4, 3
	s_and_b32 s4, s4, -8
	s_sub_i32 s39, s31, s4
	s_ashr_i32 s4, s12, 31
	s_lshr_b32 s4, s4, 29
	s_add_i32 s13, s12, s4
	s_and_b32 s4, s13, -8
	s_sub_i32 s12, s12, s4
	s_add_i32 s29, s38, 1
	s_cmp_ge_i32 s12, s39
	s_mov_b64 s[4:5], -1
	s_cbranch_scc0 .LBB0_1728
	s_sub_i32 s5, s12, s39
	s_mul_i32 s4, s29, s39
	s_mul_i32 s5, s5, s38
	s_add_i32 s31, s5, s4
	s_mov_b64 s[4:5], 0

.LBB0_1825:
	v_add_u32_e32 v128, 0x10000, v134
	ds_read_b128 v[136:139], v128
	ds_read_b128 v[140:143], v128 offset:1024
	ds_read_b128 v[144:147], v128 offset:2048
	ds_read_b128 v[148:151], v128 offset:3072
	v_add_u32_e32 v128, 0x14000, v134
	ds_read_b128 v[152:155], v128
	ds_read_b128 v[156:159], v128 offset:1024
	ds_read_b128 v[160:163], v128 offset:2048
	ds_read_b128 v[164:167], v128 offset:3072
	s_add_i32 s31, s13, 0xfff50080
	s_cmp_eq_u32 s12, 40
	s_cselect_b32 s45, s19, s41
	s_cselect_b32 s44, s18, s40
	s_cselect_b32 s47, s21, s43
	s_cselect_b32 s46, s20, s42
	s_cselect_b32 s31, 0, s31
	s_cselect_b32 s49, s23, s53
	s_cselect_b32 s48, s22, s52
	s_cselect_b32 s51, s29, s5
	s_cselect_b32 s50, s28, s4
	s_mov_b32 m0, s77
	ds_read_b128 v[168:171], v135
	ds_read_b128 v[172:175], v135 offset:1024
	ds_read_b128 v[198:201], v135 offset:2048
	ds_read_b128 v[202:205], v135 offset:3072
	ds_read_b128 v[206:209], v135 offset:4096
	ds_read_b128 v[210:213], v135 offset:5120
	ds_read_b128 v[214:217], v135 offset:6144
	ds_read_b128 v[218:221], v135 offset:7168
	buffer_load_dwordx4 v132, s[40:43], s13 offen lds
	s_mov_b32 m0, s79
	s_nop 0
	buffer_load_dwordx4 v133, s[40:43], s13 offen lds
	s_waitcnt vmcnt(8)
	s_waitcnt lgkmcnt(0)
	s_barrier
	s_setprio 1
	s_waitcnt lgkmcnt(6)
	v_mfma_f32_16x16x128_f8f6f4 v[124:127], v[136:143], v[168:175], v[124:127]
	v_mfma_f32_16x16x128_f8f6f4 v[120:123], v[144:151], v[168:175], v[120:123]
	s_waitcnt lgkmcnt(4)
	v_mfma_f32_16x16x128_f8f6f4 v[108:111], v[136:143], v[198:205], v[108:111]
	v_mfma_f32_16x16x128_f8f6f4 v[104:107], v[144:151], v[198:205], v[104:107]
	s_waitcnt lgkmcnt(2)
	v_mfma_f32_16x16x128_f8f6f4 v[178:181], v[136:143], v[206:213], v[92:95]
	v_mfma_f32_16x16x128_f8f6f4 v[182:185], v[144:151], v[206:213], v[88:91]
	s_waitcnt lgkmcnt(0)
	v_mfma_f32_16x16x128_f8f6f4 v[186:189], v[136:143], v[214:221], v[76:79]
	v_mfma_f32_16x16x128_f8f6f4 v[190:193], v[144:151], v[214:221], v[72:75]
	v_mfma_f32_16x16x128_f8f6f4 v[116:119], v[152:159], v[168:175], v[116:119]
	v_mfma_f32_16x16x128_f8f6f4 v[112:115], v[160:167], v[168:175], v[112:115]
	v_mfma_f32_16x16x128_f8f6f4 v[100:103], v[152:159], v[198:205], v[100:103]
	v_mfma_f32_16x16x128_f8f6f4 v[96:99], v[160:167], v[198:205], v[96:99]
	v_mfma_f32_16x16x128_f8f6f4 v[168:171], v[152:159], v[206:213], v[84:87]
	v_mfma_f32_16x16x128_f8f6f4 v[172:175], v[160:167], v[206:213], v[80:83]
	v_mfma_f32_16x16x128_f8f6f4 v[194:197], v[152:159], v[214:221], v[68:71]
	v_mfma_f32_16x16x128_f8f6f4 v[198:201], v[160:167], v[214:221], v[64:67]
	s_setprio 0
	s_barrier
	s_mov_b32 m0, s62
	s_nop 3
	ds_read_b128 v[64:67], v135 offset:16384
	ds_read_b128 v[68:71], v135 offset:17408
	ds_read_b128 v[72:75], v135 offset:18432
	ds_read_b128 v[76:79], v135 offset:19456
	ds_read_b128 v[80:83], v135 offset:20480
	ds_read_b128 v[84:87], v135 offset:21504
	ds_read_b128 v[88:91], v135 offset:22528
	ds_read_b128 v[92:95], v135 offset:23552
	buffer_load_dwordx4 v130, s[48:51], s31 offen lds
	s_mov_b32 m0, s63
	s_add_i32 s38, s31, 0xb0000
	buffer_load_dwordx4 v131, s[48:51], s31 offen lds
	s_mov_b32 m0, s64
	s_nop 0
	buffer_load_dwordx4 v130, s[48:51], s38 offen lds
	s_mov_b32 m0, s65
	s_nop 0
	buffer_load_dwordx4 v131, s[48:51], s38 offen lds
	s_mov_b32 m0, s61
	s_nop 0
	buffer_load_dwordx4 v132, s[44:47], s31 offen lds
	s_mov_b32 m0, s66
	s_nop 0
	buffer_load_dwordx4 v133, s[44:47], s31 offen lds
	s_waitcnt vmcnt(8)
	s_waitcnt lgkmcnt(0)
	s_barrier
	s_setprio 1
	s_waitcnt lgkmcnt(6)
	v_mfma_f32_16x16x128_f8f6f4 v[60:63], v[136:143], v[64:71], v[60:63]
	v_mfma_f32_16x16x128_f8f6f4 v[0:3], v[144:151], v[64:71], v[0:3]
	s_waitcnt lgkmcnt(4)
	v_mfma_f32_16x16x128_f8f6f4 v[202:205], v[136:143], v[72:79], v[48:51]
	v_mfma_f32_16x16x128_f8f6f4 v[206:209], v[144:151], v[72:79], v[44:47]
	s_waitcnt lgkmcnt(2)
	v_mfma_f32_16x16x128_f8f6f4 v[210:213], v[136:143], v[80:87], v[32:35]
	v_mfma_f32_16x16x128_f8f6f4 v[214:217], v[144:151], v[80:87], v[28:31]
	s_waitcnt lgkmcnt(0)
	v_mfma_f32_16x16x128_f8f6f4 v[218:221], v[136:143], v[88:95], v[16:19]
	v_mfma_f32_16x16x128_f8f6f4 v[222:225], v[144:151], v[88:95], v[12:15]
	v_mfma_f32_16x16x128_f8f6f4 v[56:59], v[152:159], v[64:71], v[56:59]
	v_mfma_f32_16x16x128_f8f6f4 v[52:55], v[160:167], v[64:71], v[52:55]
	v_mfma_f32_16x16x128_f8f6f4 v[226:229], v[152:159], v[72:79], v[40:43]
	v_mfma_f32_16x16x128_f8f6f4 v[232:235], v[160:167], v[72:79], v[36:39]
	v_mfma_f32_16x16x128_f8f6f4 v[236:239], v[152:159], v[80:87], v[24:27]
	v_mfma_f32_16x16x128_f8f6f4 v[240:243], v[160:167], v[80:87], v[20:23]
	v_mfma_f32_16x16x128_f8f6f4 v[244:247], v[152:159], v[88:95], v[8:11]
	v_mfma_f32_16x16x128_f8f6f4 v[248:251], v[160:167], v[88:95], v[4:7]
	s_setprio 0
	s_barrier
	v_add_u32_e32 v12, 0x18000, v134
	s_nop 3
	ds_read_b128 v[4:7], v12
	ds_read_b128 v[8:11], v12 offset:1024
	ds_read_b128 v[20:23], v12 offset:2048
	ds_read_b128 v[24:27], v12 offset:3072
	v_add_u32_e32 v12, 0x1c000, v134
	ds_read_b128 v[136:139], v12
	ds_read_b128 v[140:143], v12 offset:1024
	ds_read_b128 v[144:147], v12 offset:2048
	ds_read_b128 v[148:151], v12 offset:3072
	s_mov_b32 m0, s67
	ds_read_b128 v[12:15], v135 offset:32768
	ds_read_b128 v[16:19], v135 offset:33792
	ds_read_b128 v[28:31], v135 offset:34816
	ds_read_b128 v[32:35], v135 offset:35840
	ds_read_b128 v[36:39], v135 offset:36864
	ds_read_b128 v[40:43], v135 offset:37888
	ds_read_b128 v[44:47], v135 offset:38912
	ds_read_b128 v[48:51], v135 offset:39936
	buffer_load_dwordx4 v132, s[44:47], s38 offen lds
	s_mov_b32 m0, s68
	s_nop 0
	buffer_load_dwordx4 v133, s[44:47], s38 offen lds
	s_waitcnt vmcnt(8)
	s_waitcnt lgkmcnt(0)
	s_barrier
	s_setprio 1
	s_waitcnt lgkmcnt(6)
	v_mfma_f32_16x16x128_f8f6f4 v[124:127], v[4:11], v[12:19], v[124:127]
	v_mfma_f32_16x16x128_f8f6f4 v[120:123], v[20:27], v[12:19], v[120:123]
	s_waitcnt lgkmcnt(4)
	v_mfma_f32_16x16x128_f8f6f4 v[108:111], v[4:11], v[28:35], v[108:111]
	v_mfma_f32_16x16x128_f8f6f4 v[104:107], v[20:27], v[28:35], v[104:107]
	s_waitcnt lgkmcnt(2)
	v_mfma_f32_16x16x128_f8f6f4 v[92:95], v[4:11], v[36:43], v[178:181]
	v_mfma_f32_16x16x128_f8f6f4 v[88:91], v[20:27], v[36:43], v[182:185]
	s_waitcnt lgkmcnt(0)
	v_mfma_f32_16x16x128_f8f6f4 v[76:79], v[4:11], v[44:51], v[186:189]
	v_mfma_f32_16x16x128_f8f6f4 v[72:75], v[20:27], v[44:51], v[190:193]
	v_mfma_f32_16x16x128_f8f6f4 v[116:119], v[136:143], v[12:19], v[116:119]
	v_mfma_f32_16x16x128_f8f6f4 v[112:115], v[144:151], v[12:19], v[112:115]
	v_mfma_f32_16x16x128_f8f6f4 v[100:103], v[136:143], v[28:35], v[100:103]
	v_mfma_f32_16x16x128_f8f6f4 v[96:99], v[144:151], v[28:35], v[96:99]
	v_mfma_f32_16x16x128_f8f6f4 v[84:87], v[136:143], v[36:43], v[168:171]
	v_mfma_f32_16x16x128_f8f6f4 v[80:83], v[144:151], v[36:43], v[172:175]
	v_mfma_f32_16x16x128_f8f6f4 v[68:71], v[136:143], v[44:51], v[194:197]
	v_mfma_f32_16x16x128_f8f6f4 v[64:67], v[144:151], v[44:51], v[198:201]
	s_setprio 0
	s_barrier
	s_mov_b32 m0, s69
	s_or_b32 s38, s31, 0x80
	ds_read_b128 v[36:39], v135 offset:49152
	ds_read_b128 v[40:43], v135 offset:50176
	ds_read_b128 v[152:155], v135 offset:51200
	ds_read_b128 v[156:159], v135 offset:52224
	ds_read_b128 v[160:163], v135 offset:53248
	ds_read_b128 v[164:167], v135 offset:54272
	ds_read_b128 v[168:171], v135 offset:55296
	ds_read_b128 v[172:175], v135 offset:56320
	buffer_load_dwordx4 v130, s[48:51], s38 offen lds
	s_mov_b32 m0, s70
	s_add_i32 s31, s31, 0xb0080
	buffer_load_dwordx4 v131, s[48:51], s38 offen lds
	s_mov_b32 m0, s73
	s_nop 0
	buffer_load_dwordx4 v130, s[48:51], s31 offen lds
	s_mov_b32 m0, s74
	s_nop 0
	buffer_load_dwordx4 v131, s[48:51], s31 offen lds
	s_mov_b32 m0, s71
	s_nop 0
	buffer_load_dwordx4 v132, s[44:47], s38 offen lds
	s_mov_b32 m0, s72
	s_nop 0
	buffer_load_dwordx4 v133, s[44:47], s38 offen lds
	s_waitcnt vmcnt(8)
	s_waitcnt lgkmcnt(0)
	s_barrier
	s_setprio 1
	s_waitcnt lgkmcnt(6)
	v_mfma_f32_16x16x128_f8f6f4 v[60:63], v[4:11], v[36:43], v[60:63]
	v_mfma_f32_16x16x128_f8f6f4 v[0:3], v[20:27], v[36:43], v[0:3]
	s_waitcnt lgkmcnt(4)
	v_mfma_f32_16x16x128_f8f6f4 v[48:51], v[4:11], v[152:159], v[202:205]
	v_mfma_f32_16x16x128_f8f6f4 v[44:47], v[20:27], v[152:159], v[206:209]
	s_waitcnt lgkmcnt(2)
	v_mfma_f32_16x16x128_f8f6f4 v[32:35], v[4:11], v[160:167], v[210:213]
	v_mfma_f32_16x16x128_f8f6f4 v[28:31], v[20:27], v[160:167], v[214:217]
	s_waitcnt lgkmcnt(0)
	v_mfma_f32_16x16x128_f8f6f4 v[16:19], v[4:11], v[168:175], v[218:221]
	v_mfma_f32_16x16x128_f8f6f4 v[12:15], v[20:27], v[168:175], v[222:225]
	v_mfma_f32_16x16x128_f8f6f4 v[56:59], v[136:143], v[36:43], v[56:59]
	v_mfma_f32_16x16x128_f8f6f4 v[52:55], v[144:151], v[36:43], v[52:55]
	v_mfma_f32_16x16x128_f8f6f4 v[40:43], v[136:143], v[152:159], v[226:229]
	v_mfma_f32_16x16x128_f8f6f4 v[36:39], v[144:151], v[152:159], v[232:235]
	v_mfma_f32_16x16x128_f8f6f4 v[24:27], v[136:143], v[160:167], v[236:239]
	v_mfma_f32_16x16x128_f8f6f4 v[20:23], v[144:151], v[160:167], v[240:243]
	v_mfma_f32_16x16x128_f8f6f4 v[8:11], v[136:143], v[168:175], v[244:247]
	v_mfma_f32_16x16x128_f8f6f4 v[4:7], v[144:151], v[168:175], v[248:251]
	s_setprio 0
	s_barrier
	s_add_i32 s12, s12, 2
	s_addk_i32 s13, 0x100
	s_cmp_gt_u32 s12, 41
	s_cbranch_scc0 .LBB0_1825
	s_and_b64 vcc, exec, s[8:9]
	s_cbranch_vccz .LBB0_1828
	s_barrier

.LBB0_1950:
	v_add_u32_e32 v132, 0x10000, v138
	ds_read_b128 v[128:131], v132
	ds_read_b128 v[140:143], v132 offset:1024
	ds_read_b128 v[144:147], v132 offset:2048
	ds_read_b128 v[148:151], v132 offset:3072
	v_add_u32_e32 v132, 0x14000, v138
	ds_read_b128 v[152:155], v132
	ds_read_b128 v[156:159], v132 offset:1024
	ds_read_b128 v[160:163], v132 offset:2048
	ds_read_b128 v[164:167], v132 offset:3072
	s_add_i32 s48, s29, 0xfff80080
	s_cmp_eq_u32 s23, 28
	s_cselect_b32 s41, s31, s45
	s_cselect_b32 s40, s30, s44
	s_cselect_b32 s43, s35, s47
	s_cselect_b32 s42, s34, s46
	s_cselect_b32 s93, 0, s48
	s_cselect_b32 s49, s57, s53
	s_cselect_b32 s48, s56, s52
	s_cselect_b32 s51, s59, s13
	s_cselect_b32 s50, s58, s12
	s_mov_b32 m0, s88
	ds_read_b128 v[168:171], v139
	ds_read_b128 v[172:175], v139 offset:1024
	ds_read_b128 v[178:181], v139 offset:2048
	ds_read_b128 v[182:185], v139 offset:3072
	ds_read_b128 v[186:189], v139 offset:4096
	ds_read_b128 v[190:193], v139 offset:5120
	ds_read_b128 v[194:197], v139 offset:6144
	ds_read_b128 v[198:201], v139 offset:7168
	buffer_load_dwordx4 v136, s[44:47], s29 offen lds
	s_mov_b32 m0, s90
	s_nop 0
	buffer_load_dwordx4 v137, s[44:47], s29 offen lds
	s_waitcnt vmcnt(8)
	s_waitcnt lgkmcnt(0)
	s_barrier
	s_setprio 1
	s_waitcnt lgkmcnt(7)
	v_mfma_f32_16x16x32_bf16 v[124:127], v[128:131], v[168:171], v[124:127]
	v_mfma_f32_16x16x32_bf16 v[120:123], v[144:147], v[168:171], v[120:123]
	s_waitcnt lgkmcnt(5)
	v_mfma_f32_16x16x32_bf16 v[108:111], v[128:131], v[178:181], v[108:111]
	v_mfma_f32_16x16x32_bf16 v[104:107], v[144:147], v[178:181], v[104:107]
	s_waitcnt lgkmcnt(3)
	v_mfma_f32_16x16x32_bf16 v[92:95], v[128:131], v[186:189], v[92:95]
	v_mfma_f32_16x16x32_bf16 v[88:91], v[144:147], v[186:189], v[88:91]
	s_waitcnt lgkmcnt(1)
	v_mfma_f32_16x16x32_bf16 v[76:79], v[128:131], v[194:197], v[76:79]
	v_mfma_f32_16x16x32_bf16 v[72:75], v[144:147], v[194:197], v[72:75]
	v_mfma_f32_16x16x32_bf16 v[124:127], v[140:143], v[172:175], v[124:127]
	v_mfma_f32_16x16x32_bf16 v[120:123], v[148:151], v[172:175], v[120:123]
	v_mfma_f32_16x16x32_bf16 v[108:111], v[140:143], v[182:185], v[108:111]
	v_mfma_f32_16x16x32_bf16 v[104:107], v[148:151], v[182:185], v[104:107]
	v_mfma_f32_16x16x32_bf16 v[92:95], v[140:143], v[190:193], v[92:95]
	v_mfma_f32_16x16x32_bf16 v[88:91], v[148:151], v[190:193], v[88:91]
	s_waitcnt lgkmcnt(0)
	v_mfma_f32_16x16x32_bf16 v[76:79], v[140:143], v[198:201], v[76:79]
	v_mfma_f32_16x16x32_bf16 v[72:75], v[148:151], v[198:201], v[72:75]
	v_mfma_f32_16x16x32_bf16 v[116:119], v[152:155], v[168:171], v[116:119]
	v_mfma_f32_16x16x32_bf16 v[112:115], v[160:163], v[168:171], v[112:115]
	v_mfma_f32_16x16x32_bf16 v[100:103], v[152:155], v[178:181], v[100:103]
	v_mfma_f32_16x16x32_bf16 v[96:99], v[160:163], v[178:181], v[96:99]
	v_mfma_f32_16x16x32_bf16 v[84:87], v[152:155], v[186:189], v[84:87]
	v_mfma_f32_16x16x32_bf16 v[80:83], v[160:163], v[186:189], v[80:83]
	v_mfma_f32_16x16x32_bf16 v[68:71], v[152:155], v[194:197], v[68:71]
	v_mfma_f32_16x16x32_bf16 v[64:67], v[160:163], v[194:197], v[64:67]
	v_mfma_f32_16x16x32_bf16 v[116:119], v[156:159], v[172:175], v[116:119]
	v_mfma_f32_16x16x32_bf16 v[112:115], v[164:167], v[172:175], v[112:115]
	v_mfma_f32_16x16x32_bf16 v[100:103], v[156:159], v[182:185], v[100:103]
	v_mfma_f32_16x16x32_bf16 v[96:99], v[164:167], v[182:185], v[96:99]
	v_mfma_f32_16x16x32_bf16 v[84:87], v[156:159], v[190:193], v[84:87]
	v_mfma_f32_16x16x32_bf16 v[80:83], v[164:167], v[190:193], v[80:83]
	v_mfma_f32_16x16x32_bf16 v[68:71], v[156:159], v[198:201], v[68:71]
	v_mfma_f32_16x16x32_bf16 v[64:67], v[164:167], v[198:201], v[64:67]
	s_setprio 0
	s_barrier
	s_mov_b32 m0, s69
	ds_read_b128 v[168:171], v139 offset:16384
	ds_read_b128 v[172:175], v139 offset:17408
	ds_read_b128 v[178:181], v139 offset:18432
	ds_read_b128 v[182:185], v139 offset:19456
	ds_read_b128 v[186:189], v139 offset:20480
	ds_read_b128 v[190:193], v139 offset:21504
	ds_read_b128 v[194:197], v139 offset:22528
	ds_read_b128 v[198:201], v139 offset:23552
	buffer_load_dwordx4 v134, s[48:51], s93 offen lds
	s_mov_b32 m0, s70
	s_add_i32 s94, s93, 0x80000
	buffer_load_dwordx4 v135, s[48:51], s93 offen lds
	s_mov_b32 m0, s71
	s_nop 0
	buffer_load_dwordx4 v134, s[48:51], s94 offen lds
	s_mov_b32 m0, s72
	s_nop 0
	buffer_load_dwordx4 v135, s[48:51], s94 offen lds
	s_mov_b32 m0, s68
	s_nop 0
	buffer_load_dwordx4 v136, s[40:43], s93 offen lds
	s_mov_b32 m0, s73
	s_nop 0
	buffer_load_dwordx4 v137, s[40:43], s93 offen lds
	s_waitcnt vmcnt(8)
	s_waitcnt lgkmcnt(0)
	s_barrier
	s_setprio 1
	s_waitcnt lgkmcnt(7)
	v_mfma_f32_16x16x32_bf16 v[60:63], v[128:131], v[168:171], v[60:63]
	v_mfma_f32_16x16x32_bf16 v[0:3], v[144:147], v[168:171], v[0:3]
	s_waitcnt lgkmcnt(5)
	v_mfma_f32_16x16x32_bf16 v[44:47], v[128:131], v[178:181], v[44:47]
	v_mfma_f32_16x16x32_bf16 v[48:51], v[144:147], v[178:181], v[48:51]
	s_waitcnt lgkmcnt(3)
	v_mfma_f32_16x16x32_bf16 v[28:31], v[128:131], v[186:189], v[28:31]
	v_mfma_f32_16x16x32_bf16 v[32:35], v[144:147], v[186:189], v[32:35]
	s_waitcnt lgkmcnt(1)
	v_mfma_f32_16x16x32_bf16 v[12:15], v[128:131], v[194:197], v[12:15]
	v_mfma_f32_16x16x32_bf16 v[16:19], v[144:147], v[194:197], v[16:19]
	v_mfma_f32_16x16x32_bf16 v[60:63], v[140:143], v[172:175], v[60:63]
	v_mfma_f32_16x16x32_bf16 v[0:3], v[148:151], v[172:175], v[0:3]
	v_mfma_f32_16x16x32_bf16 v[44:47], v[140:143], v[182:185], v[44:47]
	v_mfma_f32_16x16x32_bf16 v[48:51], v[148:151], v[182:185], v[48:51]
	v_mfma_f32_16x16x32_bf16 v[28:31], v[140:143], v[190:193], v[28:31]
	v_mfma_f32_16x16x32_bf16 v[32:35], v[148:151], v[190:193], v[32:35]
	s_waitcnt lgkmcnt(0)
	v_mfma_f32_16x16x32_bf16 v[12:15], v[140:143], v[198:201], v[12:15]
	v_mfma_f32_16x16x32_bf16 v[16:19], v[148:151], v[198:201], v[16:19]
	v_mfma_f32_16x16x32_bf16 v[52:55], v[152:155], v[168:171], v[52:55]
	v_mfma_f32_16x16x32_bf16 v[56:59], v[160:163], v[168:171], v[56:59]
	v_mfma_f32_16x16x32_bf16 v[36:39], v[152:155], v[178:181], v[36:39]
	v_mfma_f32_16x16x32_bf16 v[40:43], v[160:163], v[178:181], v[40:43]
	v_mfma_f32_16x16x32_bf16 v[20:23], v[152:155], v[186:189], v[20:23]
	v_mfma_f32_16x16x32_bf16 v[24:27], v[160:163], v[186:189], v[24:27]
	v_mfma_f32_16x16x32_bf16 v[4:7], v[152:155], v[194:197], v[4:7]
	v_mfma_f32_16x16x32_bf16 v[8:11], v[160:163], v[194:197], v[8:11]
	v_mfma_f32_16x16x32_bf16 v[52:55], v[156:159], v[172:175], v[52:55]
	v_mfma_f32_16x16x32_bf16 v[56:59], v[164:167], v[172:175], v[56:59]
	v_mfma_f32_16x16x32_bf16 v[36:39], v[156:159], v[182:185], v[36:39]
	v_mfma_f32_16x16x32_bf16 v[40:43], v[164:167], v[182:185], v[40:43]
	v_mfma_f32_16x16x32_bf16 v[20:23], v[156:159], v[190:193], v[20:23]
	v_mfma_f32_16x16x32_bf16 v[24:27], v[164:167], v[190:193], v[24:27]
	v_mfma_f32_16x16x32_bf16 v[4:7], v[156:159], v[198:201], v[4:7]
	v_mfma_f32_16x16x32_bf16 v[8:11], v[164:167], v[198:201], v[8:11]
	s_setprio 0
	s_barrier
	v_add_u32_e32 v132, 0x18000, v138
	ds_read_b128 v[128:131], v132
	ds_read_b128 v[140:143], v132 offset:1024
	ds_read_b128 v[144:147], v132 offset:2048
	ds_read_b128 v[148:151], v132 offset:3072
	v_add_u32_e32 v132, 0x1c000, v138
	ds_read_b128 v[152:155], v132
	ds_read_b128 v[156:159], v132 offset:1024
	ds_read_b128 v[160:163], v132 offset:2048
	ds_read_b128 v[164:167], v132 offset:3072
	s_mov_b32 m0, s74
	ds_read_b128 v[168:171], v139 offset:32768
	ds_read_b128 v[172:175], v139 offset:33792
	ds_read_b128 v[178:181], v139 offset:34816
	ds_read_b128 v[182:185], v139 offset:35840
	ds_read_b128 v[186:189], v139 offset:36864
	ds_read_b128 v[190:193], v139 offset:37888
	ds_read_b128 v[194:197], v139 offset:38912
	ds_read_b128 v[198:201], v139 offset:39936
	buffer_load_dwordx4 v136, s[40:43], s94 offen lds
	s_mov_b32 m0, s75
	s_nop 0
	buffer_load_dwordx4 v137, s[40:43], s94 offen lds
	s_waitcnt vmcnt(8)
	s_waitcnt lgkmcnt(0)
	s_barrier
	s_setprio 1
	s_waitcnt lgkmcnt(7)
	v_mfma_f32_16x16x32_bf16 v[124:127], v[128:131], v[168:171], v[124:127]
	v_mfma_f32_16x16x32_bf16 v[120:123], v[144:147], v[168:171], v[120:123]
	s_waitcnt lgkmcnt(5)
	v_mfma_f32_16x16x32_bf16 v[108:111], v[128:131], v[178:181], v[108:111]
	v_mfma_f32_16x16x32_bf16 v[104:107], v[144:147], v[178:181], v[104:107]
	s_waitcnt lgkmcnt(3)
	v_mfma_f32_16x16x32_bf16 v[92:95], v[128:131], v[186:189], v[92:95]
	v_mfma_f32_16x16x32_bf16 v[88:91], v[144:147], v[186:189], v[88:91]
	s_waitcnt lgkmcnt(1)
	v_mfma_f32_16x16x32_bf16 v[76:79], v[128:131], v[194:197], v[76:79]
	v_mfma_f32_16x16x32_bf16 v[72:75], v[144:147], v[194:197], v[72:75]
	v_mfma_f32_16x16x32_bf16 v[124:127], v[140:143], v[172:175], v[124:127]
	v_mfma_f32_16x16x32_bf16 v[120:123], v[148:151], v[172:175], v[120:123]
	v_mfma_f32_16x16x32_bf16 v[108:111], v[140:143], v[182:185], v[108:111]
	v_mfma_f32_16x16x32_bf16 v[104:107], v[148:151], v[182:185], v[104:107]
	v_mfma_f32_16x16x32_bf16 v[92:95], v[140:143], v[190:193], v[92:95]
	v_mfma_f32_16x16x32_bf16 v[88:91], v[148:151], v[190:193], v[88:91]
	s_waitcnt lgkmcnt(0)
	v_mfma_f32_16x16x32_bf16 v[76:79], v[140:143], v[198:201], v[76:79]
	v_mfma_f32_16x16x32_bf16 v[72:75], v[148:151], v[198:201], v[72:75]
	v_mfma_f32_16x16x32_bf16 v[116:119], v[152:155], v[168:171], v[116:119]
	v_mfma_f32_16x16x32_bf16 v[112:115], v[160:163], v[168:171], v[112:115]
	v_mfma_f32_16x16x32_bf16 v[100:103], v[152:155], v[178:181], v[100:103]
	v_mfma_f32_16x16x32_bf16 v[96:99], v[160:163], v[178:181], v[96:99]
	v_mfma_f32_16x16x32_bf16 v[84:87], v[152:155], v[186:189], v[84:87]
	v_mfma_f32_16x16x32_bf16 v[80:83], v[160:163], v[186:189], v[80:83]
	v_mfma_f32_16x16x32_bf16 v[68:71], v[152:155], v[194:197], v[68:71]
	v_mfma_f32_16x16x32_bf16 v[64:67], v[160:163], v[194:197], v[64:67]
	v_mfma_f32_16x16x32_bf16 v[116:119], v[156:159], v[172:175], v[116:119]
	v_mfma_f32_16x16x32_bf16 v[112:115], v[164:167], v[172:175], v[112:115]
	v_mfma_f32_16x16x32_bf16 v[100:103], v[156:159], v[182:185], v[100:103]
	v_mfma_f32_16x16x32_bf16 v[96:99], v[164:167], v[182:185], v[96:99]
	v_mfma_f32_16x16x32_bf16 v[84:87], v[156:159], v[190:193], v[84:87]
	v_mfma_f32_16x16x32_bf16 v[80:83], v[164:167], v[190:193], v[80:83]
	v_mfma_f32_16x16x32_bf16 v[68:71], v[156:159], v[198:201], v[68:71]
	v_mfma_f32_16x16x32_bf16 v[64:67], v[164:167], v[198:201], v[64:67]
	s_setprio 0
	s_barrier
	s_mov_b32 m0, s76
	s_or_b32 s94, s93, 0x80
	ds_read_b128 v[168:171], v139 offset:49152
	ds_read_b128 v[172:175], v139 offset:50176
	ds_read_b128 v[178:181], v139 offset:51200
	ds_read_b128 v[182:185], v139 offset:52224
	ds_read_b128 v[186:189], v139 offset:53248
	ds_read_b128 v[190:193], v139 offset:54272
	ds_read_b128 v[194:197], v139 offset:55296
	ds_read_b128 v[198:201], v139 offset:56320
	buffer_load_dwordx4 v134, s[48:51], s94 offen lds
	s_mov_b32 m0, s77
	s_add_i32 s93, s93, 0x80080
	buffer_load_dwordx4 v135, s[48:51], s94 offen lds
	s_mov_b32 m0, s80
	s_nop 0
	buffer_load_dwordx4 v134, s[48:51], s93 offen lds
	s_mov_b32 m0, s82
	s_nop 0
	buffer_load_dwordx4 v135, s[48:51], s93 offen lds
	s_mov_b32 m0, s78
	s_nop 0
	buffer_load_dwordx4 v136, s[40:43], s94 offen lds
	s_mov_b32 m0, s79
	s_nop 0
	buffer_load_dwordx4 v137, s[40:43], s94 offen lds
	s_waitcnt vmcnt(8)
	s_waitcnt lgkmcnt(0)
	s_barrier
	s_setprio 1
	s_waitcnt lgkmcnt(7)
	v_mfma_f32_16x16x32_bf16 v[60:63], v[128:131], v[168:171], v[60:63]
	v_mfma_f32_16x16x32_bf16 v[0:3], v[144:147], v[168:171], v[0:3]
	s_waitcnt lgkmcnt(5)
	v_mfma_f32_16x16x32_bf16 v[44:47], v[128:131], v[178:181], v[44:47]
	v_mfma_f32_16x16x32_bf16 v[48:51], v[144:147], v[178:181], v[48:51]
	s_waitcnt lgkmcnt(3)
	v_mfma_f32_16x16x32_bf16 v[28:31], v[128:131], v[186:189], v[28:31]
	v_mfma_f32_16x16x32_bf16 v[32:35], v[144:147], v[186:189], v[32:35]
	s_waitcnt lgkmcnt(1)
	v_mfma_f32_16x16x32_bf16 v[12:15], v[128:131], v[194:197], v[12:15]
	v_mfma_f32_16x16x32_bf16 v[16:19], v[144:147], v[194:197], v[16:19]
	v_mfma_f32_16x16x32_bf16 v[60:63], v[140:143], v[172:175], v[60:63]
	v_mfma_f32_16x16x32_bf16 v[0:3], v[148:151], v[172:175], v[0:3]
	v_mfma_f32_16x16x32_bf16 v[44:47], v[140:143], v[182:185], v[44:47]
	v_mfma_f32_16x16x32_bf16 v[48:51], v[148:151], v[182:185], v[48:51]
	v_mfma_f32_16x16x32_bf16 v[28:31], v[140:143], v[190:193], v[28:31]
	v_mfma_f32_16x16x32_bf16 v[32:35], v[148:151], v[190:193], v[32:35]
	s_waitcnt lgkmcnt(0)
	v_mfma_f32_16x16x32_bf16 v[12:15], v[140:143], v[198:201], v[12:15]
	v_mfma_f32_16x16x32_bf16 v[16:19], v[148:151], v[198:201], v[16:19]
	v_mfma_f32_16x16x32_bf16 v[52:55], v[152:155], v[168:171], v[52:55]
	v_mfma_f32_16x16x32_bf16 v[56:59], v[160:163], v[168:171], v[56:59]
	v_mfma_f32_16x16x32_bf16 v[36:39], v[152:155], v[178:181], v[36:39]
	v_mfma_f32_16x16x32_bf16 v[40:43], v[160:163], v[178:181], v[40:43]
	v_mfma_f32_16x16x32_bf16 v[20:23], v[152:155], v[186:189], v[20:23]
	v_mfma_f32_16x16x32_bf16 v[24:27], v[160:163], v[186:189], v[24:27]
	v_mfma_f32_16x16x32_bf16 v[4:7], v[152:155], v[194:197], v[4:7]
	v_mfma_f32_16x16x32_bf16 v[8:11], v[160:163], v[194:197], v[8:11]
	v_mfma_f32_16x16x32_bf16 v[52:55], v[156:159], v[172:175], v[52:55]
	v_mfma_f32_16x16x32_bf16 v[56:59], v[164:167], v[172:175], v[56:59]
	v_mfma_f32_16x16x32_bf16 v[36:39], v[156:159], v[182:185], v[36:39]
	v_mfma_f32_16x16x32_bf16 v[40:43], v[164:167], v[182:185], v[40:43]
	v_mfma_f32_16x16x32_bf16 v[20:23], v[156:159], v[190:193], v[20:23]
	v_mfma_f32_16x16x32_bf16 v[24:27], v[164:167], v[190:193], v[24:27]
	v_mfma_f32_16x16x32_bf16 v[4:7], v[156:159], v[198:201], v[4:7]
	v_mfma_f32_16x16x32_bf16 v[8:11], v[164:167], v[198:201], v[8:11]
	s_setprio 0
	s_barrier
	s_add_i32 s23, s23, 2
	s_addk_i32 s29, 0x100
	s_cmp_gt_u32 s23, 29
	s_cbranch_scc0 .LBB0_1950
	s_and_b64 vcc, exec, s[20:21]
	s_cbranch_vccz .LBB0_1953
	s_barrier

.LBB0_2033:
	v_add_u32_e32 v124, 0x10000, v199
	v_add_u32_e32 v156, 0x14000, v199
	ds_read_b128 v[96:99], v124
	ds_read_b128 v[108:111], v124 offset:1024
	ds_read_b128 v[120:123], v124 offset:2048
	ds_read_b128 v[124:127], v124 offset:3072
	ds_read_b128 v[128:131], v156
	ds_read_b128 v[132:135], v156 offset:1024
	ds_read_b128 v[152:155], v156 offset:2048
	ds_read_b128 v[156:159], v156 offset:3072
	s_add_i32 s48, s13, 0xffe9c080
	s_cmpk_eq_i32 s12, 0x54
	s_cselect_b32 s41, s23, s45
	s_cselect_b32 s40, s22, s44
	s_cselect_b32 s43, s29, s47
	s_cselect_b32 s42, s28, s46
	s_cselect_b32 s57, 0, s48
	s_cselect_b32 s49, s31, s53
	s_cselect_b32 s48, s30, s52
	s_cselect_b32 s51, s35, s5
	s_cselect_b32 s50, s34, s4
	s_mov_b32 m0, s83
	ds_read_b128 v[160:163], v200
	ds_read_b128 v[164:167], v200 offset:1024
	ds_read_b128 v[168:171], v200 offset:2048
	ds_read_b128 v[178:181], v200 offset:3072
	ds_read_b128 v[182:185], v200 offset:4096
	ds_read_b128 v[186:189], v200 offset:5120
	ds_read_b128 v[190:193], v200 offset:6144
	ds_read_b128 v[194:197], v200 offset:7168
	buffer_load_dwordx4 v176, s[44:47], s13 offen lds
	s_mov_b32 m0, s89
	s_nop 0
	buffer_load_dwordx4 v198, s[44:47], s13 offen lds
	s_waitcnt vmcnt(8)
	s_waitcnt lgkmcnt(0)
	s_barrier
	s_setprio 1
	s_waitcnt lgkmcnt(7)
	v_mfma_f32_16x16x32_bf16 v[148:151], v[96:99], v[160:163], v[148:151]
	v_mfma_f32_16x16x32_bf16 v[144:147], v[120:123], v[160:163], v[144:147]
	s_waitcnt lgkmcnt(5)
	v_mfma_f32_16x16x32_bf16 v[116:119], v[96:99], v[168:171], v[116:119]
	v_mfma_f32_16x16x32_bf16 v[112:115], v[120:123], v[168:171], v[112:115]
	s_waitcnt lgkmcnt(3)
	v_mfma_f32_16x16x32_bf16 v[92:95], v[96:99], v[182:185], v[92:95]
	v_mfma_f32_16x16x32_bf16 v[88:91], v[120:123], v[182:185], v[88:91]
	s_waitcnt lgkmcnt(1)
	v_mfma_f32_16x16x32_bf16 v[76:79], v[96:99], v[190:193], v[76:79]
	v_mfma_f32_16x16x32_bf16 v[72:75], v[120:123], v[190:193], v[72:75]
	v_mfma_f32_16x16x32_bf16 v[148:151], v[108:111], v[164:167], v[148:151]
	v_mfma_f32_16x16x32_bf16 v[144:147], v[124:127], v[164:167], v[144:147]
	v_mfma_f32_16x16x32_bf16 v[116:119], v[108:111], v[178:181], v[116:119]
	v_mfma_f32_16x16x32_bf16 v[112:115], v[124:127], v[178:181], v[112:115]
	v_mfma_f32_16x16x32_bf16 v[92:95], v[108:111], v[186:189], v[92:95]
	v_mfma_f32_16x16x32_bf16 v[88:91], v[124:127], v[186:189], v[88:91]
	s_waitcnt lgkmcnt(0)
	v_mfma_f32_16x16x32_bf16 v[76:79], v[108:111], v[194:197], v[76:79]
	v_mfma_f32_16x16x32_bf16 v[72:75], v[124:127], v[194:197], v[72:75]
	v_mfma_f32_16x16x32_bf16 v[140:143], v[128:131], v[160:163], v[140:143]
	v_mfma_f32_16x16x32_bf16 v[136:139], v[152:155], v[160:163], v[136:139]
	v_mfma_f32_16x16x32_bf16 v[104:107], v[128:131], v[168:171], v[104:107]
	v_mfma_f32_16x16x32_bf16 v[100:103], v[152:155], v[168:171], v[100:103]
	v_mfma_f32_16x16x32_bf16 v[84:87], v[128:131], v[182:185], v[84:87]
	v_mfma_f32_16x16x32_bf16 v[80:83], v[152:155], v[182:185], v[80:83]
	v_mfma_f32_16x16x32_bf16 v[68:71], v[128:131], v[190:193], v[68:71]
	v_mfma_f32_16x16x32_bf16 v[64:67], v[152:155], v[190:193], v[64:67]
	v_mfma_f32_16x16x32_bf16 v[140:143], v[132:135], v[164:167], v[140:143]
	v_mfma_f32_16x16x32_bf16 v[136:139], v[156:159], v[164:167], v[136:139]
	v_mfma_f32_16x16x32_bf16 v[104:107], v[132:135], v[178:181], v[104:107]
	v_mfma_f32_16x16x32_bf16 v[100:103], v[156:159], v[178:181], v[100:103]
	v_mfma_f32_16x16x32_bf16 v[84:87], v[132:135], v[186:189], v[84:87]
	v_mfma_f32_16x16x32_bf16 v[80:83], v[156:159], v[186:189], v[80:83]
	v_mfma_f32_16x16x32_bf16 v[68:71], v[132:135], v[194:197], v[68:71]
	v_mfma_f32_16x16x32_bf16 v[64:67], v[156:159], v[194:197], v[64:67]
	s_setprio 0
	s_barrier
	s_mov_b32 m0, s65
	ds_read_b128 v[160:163], v200 offset:16384
	ds_read_b128 v[164:167], v200 offset:17408
	ds_read_b128 v[168:171], v200 offset:18432
	ds_read_b128 v[178:181], v200 offset:19456
	ds_read_b128 v[182:185], v200 offset:20480
	ds_read_b128 v[186:189], v200 offset:21504
	ds_read_b128 v[190:193], v200 offset:22528
	ds_read_b128 v[194:197], v200 offset:23552
	buffer_load_dwordx4 v174, s[48:51], s57 offen lds
	s_mov_b32 m0, s66
	s_add_i32 s95, s57, 0x164000
	buffer_load_dwordx4 v175, s[48:51], s57 offen lds
	s_mov_b32 m0, s67
	s_nop 0
	buffer_load_dwordx4 v174, s[48:51], s95 offen lds
	s_mov_b32 m0, s68
	s_nop 0
	buffer_load_dwordx4 v175, s[48:51], s95 offen lds
	s_mov_b32 m0, s64
	s_nop 0
	buffer_load_dwordx4 v176, s[40:43], s57 offen lds
	s_mov_b32 m0, s69
	s_nop 0
	buffer_load_dwordx4 v198, s[40:43], s57 offen lds
	s_waitcnt vmcnt(8)
	s_waitcnt lgkmcnt(0)
	s_barrier
	s_setprio 1
	s_waitcnt lgkmcnt(7)
	v_mfma_f32_16x16x32_bf16 v[60:63], v[96:99], v[160:163], v[60:63]
	v_mfma_f32_16x16x32_bf16 v[48:51], v[120:123], v[160:163], v[48:51]
	s_waitcnt lgkmcnt(5)
	v_mfma_f32_16x16x32_bf16 v[44:47], v[96:99], v[168:171], v[44:47]
	v_mfma_f32_16x16x32_bf16 v[40:43], v[120:123], v[168:171], v[40:43]
	s_waitcnt lgkmcnt(3)
	v_mfma_f32_16x16x32_bf16 v[28:31], v[96:99], v[182:185], v[28:31]
	v_mfma_f32_16x16x32_bf16 v[24:27], v[120:123], v[182:185], v[24:27]
	s_waitcnt lgkmcnt(1)
	v_mfma_f32_16x16x32_bf16 v[12:15], v[96:99], v[190:193], v[12:15]
	v_mfma_f32_16x16x32_bf16 v[8:11], v[120:123], v[190:193], v[8:11]
	v_mfma_f32_16x16x32_bf16 v[60:63], v[108:111], v[164:167], v[60:63]
	v_mfma_f32_16x16x32_bf16 v[48:51], v[124:127], v[164:167], v[48:51]
	v_mfma_f32_16x16x32_bf16 v[44:47], v[108:111], v[178:181], v[44:47]
	v_mfma_f32_16x16x32_bf16 v[40:43], v[124:127], v[178:181], v[40:43]
	v_mfma_f32_16x16x32_bf16 v[28:31], v[108:111], v[186:189], v[28:31]
	v_mfma_f32_16x16x32_bf16 v[24:27], v[124:127], v[186:189], v[24:27]
	s_waitcnt lgkmcnt(0)
	v_mfma_f32_16x16x32_bf16 v[12:15], v[108:111], v[194:197], v[12:15]
	v_mfma_f32_16x16x32_bf16 v[8:11], v[124:127], v[194:197], v[8:11]
	v_mfma_f32_16x16x32_bf16 v[56:59], v[128:131], v[160:163], v[56:59]
	v_mfma_f32_16x16x32_bf16 v[52:55], v[152:155], v[160:163], v[52:55]
	v_mfma_f32_16x16x32_bf16 v[36:39], v[128:131], v[168:171], v[36:39]
	v_mfma_f32_16x16x32_bf16 v[32:35], v[152:155], v[168:171], v[32:35]
	v_mfma_f32_16x16x32_bf16 v[20:23], v[128:131], v[182:185], v[20:23]
	v_mfma_f32_16x16x32_bf16 v[16:19], v[152:155], v[182:185], v[16:19]
	v_mfma_f32_16x16x32_bf16 v[4:7], v[128:131], v[190:193], v[4:7]
	v_mfma_f32_16x16x32_bf16 v[0:3], v[152:155], v[190:193], v[0:3]
	v_mfma_f32_16x16x32_bf16 v[56:59], v[132:135], v[164:167], v[56:59]
	v_mfma_f32_16x16x32_bf16 v[52:55], v[156:159], v[164:167], v[52:55]
	v_mfma_f32_16x16x32_bf16 v[36:39], v[132:135], v[178:181], v[36:39]
	v_mfma_f32_16x16x32_bf16 v[32:35], v[156:159], v[178:181], v[32:35]
	v_mfma_f32_16x16x32_bf16 v[20:23], v[132:135], v[186:189], v[20:23]
	v_mfma_f32_16x16x32_bf16 v[16:19], v[156:159], v[186:189], v[16:19]
	v_mfma_f32_16x16x32_bf16 v[4:7], v[132:135], v[194:197], v[4:7]
	v_mfma_f32_16x16x32_bf16 v[0:3], v[156:159], v[194:197], v[0:3]
	s_setprio 0
	s_barrier
	v_add_u32_e32 v124, 0x18000, v199
	v_add_u32_e32 v156, 0x1c000, v199
	ds_read_b128 v[96:99], v124
	ds_read_b128 v[108:111], v124 offset:1024
	ds_read_b128 v[120:123], v124 offset:2048
	ds_read_b128 v[124:127], v124 offset:3072
	ds_read_b128 v[128:131], v156
	ds_read_b128 v[132:135], v156 offset:1024
	ds_read_b128 v[152:155], v156 offset:2048
	ds_read_b128 v[156:159], v156 offset:3072
	s_mov_b32 m0, s70
	ds_read_b128 v[160:163], v200 offset:32768
	ds_read_b128 v[164:167], v200 offset:33792
	ds_read_b128 v[168:171], v200 offset:34816
	ds_read_b128 v[178:181], v200 offset:35840
	ds_read_b128 v[182:185], v200 offset:36864
	ds_read_b128 v[186:189], v200 offset:37888
	ds_read_b128 v[190:193], v200 offset:38912
	ds_read_b128 v[194:197], v200 offset:39936
	buffer_load_dwordx4 v176, s[40:43], s95 offen lds
	s_mov_b32 m0, s71
	s_nop 0
	buffer_load_dwordx4 v198, s[40:43], s95 offen lds
	s_waitcnt vmcnt(8)
	s_waitcnt lgkmcnt(0)
	s_barrier
	s_setprio 1
	s_waitcnt lgkmcnt(7)
	v_mfma_f32_16x16x32_bf16 v[148:151], v[96:99], v[160:163], v[148:151]
	v_mfma_f32_16x16x32_bf16 v[144:147], v[120:123], v[160:163], v[144:147]
	s_waitcnt lgkmcnt(5)
	v_mfma_f32_16x16x32_bf16 v[116:119], v[96:99], v[168:171], v[116:119]
	v_mfma_f32_16x16x32_bf16 v[112:115], v[120:123], v[168:171], v[112:115]
	s_waitcnt lgkmcnt(3)
	v_mfma_f32_16x16x32_bf16 v[92:95], v[96:99], v[182:185], v[92:95]
	v_mfma_f32_16x16x32_bf16 v[88:91], v[120:123], v[182:185], v[88:91]
	s_waitcnt lgkmcnt(1)
	v_mfma_f32_16x16x32_bf16 v[76:79], v[96:99], v[190:193], v[76:79]
	v_mfma_f32_16x16x32_bf16 v[72:75], v[120:123], v[190:193], v[72:75]
	v_mfma_f32_16x16x32_bf16 v[148:151], v[108:111], v[164:167], v[148:151]
	v_mfma_f32_16x16x32_bf16 v[144:147], v[124:127], v[164:167], v[144:147]
	v_mfma_f32_16x16x32_bf16 v[116:119], v[108:111], v[178:181], v[116:119]
	v_mfma_f32_16x16x32_bf16 v[112:115], v[124:127], v[178:181], v[112:115]
	v_mfma_f32_16x16x32_bf16 v[92:95], v[108:111], v[186:189], v[92:95]
	v_mfma_f32_16x16x32_bf16 v[88:91], v[124:127], v[186:189], v[88:91]
	s_waitcnt lgkmcnt(0)
	v_mfma_f32_16x16x32_bf16 v[76:79], v[108:111], v[194:197], v[76:79]
	v_mfma_f32_16x16x32_bf16 v[72:75], v[124:127], v[194:197], v[72:75]
	v_mfma_f32_16x16x32_bf16 v[140:143], v[128:131], v[160:163], v[140:143]
	v_mfma_f32_16x16x32_bf16 v[136:139], v[152:155], v[160:163], v[136:139]
	v_mfma_f32_16x16x32_bf16 v[104:107], v[128:131], v[168:171], v[104:107]
	v_mfma_f32_16x16x32_bf16 v[100:103], v[152:155], v[168:171], v[100:103]
	v_mfma_f32_16x16x32_bf16 v[84:87], v[128:131], v[182:185], v[84:87]
	v_mfma_f32_16x16x32_bf16 v[80:83], v[152:155], v[182:185], v[80:83]
	v_mfma_f32_16x16x32_bf16 v[68:71], v[128:131], v[190:193], v[68:71]
	v_mfma_f32_16x16x32_bf16 v[64:67], v[152:155], v[190:193], v[64:67]
	v_mfma_f32_16x16x32_bf16 v[140:143], v[132:135], v[164:167], v[140:143]
	v_mfma_f32_16x16x32_bf16 v[136:139], v[156:159], v[164:167], v[136:139]
	v_mfma_f32_16x16x32_bf16 v[104:107], v[132:135], v[178:181], v[104:107]
	v_mfma_f32_16x16x32_bf16 v[100:103], v[156:159], v[178:181], v[100:103]
	v_mfma_f32_16x16x32_bf16 v[84:87], v[132:135], v[186:189], v[84:87]
	v_mfma_f32_16x16x32_bf16 v[80:83], v[156:159], v[186:189], v[80:83]
	v_mfma_f32_16x16x32_bf16 v[68:71], v[132:135], v[194:197], v[68:71]
	v_mfma_f32_16x16x32_bf16 v[64:67], v[156:159], v[194:197], v[64:67]
	s_setprio 0
	s_barrier
	s_mov_b32 m0, s72
	s_or_b32 s95, s57, 0x80
	ds_read_b128 v[160:163], v200 offset:49152
	ds_read_b128 v[164:167], v200 offset:50176
	ds_read_b128 v[168:171], v200 offset:51200
	ds_read_b128 v[178:181], v200 offset:52224
	ds_read_b128 v[182:185], v200 offset:53248
	ds_read_b128 v[186:189], v200 offset:54272
	ds_read_b128 v[190:193], v200 offset:55296
	ds_read_b128 v[194:197], v200 offset:56320
	buffer_load_dwordx4 v174, s[48:51], s95 offen lds
	s_mov_b32 m0, s73
	s_add_i32 s57, s57, 0x164080
	buffer_load_dwordx4 v175, s[48:51], s95 offen lds
	s_mov_b32 m0, s76
	s_nop 0
	buffer_load_dwordx4 v174, s[48:51], s57 offen lds
	s_mov_b32 m0, s77
	s_nop 0
	buffer_load_dwordx4 v175, s[48:51], s57 offen lds
	s_mov_b32 m0, s74
	s_nop 0
	buffer_load_dwordx4 v176, s[40:43], s95 offen lds
	s_mov_b32 m0, s75
	s_nop 0
	buffer_load_dwordx4 v198, s[40:43], s95 offen lds
	s_waitcnt vmcnt(8)
	s_waitcnt lgkmcnt(0)
	s_barrier
	s_setprio 1
	s_waitcnt lgkmcnt(7)
	v_mfma_f32_16x16x32_bf16 v[60:63], v[96:99], v[160:163], v[60:63]
	v_mfma_f32_16x16x32_bf16 v[48:51], v[120:123], v[160:163], v[48:51]
	s_waitcnt lgkmcnt(5)
	v_mfma_f32_16x16x32_bf16 v[44:47], v[96:99], v[168:171], v[44:47]
	v_mfma_f32_16x16x32_bf16 v[40:43], v[120:123], v[168:171], v[40:43]
	s_waitcnt lgkmcnt(3)
	v_mfma_f32_16x16x32_bf16 v[28:31], v[96:99], v[182:185], v[28:31]
	v_mfma_f32_16x16x32_bf16 v[24:27], v[120:123], v[182:185], v[24:27]
	s_waitcnt lgkmcnt(1)
	v_mfma_f32_16x16x32_bf16 v[12:15], v[96:99], v[190:193], v[12:15]
	v_mfma_f32_16x16x32_bf16 v[8:11], v[120:123], v[190:193], v[8:11]
	v_mfma_f32_16x16x32_bf16 v[60:63], v[108:111], v[164:167], v[60:63]
	v_mfma_f32_16x16x32_bf16 v[48:51], v[124:127], v[164:167], v[48:51]
	v_mfma_f32_16x16x32_bf16 v[44:47], v[108:111], v[178:181], v[44:47]
	v_mfma_f32_16x16x32_bf16 v[40:43], v[124:127], v[178:181], v[40:43]
	v_mfma_f32_16x16x32_bf16 v[28:31], v[108:111], v[186:189], v[28:31]
	v_mfma_f32_16x16x32_bf16 v[24:27], v[124:127], v[186:189], v[24:27]
	s_waitcnt lgkmcnt(0)
	v_mfma_f32_16x16x32_bf16 v[12:15], v[108:111], v[194:197], v[12:15]
	v_mfma_f32_16x16x32_bf16 v[8:11], v[124:127], v[194:197], v[8:11]
	v_mfma_f32_16x16x32_bf16 v[56:59], v[128:131], v[160:163], v[56:59]
	v_mfma_f32_16x16x32_bf16 v[52:55], v[152:155], v[160:163], v[52:55]
	v_mfma_f32_16x16x32_bf16 v[36:39], v[128:131], v[168:171], v[36:39]
	v_mfma_f32_16x16x32_bf16 v[32:35], v[152:155], v[168:171], v[32:35]
	v_mfma_f32_16x16x32_bf16 v[20:23], v[128:131], v[182:185], v[20:23]
	v_mfma_f32_16x16x32_bf16 v[16:19], v[152:155], v[182:185], v[16:19]
	v_mfma_f32_16x16x32_bf16 v[4:7], v[128:131], v[190:193], v[4:7]
	v_mfma_f32_16x16x32_bf16 v[0:3], v[152:155], v[190:193], v[0:3]
	v_mfma_f32_16x16x32_bf16 v[56:59], v[132:135], v[164:167], v[56:59]
	v_mfma_f32_16x16x32_bf16 v[52:55], v[156:159], v[164:167], v[52:55]
	v_mfma_f32_16x16x32_bf16 v[36:39], v[132:135], v[178:181], v[36:39]
	v_mfma_f32_16x16x32_bf16 v[32:35], v[156:159], v[178:181], v[32:35]
	v_mfma_f32_16x16x32_bf16 v[20:23], v[132:135], v[186:189], v[20:23]
	v_mfma_f32_16x16x32_bf16 v[16:19], v[156:159], v[186:189], v[16:19]
	v_mfma_f32_16x16x32_bf16 v[4:7], v[132:135], v[194:197], v[4:7]
	v_mfma_f32_16x16x32_bf16 v[0:3], v[156:159], v[194:197], v[0:3]
	s_setprio 0
	s_barrier
	s_add_i32 s12, s12, 2
	s_addk_i32 s13, 0x100
	s_cmpk_gt_u32 s12, 0x55
	s_cbranch_scc0 .LBB0_2033
	s_and_b64 vcc, exec, s[20:21]
	s_cbranch_vccz .LBB0_2036
	s_barrier
